# v6 + GEMM epilogue stores re-assigned to lanes with ds_bpermute (data+address) so that each lane quad writes one contiguous 64-byte segment; memory image unchanged
# speedup vs baseline: 1.0071x; 1.0042x over previous
.LBB0_174:
	v_mbcnt_lo_u32_b32 v244, -1, 0
	v_mbcnt_hi_u32_b32 v244, -1, v244
	v_lshrrev_b32_e32 v245, 2, v244
	v_and_b32_e32 v244, 3, v244
	v_lshl_add_u32 v244, v244, 4, v245
	v_lshlrev_b32_e32 v244, 2, v244
	s_ashr_i32 s15, s60, 3
	s_add_i32 s62, s15, s75
	s_lshl_b32 s15, s60, 8
	s_and_b32 s15, s15, 0x700
	s_cmp_eq_u32 s62, 0
	v_lshl_add_u32 v174, s28, 8, v1
	s_cselect_b64 s[26:27], -1, 0
	v_or_b32_e32 v82, s15, v209
	s_and_b64 s[26:27], s[50:51], s[26:27]
	v_or_b32_e32 v180, 16, v174
	v_or_b32_e32 v178, 32, v174
	v_or_b32_e32 v176, 48, v174
	s_mov_b64 s[64:65], -1
	s_and_b64 vcc, exec, s[26:27]
	v_lshlrev_b32_e32 v114, 1, v82
	v_ashrrev_i32_e32 v175, 31, v174
	v_ashrrev_i32_e32 v181, 31, v180
	v_ashrrev_i32_e32 v179, 31, v178
	v_ashrrev_i32_e32 v177, 31, v176
	s_cbranch_vccnz .LBB0_177
	v_lshl_add_u32 v158, s14, 10, v210
	ds_read2_b32 v[88:89], v158 offset1:16
	s_ashr_i32 s63, s62, 31
	s_lshl_b64 s[26:27], s[62:63], 25
	s_add_u32 s26, s84, s26
	s_addc_u32 s27, s85, s27
	v_lshl_add_u64 v[90:91], s[26:27], 0, v[114:115]
	v_lshlrev_b64 v[82:83], 12, v[174:175]
	s_waitcnt lgkmcnt(0)
	v_pk_mul_f32 v[84:85], v[144:145], v[88:89] op_sel_hi:[1,0]
	v_lshl_add_u64 v[82:83], v[90:91], 0, v[82:83]
	v_pk_mul_f32 v[86:87], v[146:147], v[88:89] op_sel_hi:[1,0]
	v_cvt_pk_bf16_f32 v84, v84, v85
	v_pk_mul_f32 v[92:93], v[142:143], v[88:89] op_sel_hi:[1,0]
	v_cvt_pk_bf16_f32 v85, v86, v87
	v_pk_mul_f32 v[94:95], v[140:141], v[88:89] op_sel_hi:[1,0]
	v_cvt_pk_bf16_f32 v87, v92, v93
	v_pk_mul_f32 v[92:93], v[134:135], v[88:89] op_sel_hi:[1,0]
	v_cvt_pk_bf16_f32 v86, v94, v95
	ds_bpermute_b32 v232, v244, v84
	ds_bpermute_b32 v233, v244, v85
	ds_bpermute_b32 v234, v244, v86
	ds_bpermute_b32 v235, v244, v87
	ds_bpermute_b32 v236, v244, v82
	ds_bpermute_b32 v237, v244, v83
	s_waitcnt lgkmcnt(0)
	global_store_dwordx4 v[236:237], v[232:235], off
	v_pk_mul_f32 v[94:95], v[132:133], v[88:89] op_sel_hi:[1,0]
	s_mov_b32 s15, 0x80000
	v_pk_mul_f32 v[84:85], v[136:137], v[88:89] op_sel_hi:[1,0]
	v_pk_mul_f32 v[86:87], v[138:139], v[88:89] op_sel_hi:[1,0]
	v_cvt_pk_bf16_f32 v84, v84, v85
	v_mov_b32_e32 v88, v89
	v_cvt_pk_bf16_f32 v85, v86, v87
	v_cvt_pk_bf16_f32 v86, v94, v95
	v_cvt_pk_bf16_f32 v87, v92, v93
	ds_bpermute_b32 v238, v244, v84
	ds_bpermute_b32 v239, v244, v85
	ds_bpermute_b32 v240, v244, v86
	ds_bpermute_b32 v241, v244, v87
	ds_bpermute_b32 v242, v244, v82
	ds_bpermute_b32 v243, v244, v83
	s_waitcnt lgkmcnt(0)
	global_store_dwordx4 v[242:243], v[238:241], off offset:64
	v_pk_mul_f32 v[94:95], v[126:127], v[88:89] op_sel_hi:[1,0]
	v_pk_mul_f32 v[96:97], v[124:125], v[88:89] op_sel_hi:[1,0]
	v_lshlrev_b64 v[84:85], 12, v[180:181]
	v_lshl_add_u64 v[92:93], v[90:91], 0, v[84:85]
	v_pk_mul_f32 v[86:87], v[130:131], v[88:89] op_sel_hi:[1,0]
	v_pk_mul_f32 v[84:85], v[128:129], v[88:89] op_sel_hi:[1,0]
	s_mov_b64 s[16:17], 0x80000
	v_cvt_pk_bf16_f32 v84, v84, v85
	v_cvt_pk_bf16_f32 v85, v86, v87
	v_cvt_pk_bf16_f32 v86, v96, v97
	v_cvt_pk_bf16_f32 v87, v94, v95
	ds_bpermute_b32 v232, v244, v84
	ds_bpermute_b32 v233, v244, v85
	ds_bpermute_b32 v234, v244, v86
	ds_bpermute_b32 v235, v244, v87
	ds_bpermute_b32 v236, v244, v92
	ds_bpermute_b32 v237, v244, v93
	s_waitcnt lgkmcnt(0)
	global_store_dwordx4 v[236:237], v[232:235], off
	v_pk_mul_f32 v[94:95], v[118:119], v[88:89] op_sel_hi:[1,0]
	s_nop 0
	v_pk_mul_f32 v[86:87], v[122:123], v[88:89] op_sel_hi:[1,0]
	v_pk_mul_f32 v[84:85], v[120:121], v[88:89] op_sel_hi:[1,0]
	v_pk_mul_f32 v[88:89], v[116:117], v[88:89] op_sel_hi:[1,0]
	v_cvt_pk_bf16_f32 v84, v84, v85
	v_cvt_pk_bf16_f32 v85, v86, v87
	v_cvt_pk_bf16_f32 v87, v94, v95
	s_nop 0
	v_cvt_pk_bf16_f32 v86, v88, v89
	ds_read2_b32 v[88:89], v158 offset0:32 offset1:48
	ds_bpermute_b32 v238, v244, v84
	ds_bpermute_b32 v239, v244, v85
	ds_bpermute_b32 v240, v244, v86
	ds_bpermute_b32 v241, v244, v87
	ds_bpermute_b32 v242, v244, v92
	ds_bpermute_b32 v243, v244, v93
	s_waitcnt lgkmcnt(0)
	global_store_dwordx4 v[242:243], v[238:241], off offset:64
	s_waitcnt lgkmcnt(0)
	v_pk_mul_f32 v[94:95], v[108:109], v[88:89] op_sel_hi:[1,0]
	v_lshlrev_b64 v[84:85], 12, v[178:179]
	v_lshl_add_u64 v[92:93], v[90:91], 0, v[84:85]
	v_pk_mul_f32 v[84:85], v[110:111], v[88:89] op_sel_hi:[1,0]
	v_pk_mul_f32 v[86:87], v[112:113], v[88:89] op_sel_hi:[1,0]
	v_cvt_pk_bf16_f32 v84, v84, v85
	v_pk_mul_f32 v[96:97], v[106:107], v[88:89] op_sel_hi:[1,0]
	v_cvt_pk_bf16_f32 v85, v86, v87
	v_cvt_pk_bf16_f32 v87, v94, v95
	v_pk_mul_f32 v[94:95], v[100:101], v[88:89] op_sel_hi:[1,0]
	v_cvt_pk_bf16_f32 v86, v96, v97
	ds_bpermute_b32 v232, v244, v84
	ds_bpermute_b32 v233, v244, v85
	ds_bpermute_b32 v234, v244, v86
	ds_bpermute_b32 v235, v244, v87
	ds_bpermute_b32 v236, v244, v92
	ds_bpermute_b32 v237, v244, v93
	s_waitcnt lgkmcnt(0)
	global_store_dwordx4 v[236:237], v[232:235], off
	v_pk_mul_f32 v[96:97], v[98:99], v[88:89] op_sel_hi:[1,0]
	s_nop 0
	v_pk_mul_f32 v[84:85], v[102:103], v[88:89] op_sel_hi:[1,0]
	v_pk_mul_f32 v[86:87], v[104:105], v[88:89] op_sel_hi:[1,0]
	v_cvt_pk_bf16_f32 v84, v84, v85
	v_mov_b32_e32 v88, v89
	v_cvt_pk_bf16_f32 v85, v86, v87
	v_cvt_pk_bf16_f32 v86, v96, v97
	v_cvt_pk_bf16_f32 v87, v94, v95
	ds_bpermute_b32 v238, v244, v84
	ds_bpermute_b32 v239, v244, v85
	ds_bpermute_b32 v240, v244, v86
	ds_bpermute_b32 v241, v244, v87
	ds_bpermute_b32 v242, v244, v92
	ds_bpermute_b32 v243, v244, v93
	s_waitcnt lgkmcnt(0)
	global_store_dwordx4 v[242:243], v[238:241], off offset:64
	v_pk_mul_f32 v[94:95], v[74:75], v[88:89] op_sel_hi:[1,0]
	v_pk_mul_f32 v[92:93], v[76:77], v[88:89] op_sel_hi:[1,0]
	v_lshlrev_b64 v[84:85], 12, v[176:177]
	v_lshl_add_u64 v[90:91], v[90:91], 0, v[84:85]
	v_pk_mul_f32 v[86:87], v[80:81], v[88:89] op_sel_hi:[1,0]
	v_pk_mul_f32 v[84:85], v[78:79], v[88:89] op_sel_hi:[1,0]
	s_nop 0
	v_cvt_pk_bf16_f32 v84, v84, v85
	v_cvt_pk_bf16_f32 v85, v86, v87
	v_cvt_pk_bf16_f32 v86, v94, v95
	ds_read2_b32 v[94:95], v158 offset0:128 offset1:144
	v_cvt_pk_bf16_f32 v87, v92, v93
	ds_bpermute_b32 v232, v244, v84
	ds_bpermute_b32 v233, v244, v85
	ds_bpermute_b32 v234, v244, v86
	ds_bpermute_b32 v235, v244, v87
	ds_bpermute_b32 v236, v244, v90
	ds_bpermute_b32 v237, v244, v91
	s_waitcnt lgkmcnt(0)
	global_store_dwordx4 v[236:237], v[232:235], off
	v_pk_mul_f32 v[92:93], v[68:69], v[88:89] op_sel_hi:[1,0]
	s_nop 0
	v_pk_mul_f32 v[86:87], v[72:73], v[88:89] op_sel_hi:[1,0]
	v_pk_mul_f32 v[84:85], v[70:71], v[88:89] op_sel_hi:[1,0]
	v_pk_mul_f32 v[88:89], v[66:67], v[88:89] op_sel_hi:[1,0]
	v_cvt_pk_bf16_f32 v84, v84, v85
	v_cvt_pk_bf16_f32 v85, v86, v87
	v_cvt_pk_bf16_f32 v87, v92, v93
	s_waitcnt lgkmcnt(0)
	v_pk_mul_f32 v[92:93], v[58:59], v[94:95] op_sel_hi:[1,0]
	v_cvt_pk_bf16_f32 v86, v88, v89
	ds_bpermute_b32 v238, v244, v84
	ds_bpermute_b32 v239, v244, v85
	ds_bpermute_b32 v240, v244, v86
	ds_bpermute_b32 v241, v244, v87
	ds_bpermute_b32 v242, v244, v90
	ds_bpermute_b32 v243, v244, v91
	s_waitcnt lgkmcnt(0)
	global_store_dwordx4 v[242:243], v[238:241], off offset:64
	v_pk_mul_f32 v[90:91], v[60:61], v[94:95] op_sel_hi:[1,0]
	v_lshl_add_u64 v[88:89], v[82:83], 0, s[16:17]
	v_pk_mul_f32 v[86:87], v[64:65], v[94:95] op_sel_hi:[1,0]
	v_pk_mul_f32 v[84:85], v[62:63], v[94:95] op_sel_hi:[1,0]
	s_mov_b64 s[16:17], 0x90000
	v_cvt_pk_bf16_f32 v84, v84, v85
	v_cvt_pk_bf16_f32 v85, v86, v87
	v_cvt_pk_bf16_f32 v87, v90, v91
	v_add_co_u32_e32 v90, vcc, s15, v82
	v_cvt_pk_bf16_f32 v86, v92, v93
	v_pk_mul_f32 v[92:93], v[50:51], v[94:95] op_sel_hi:[1,0]
	s_nop 0
	v_addc_co_u32_e32 v91, vcc, 0, v83, vcc
	ds_bpermute_b32 v232, v244, v84
	ds_bpermute_b32 v233, v244, v85
	ds_bpermute_b32 v234, v244, v86
	ds_bpermute_b32 v235, v244, v87
	ds_bpermute_b32 v236, v244, v90
	ds_bpermute_b32 v237, v244, v91
	s_waitcnt lgkmcnt(0)
	global_store_dwordx4 v[236:237], v[232:235], off
	v_pk_mul_f32 v[90:91], v[52:53], v[94:95] op_sel_hi:[1,0]
	s_mov_b32 s15, 0x90000
	v_pk_mul_f32 v[86:87], v[56:57], v[94:95] op_sel_hi:[1,0]
	v_pk_mul_f32 v[84:85], v[54:55], v[94:95] op_sel_hi:[1,0]
	s_nop 0
	v_cvt_pk_bf16_f32 v84, v84, v85
	v_cvt_pk_bf16_f32 v85, v86, v87
	v_cvt_pk_bf16_f32 v86, v92, v93
	v_cvt_pk_bf16_f32 v87, v90, v91
	v_mov_b32_e32 v90, v95
	ds_bpermute_b32 v238, v244, v84
	ds_bpermute_b32 v239, v244, v85
	ds_bpermute_b32 v240, v244, v86
	ds_bpermute_b32 v241, v244, v87
	ds_bpermute_b32 v242, v244, v88
	ds_bpermute_b32 v243, v244, v89
	s_waitcnt lgkmcnt(0)
	global_store_dwordx4 v[242:243], v[238:241], off offset:64
	v_pk_mul_f32 v[94:95], v[42:43], v[90:91] op_sel_hi:[1,0]
	v_pk_mul_f32 v[92:93], v[44:45], v[90:91] op_sel_hi:[1,0]
	v_pk_mul_f32 v[86:87], v[48:49], v[90:91] op_sel_hi:[1,0]
	v_pk_mul_f32 v[84:85], v[46:47], v[90:91] op_sel_hi:[1,0]
	v_lshl_add_u64 v[88:89], v[82:83], 0, s[16:17]
	v_cvt_pk_bf16_f32 v84, v84, v85
	v_cvt_pk_bf16_f32 v85, v86, v87
	v_cvt_pk_bf16_f32 v86, v94, v95
	ds_read2_b32 v[94:95], v158 offset0:160 offset1:176
	v_cvt_pk_bf16_f32 v87, v92, v93
	v_add_co_u32_e32 v92, vcc, s15, v82
	s_mov_b32 s15, 0xa0000
	s_nop 0
	v_addc_co_u32_e32 v93, vcc, 0, v83, vcc
	ds_bpermute_b32 v232, v244, v84
	ds_bpermute_b32 v233, v244, v85
	ds_bpermute_b32 v234, v244, v86
	ds_bpermute_b32 v235, v244, v87
	ds_bpermute_b32 v236, v244, v92
	ds_bpermute_b32 v237, v244, v93
	s_waitcnt lgkmcnt(0)
	global_store_dwordx4 v[236:237], v[232:235], off
	v_pk_mul_f32 v[92:93], v[36:37], v[90:91] op_sel_hi:[1,0]
	s_mov_b64 s[16:17], 0xa0000
	v_pk_mul_f32 v[86:87], v[40:41], v[90:91] op_sel_hi:[1,0]
	v_pk_mul_f32 v[84:85], v[38:39], v[90:91] op_sel_hi:[1,0]
	v_pk_mul_f32 v[90:91], v[34:35], v[90:91] op_sel_hi:[1,0]
	v_cvt_pk_bf16_f32 v84, v84, v85
	v_cvt_pk_bf16_f32 v85, v86, v87
	v_cvt_pk_bf16_f32 v87, v92, v93
	s_waitcnt lgkmcnt(0)
	v_pk_mul_f32 v[92:93], v[26:27], v[94:95] op_sel_hi:[1,0]
	v_cvt_pk_bf16_f32 v86, v90, v91
	ds_bpermute_b32 v238, v244, v84
	ds_bpermute_b32 v239, v244, v85
	ds_bpermute_b32 v240, v244, v86
	ds_bpermute_b32 v241, v244, v87
	ds_bpermute_b32 v242, v244, v88
	ds_bpermute_b32 v243, v244, v89
	s_waitcnt lgkmcnt(0)
	global_store_dwordx4 v[242:243], v[238:241], off offset:64
	v_pk_mul_f32 v[90:91], v[28:29], v[94:95] op_sel_hi:[1,0]
	v_lshl_add_u64 v[88:89], v[82:83], 0, s[16:17]
	v_pk_mul_f32 v[86:87], v[32:33], v[94:95] op_sel_hi:[1,0]
	v_pk_mul_f32 v[84:85], v[30:31], v[94:95] op_sel_hi:[1,0]
	s_mov_b64 s[16:17], 0xb0000
	v_cvt_pk_bf16_f32 v84, v84, v85
	v_cvt_pk_bf16_f32 v85, v86, v87
	v_cvt_pk_bf16_f32 v87, v90, v91
	v_add_co_u32_e32 v90, vcc, s15, v82
	v_cvt_pk_bf16_f32 v86, v92, v93
	s_mov_b32 s15, 0xb0000
	s_nop 0
	v_addc_co_u32_e32 v91, vcc, 0, v83, vcc
	ds_bpermute_b32 v232, v244, v84
	ds_bpermute_b32 v233, v244, v85
	ds_bpermute_b32 v234, v244, v86
	ds_bpermute_b32 v235, v244, v87
	ds_bpermute_b32 v236, v244, v90
	ds_bpermute_b32 v237, v244, v91
	s_waitcnt lgkmcnt(0)
	global_store_dwordx4 v[236:237], v[232:235], off
	v_pk_mul_f32 v[90:91], v[20:21], v[94:95] op_sel_hi:[1,0]
	v_pk_mul_f32 v[92:93], v[18:19], v[94:95] op_sel_hi:[1,0]
	v_pk_mul_f32 v[86:87], v[24:25], v[94:95] op_sel_hi:[1,0]
	v_pk_mul_f32 v[84:85], v[22:23], v[94:95] op_sel_hi:[1,0]
	s_nop 0
	v_cvt_pk_bf16_f32 v84, v84, v85
	v_cvt_pk_bf16_f32 v85, v86, v87
	v_cvt_pk_bf16_f32 v87, v90, v91
	v_mov_b32_e32 v90, v95
	v_cvt_pk_bf16_f32 v86, v92, v93
	ds_bpermute_b32 v238, v244, v84
	ds_bpermute_b32 v239, v244, v85
	ds_bpermute_b32 v240, v244, v86
	ds_bpermute_b32 v241, v244, v87
	ds_bpermute_b32 v242, v244, v88
	ds_bpermute_b32 v243, v244, v89
	s_waitcnt lgkmcnt(0)
	global_store_dwordx4 v[242:243], v[238:241], off offset:64
	v_lshl_add_u64 v[88:89], v[82:83], 0, s[16:17]
	v_add_co_u32_e32 v82, vcc, s15, v82
	v_pk_mul_f32 v[84:85], v[14:15], v[90:91] op_sel_hi:[1,0]
	v_pk_mul_f32 v[86:87], v[16:17], v[90:91] op_sel_hi:[1,0]
	v_cvt_pk_bf16_f32 v84, v84, v85
	v_addc_co_u32_e32 v83, vcc, 0, v83, vcc
	v_cvt_pk_bf16_f32 v85, v86, v87
	v_pk_mul_f32 v[92:93], v[12:13], v[90:91] op_sel_hi:[1,0]
	v_pk_mul_f32 v[94:95], v[10:11], v[90:91] op_sel_hi:[1,0]
	v_cvt_pk_bf16_f32 v87, v92, v93
	s_nop 0
	v_cvt_pk_bf16_f32 v86, v94, v95
	ds_bpermute_b32 v232, v244, v84
	ds_bpermute_b32 v233, v244, v85
	ds_bpermute_b32 v234, v244, v86
	ds_bpermute_b32 v235, v244, v87
	ds_bpermute_b32 v236, v244, v82
	ds_bpermute_b32 v237, v244, v83
	s_waitcnt lgkmcnt(0)
	global_store_dwordx4 v[236:237], v[232:235], off
	v_pk_mul_f32 v[82:83], v[6:7], v[90:91] op_sel_hi:[1,0]
	s_nop 0
	v_pk_mul_f32 v[84:85], v[8:9], v[90:91] op_sel_hi:[1,0]
	v_pk_mul_f32 v[86:87], v[4:5], v[90:91] op_sel_hi:[1,0]
	v_pk_mul_f32 v[90:91], v[2:3], v[90:91] op_sel_hi:[1,0]
	v_cvt_pk_bf16_f32 v82, v82, v83
	v_cvt_pk_bf16_f32 v83, v84, v85
	v_cvt_pk_bf16_f32 v85, v86, v87
	s_nop 0
	v_cvt_pk_bf16_f32 v84, v90, v91
	ds_bpermute_b32 v238, v244, v82
	ds_bpermute_b32 v239, v244, v83
	ds_bpermute_b32 v240, v244, v84
	ds_bpermute_b32 v241, v244, v85
	ds_bpermute_b32 v242, v244, v88
	ds_bpermute_b32 v243, v244, v89
	s_waitcnt lgkmcnt(0)
	global_store_dwordx4 v[242:243], v[238:241], off offset:64
	s_cbranch_execz .LBB0_178

.LBB0_178:
	s_lshl_b32 s14, s14, 10
	v_add_u32_e32 v213, s14, v211
	ds_read_b32 v82, v213
	s_waitcnt lgkmcnt(0)
	v_pk_mul_f32 v[84:85], v[146:147], v[82:83] op_sel_hi:[1,0]
	v_pk_mul_f32 v[86:87], v[144:145], v[82:83] op_sel_hi:[1,0]
	v_pk_mul_f32 v[84:85], v[84:85], v[84:85]
	v_pk_mul_f32 v[88:89], v[140:141], v[82:83] op_sel_hi:[1,0]
	v_pk_fma_f32 v[84:85], v[86:87], v[86:87], v[84:85]
	v_pk_mul_f32 v[86:87], v[142:143], v[82:83] op_sel_hi:[1,0]
	s_nop 0
	v_pk_mul_f32 v[86:87], v[86:87], v[86:87]
	s_nop 0
	v_pk_fma_f32 v[86:87], v[88:89], v[88:89], v[86:87]
	v_pk_mul_f32 v[88:89], v[136:137], v[82:83] op_sel_hi:[1,0]
	v_pk_add_f32 v[84:85], v[84:85], v[86:87]
	v_pk_mul_f32 v[86:87], v[138:139], v[82:83] op_sel_hi:[1,0]
	s_nop 0
	v_pk_mul_f32 v[86:87], v[86:87], v[86:87]
	s_nop 0
	v_pk_fma_f32 v[86:87], v[88:89], v[88:89], v[86:87]
	s_nop 0
	v_pk_add_f32 v[84:85], v[86:87], v[84:85]
	v_pk_mul_f32 v[86:87], v[134:135], v[82:83] op_sel_hi:[1,0]
	v_pk_mul_f32 v[82:83], v[132:133], v[82:83] op_sel_hi:[1,0]
	v_pk_mul_f32 v[86:87], v[86:87], v[86:87]
	s_nop 0
	v_pk_fma_f32 v[82:83], v[82:83], v[82:83], v[86:87]
	s_nop 0
	v_pk_add_f32 v[82:83], v[82:83], v[84:85]
	s_nop 0
	v_add_f32_e32 v82, v82, v83
	ds_swizzle_b32 v83, v82 offset:swizzle(SWAP,16)
	s_waitcnt lgkmcnt(0)
	v_add_f32_e32 v82, v82, v83
	v_mov_b32_e32 v83, v82
	s_nop 1
	v_permlane32_swap_b32_e32 v82, v83
	s_and_saveexec_b64 s[62:63], s[38:39]
	v_add_f32_e32 v82, v82, v83
	ds_write_b32 v183, v82
	s_or_b64 exec, exec, s[62:63]
	ds_read_b32 v82, v213 offset:64
	s_waitcnt lgkmcnt(0)
	v_pk_mul_f32 v[84:85], v[130:131], v[82:83] op_sel_hi:[1,0]
	v_pk_mul_f32 v[86:87], v[128:129], v[82:83] op_sel_hi:[1,0]
	v_pk_mul_f32 v[84:85], v[84:85], v[84:85]
	v_pk_mul_f32 v[88:89], v[124:125], v[82:83] op_sel_hi:[1,0]
	v_pk_fma_f32 v[84:85], v[86:87], v[86:87], v[84:85]
	v_pk_mul_f32 v[86:87], v[126:127], v[82:83] op_sel_hi:[1,0]
	s_nop 0
	v_pk_mul_f32 v[86:87], v[86:87], v[86:87]
	s_nop 0
	v_pk_fma_f32 v[86:87], v[88:89], v[88:89], v[86:87]
	v_pk_mul_f32 v[88:89], v[120:121], v[82:83] op_sel_hi:[1,0]
	v_pk_add_f32 v[84:85], v[84:85], v[86:87]
	v_pk_mul_f32 v[86:87], v[122:123], v[82:83] op_sel_hi:[1,0]
	s_nop 0
	v_pk_mul_f32 v[86:87], v[86:87], v[86:87]
	s_nop 0
	v_pk_fma_f32 v[86:87], v[88:89], v[88:89], v[86:87]
	s_nop 0
	v_pk_add_f32 v[84:85], v[86:87], v[84:85]
	v_pk_mul_f32 v[86:87], v[118:119], v[82:83] op_sel_hi:[1,0]
	v_pk_mul_f32 v[82:83], v[116:117], v[82:83] op_sel_hi:[1,0]
	v_pk_mul_f32 v[86:87], v[86:87], v[86:87]
	s_nop 0
	v_pk_fma_f32 v[82:83], v[82:83], v[82:83], v[86:87]
	s_nop 0
	v_pk_add_f32 v[82:83], v[82:83], v[84:85]
	s_nop 0
	v_add_f32_e32 v82, v82, v83
	ds_swizzle_b32 v83, v82 offset:swizzle(SWAP,16)
	s_waitcnt lgkmcnt(0)
	v_add_f32_e32 v82, v82, v83
	v_mov_b32_e32 v83, v82
	s_nop 1
	v_permlane32_swap_b32_e32 v82, v83
	s_and_saveexec_b64 s[62:63], s[38:39]
	v_add_f32_e32 v82, v82, v83
	ds_write_b32 v195, v82
	s_or_b64 exec, exec, s[62:63]
	ds_read_b32 v82, v213 offset:128
	s_waitcnt lgkmcnt(0)
	v_pk_mul_f32 v[84:85], v[112:113], v[82:83] op_sel_hi:[1,0]
	v_pk_mul_f32 v[86:87], v[110:111], v[82:83] op_sel_hi:[1,0]
	v_pk_mul_f32 v[84:85], v[84:85], v[84:85]
	v_pk_mul_f32 v[88:89], v[106:107], v[82:83] op_sel_hi:[1,0]
	v_pk_fma_f32 v[84:85], v[86:87], v[86:87], v[84:85]
	v_pk_mul_f32 v[86:87], v[108:109], v[82:83] op_sel_hi:[1,0]
	s_nop 0
	v_pk_mul_f32 v[86:87], v[86:87], v[86:87]
	s_nop 0
	v_pk_fma_f32 v[86:87], v[88:89], v[88:89], v[86:87]
	v_pk_mul_f32 v[88:89], v[102:103], v[82:83] op_sel_hi:[1,0]
	v_pk_add_f32 v[84:85], v[84:85], v[86:87]
	v_pk_mul_f32 v[86:87], v[104:105], v[82:83] op_sel_hi:[1,0]
	s_nop 0
	v_pk_mul_f32 v[86:87], v[86:87], v[86:87]
	s_nop 0
	v_pk_fma_f32 v[86:87], v[88:89], v[88:89], v[86:87]
	s_nop 0
	v_pk_add_f32 v[84:85], v[86:87], v[84:85]
	v_pk_mul_f32 v[86:87], v[100:101], v[82:83] op_sel_hi:[1,0]
	v_pk_mul_f32 v[82:83], v[98:99], v[82:83] op_sel_hi:[1,0]
	v_pk_mul_f32 v[86:87], v[86:87], v[86:87]
	s_nop 0
	v_pk_fma_f32 v[82:83], v[82:83], v[82:83], v[86:87]
	s_nop 0
	v_pk_add_f32 v[82:83], v[82:83], v[84:85]
	s_nop 0
	v_add_f32_e32 v82, v82, v83
	ds_swizzle_b32 v83, v82 offset:swizzle(SWAP,16)
	s_waitcnt lgkmcnt(0)
	v_add_f32_e32 v82, v82, v83
	v_mov_b32_e32 v83, v82
	s_nop 1
	v_permlane32_swap_b32_e32 v82, v83
	s_and_saveexec_b64 s[62:63], s[38:39]
	v_add_f32_e32 v82, v82, v83
	ds_write_b32 v197, v82
	s_or_b64 exec, exec, s[62:63]
	ds_read_b32 v82, v213 offset:192
	s_waitcnt lgkmcnt(0)
	v_pk_mul_f32 v[84:85], v[80:81], v[82:83] op_sel_hi:[1,0]
	v_pk_mul_f32 v[86:87], v[78:79], v[82:83] op_sel_hi:[1,0]
	v_pk_mul_f32 v[84:85], v[84:85], v[84:85]
	v_pk_mul_f32 v[88:89], v[74:75], v[82:83] op_sel_hi:[1,0]
	v_pk_fma_f32 v[84:85], v[86:87], v[86:87], v[84:85]
	v_pk_mul_f32 v[86:87], v[76:77], v[82:83] op_sel_hi:[1,0]
	s_nop 0
	v_pk_mul_f32 v[86:87], v[86:87], v[86:87]
	s_nop 0
	v_pk_fma_f32 v[86:87], v[88:89], v[88:89], v[86:87]
	v_pk_mul_f32 v[88:89], v[70:71], v[82:83] op_sel_hi:[1,0]
	v_pk_add_f32 v[84:85], v[84:85], v[86:87]
	v_pk_mul_f32 v[86:87], v[72:73], v[82:83] op_sel_hi:[1,0]
	s_nop 0
	v_pk_mul_f32 v[86:87], v[86:87], v[86:87]
	s_nop 0
	v_pk_fma_f32 v[86:87], v[88:89], v[88:89], v[86:87]
	s_nop 0
	v_pk_add_f32 v[84:85], v[86:87], v[84:85]
	v_pk_mul_f32 v[86:87], v[68:69], v[82:83] op_sel_hi:[1,0]
	v_pk_mul_f32 v[82:83], v[66:67], v[82:83] op_sel_hi:[1,0]
	v_pk_mul_f32 v[86:87], v[86:87], v[86:87]
	s_nop 0
	v_pk_fma_f32 v[82:83], v[82:83], v[82:83], v[86:87]
	s_nop 0
	v_pk_add_f32 v[82:83], v[82:83], v[84:85]
	s_nop 0
	v_add_f32_e32 v82, v82, v83
	ds_swizzle_b32 v83, v82 offset:swizzle(SWAP,16)
	s_waitcnt lgkmcnt(0)
	v_add_f32_e32 v82, v82, v83
	v_mov_b32_e32 v83, v82
	s_nop 1
	v_permlane32_swap_b32_e32 v82, v83
	s_and_saveexec_b64 s[62:63], s[38:39]
	v_add_f32_e32 v82, v82, v83
	ds_write_b32 v199, v82
	s_or_b64 exec, exec, s[62:63]
	ds_read_b32 v82, v213 offset:512
	s_waitcnt lgkmcnt(0)
	v_pk_mul_f32 v[84:85], v[64:65], v[82:83] op_sel_hi:[1,0]
	v_pk_mul_f32 v[86:87], v[62:63], v[82:83] op_sel_hi:[1,0]
	v_pk_mul_f32 v[84:85], v[84:85], v[84:85]
	v_pk_mul_f32 v[88:89], v[58:59], v[82:83] op_sel_hi:[1,0]
	v_pk_fma_f32 v[84:85], v[86:87], v[86:87], v[84:85]
	v_pk_mul_f32 v[86:87], v[60:61], v[82:83] op_sel_hi:[1,0]
	s_nop 0
	v_pk_mul_f32 v[86:87], v[86:87], v[86:87]
	s_nop 0
	v_pk_fma_f32 v[86:87], v[88:89], v[88:89], v[86:87]
	v_pk_mul_f32 v[88:89], v[54:55], v[82:83] op_sel_hi:[1,0]
	v_pk_add_f32 v[84:85], v[84:85], v[86:87]
	v_pk_mul_f32 v[86:87], v[56:57], v[82:83] op_sel_hi:[1,0]
	s_nop 0
	v_pk_mul_f32 v[86:87], v[86:87], v[86:87]
	s_nop 0
	v_pk_fma_f32 v[86:87], v[88:89], v[88:89], v[86:87]
	s_nop 0
	v_pk_add_f32 v[84:85], v[86:87], v[84:85]
	v_pk_mul_f32 v[86:87], v[52:53], v[82:83] op_sel_hi:[1,0]
	v_pk_mul_f32 v[82:83], v[50:51], v[82:83] op_sel_hi:[1,0]
	v_pk_mul_f32 v[86:87], v[86:87], v[86:87]
	s_nop 0
	v_pk_fma_f32 v[82:83], v[82:83], v[82:83], v[86:87]
	s_nop 0
	v_pk_add_f32 v[82:83], v[82:83], v[84:85]
	s_nop 0
	v_add_f32_e32 v82, v82, v83
	ds_swizzle_b32 v83, v82 offset:swizzle(SWAP,16)
	s_waitcnt lgkmcnt(0)
	v_add_f32_e32 v82, v82, v83
	v_mov_b32_e32 v83, v82
	s_nop 1
	v_permlane32_swap_b32_e32 v82, v83
	s_and_saveexec_b64 s[62:63], s[38:39]
	v_add_f32_e32 v82, v82, v83
	ds_write_b32 v201, v82
	s_or_b64 exec, exec, s[62:63]
	ds_read_b32 v82, v213 offset:576
	s_waitcnt lgkmcnt(0)
	v_pk_mul_f32 v[84:85], v[48:49], v[82:83] op_sel_hi:[1,0]
	v_pk_mul_f32 v[86:87], v[46:47], v[82:83] op_sel_hi:[1,0]
	v_pk_mul_f32 v[84:85], v[84:85], v[84:85]
	v_pk_mul_f32 v[88:89], v[42:43], v[82:83] op_sel_hi:[1,0]
	v_pk_fma_f32 v[84:85], v[86:87], v[86:87], v[84:85]
	v_pk_mul_f32 v[86:87], v[44:45], v[82:83] op_sel_hi:[1,0]
	s_nop 0
	v_pk_mul_f32 v[86:87], v[86:87], v[86:87]
	s_nop 0
	v_pk_fma_f32 v[86:87], v[88:89], v[88:89], v[86:87]
	v_pk_mul_f32 v[88:89], v[38:39], v[82:83] op_sel_hi:[1,0]
	v_pk_add_f32 v[84:85], v[84:85], v[86:87]
	v_pk_mul_f32 v[86:87], v[40:41], v[82:83] op_sel_hi:[1,0]
	s_nop 0
	v_pk_mul_f32 v[86:87], v[86:87], v[86:87]
	s_nop 0
	v_pk_fma_f32 v[86:87], v[88:89], v[88:89], v[86:87]
	s_nop 0
	v_pk_add_f32 v[84:85], v[86:87], v[84:85]
	v_pk_mul_f32 v[86:87], v[36:37], v[82:83] op_sel_hi:[1,0]
	v_pk_mul_f32 v[82:83], v[34:35], v[82:83] op_sel_hi:[1,0]
	v_pk_mul_f32 v[86:87], v[86:87], v[86:87]
	s_nop 0
	v_pk_fma_f32 v[82:83], v[82:83], v[82:83], v[86:87]
	s_nop 0
	v_pk_add_f32 v[82:83], v[82:83], v[84:85]
	s_nop 0
	v_add_f32_e32 v82, v82, v83
	ds_swizzle_b32 v83, v82 offset:swizzle(SWAP,16)
	s_waitcnt lgkmcnt(0)
	v_add_f32_e32 v82, v82, v83
	v_mov_b32_e32 v83, v82
	s_nop 1
	v_permlane32_swap_b32_e32 v82, v83
	s_and_saveexec_b64 s[62:63], s[38:39]
	v_add_f32_e32 v82, v82, v83
	ds_write_b32 v203, v82
	s_or_b64 exec, exec, s[62:63]
	ds_read_b32 v82, v213 offset:640
	s_waitcnt lgkmcnt(0)
	v_pk_mul_f32 v[84:85], v[32:33], v[82:83] op_sel_hi:[1,0]
	v_pk_mul_f32 v[86:87], v[30:31], v[82:83] op_sel_hi:[1,0]
	v_pk_mul_f32 v[84:85], v[84:85], v[84:85]
	v_pk_mul_f32 v[88:89], v[26:27], v[82:83] op_sel_hi:[1,0]
	v_pk_fma_f32 v[84:85], v[86:87], v[86:87], v[84:85]
	v_pk_mul_f32 v[86:87], v[28:29], v[82:83] op_sel_hi:[1,0]
	s_nop 0
	v_pk_mul_f32 v[86:87], v[86:87], v[86:87]
	s_nop 0
	v_pk_fma_f32 v[86:87], v[88:89], v[88:89], v[86:87]
	v_pk_mul_f32 v[88:89], v[22:23], v[82:83] op_sel_hi:[1,0]
	v_pk_add_f32 v[84:85], v[84:85], v[86:87]
	v_pk_mul_f32 v[86:87], v[24:25], v[82:83] op_sel_hi:[1,0]
	s_nop 0
	v_pk_mul_f32 v[86:87], v[86:87], v[86:87]
	s_nop 0
	v_pk_fma_f32 v[86:87], v[88:89], v[88:89], v[86:87]
	s_nop 0
	v_pk_add_f32 v[84:85], v[86:87], v[84:85]
	v_pk_mul_f32 v[86:87], v[20:21], v[82:83] op_sel_hi:[1,0]
	v_pk_mul_f32 v[82:83], v[18:19], v[82:83] op_sel_hi:[1,0]
	v_pk_mul_f32 v[86:87], v[86:87], v[86:87]
	s_nop 0
	v_pk_fma_f32 v[82:83], v[82:83], v[82:83], v[86:87]
	s_nop 0
	v_pk_add_f32 v[82:83], v[82:83], v[84:85]
	s_nop 0
	v_add_f32_e32 v82, v82, v83
	ds_swizzle_b32 v83, v82 offset:swizzle(SWAP,16)
	s_waitcnt lgkmcnt(0)
	v_add_f32_e32 v82, v82, v83
	v_mov_b32_e32 v83, v82
	s_nop 1
	v_permlane32_swap_b32_e32 v82, v83
	s_and_saveexec_b64 s[62:63], s[38:39]
	v_add_f32_e32 v82, v82, v83
	ds_write_b32 v205, v82
	s_or_b64 exec, exec, s[62:63]
	ds_read_b32 v82, v213 offset:704
	s_waitcnt lgkmcnt(0)
	v_pk_mul_f32 v[84:85], v[16:17], v[82:83] op_sel_hi:[1,0]
	v_pk_mul_f32 v[86:87], v[14:15], v[82:83] op_sel_hi:[1,0]
	v_pk_mul_f32 v[84:85], v[84:85], v[84:85]
	v_pk_mul_f32 v[88:89], v[10:11], v[82:83] op_sel_hi:[1,0]
	v_pk_fma_f32 v[84:85], v[86:87], v[86:87], v[84:85]
	v_pk_mul_f32 v[86:87], v[12:13], v[82:83] op_sel_hi:[1,0]
	s_nop 0
	v_pk_mul_f32 v[86:87], v[86:87], v[86:87]
	s_nop 0
	v_pk_fma_f32 v[86:87], v[88:89], v[88:89], v[86:87]
	v_pk_mul_f32 v[88:89], v[6:7], v[82:83] op_sel_hi:[1,0]
	v_pk_add_f32 v[84:85], v[84:85], v[86:87]
	v_pk_mul_f32 v[86:87], v[8:9], v[82:83] op_sel_hi:[1,0]
	s_nop 0
	v_pk_mul_f32 v[86:87], v[86:87], v[86:87]
	s_nop 0
	v_pk_fma_f32 v[86:87], v[88:89], v[88:89], v[86:87]
	s_nop 0
	v_pk_add_f32 v[84:85], v[86:87], v[84:85]
	v_pk_mul_f32 v[86:87], v[4:5], v[82:83] op_sel_hi:[1,0]
	v_pk_mul_f32 v[82:83], v[2:3], v[82:83] op_sel_hi:[1,0]
	v_pk_mul_f32 v[86:87], v[86:87], v[86:87]
	s_nop 0
	v_pk_fma_f32 v[82:83], v[82:83], v[82:83], v[86:87]
	s_nop 0
	v_pk_add_f32 v[82:83], v[82:83], v[84:85]
	s_nop 0
	v_add_f32_e32 v82, v82, v83
	ds_swizzle_b32 v83, v82 offset:swizzle(SWAP,16)
	s_waitcnt lgkmcnt(0)
	v_add_f32_e32 v82, v82, v83
	v_mov_b32_e32 v83, v82
	s_nop 1
	v_permlane32_swap_b32_e32 v82, v83
	s_and_saveexec_b64 s[62:63], s[38:39]
	v_add_f32_e32 v82, v82, v83
	ds_write_b32 v207, v82
	s_or_b64 exec, exec, s[62:63]
	s_waitcnt lgkmcnt(0)
	s_barrier
	global_load_dwordx4 v[94:97], v[168:169], off offset:16
	global_load_dwordx4 v[90:93], v[168:169], off
	global_load_dwordx4 v[82:85], v[168:169], off offset:144
	global_load_dwordx4 v[86:89], v[168:169], off offset:128
	ds_read_b32 v158, v183
	ds_read_b32 v159, v194
	s_lshl_b32 s14, s60, 1
	s_and_b32 s14, s14, 14
	s_lshl_b32 s15, s28, 1
	s_or_b32 s14, s88, s14
	s_waitcnt lgkmcnt(0)
	v_add_f32_e32 v158, v158, v159
	v_fmamk_f32 v158, v158, 0x3c000000, v185
	v_rsq_f32_e32 v160, v158
	ds_read2_b32 v[158:159], v213 offset1:16
	s_and_b32 s15, s15, 0x7fffff0
	s_or_b32 s14, s15, s14
	s_lshl_b32 s15, s28, 2
	s_and_b32 s15, s15, 28
	s_waitcnt lgkmcnt(0)
	v_mul_f32_e32 v158, v158, v160
	v_lshlrev_b64 v[160:161], 12, v[174:175]
	v_lshl_add_u64 v[160:161], s[46:47], 0, v[160:161]
	v_pk_mul_f32 v[144:145], v[144:145], v[158:159] op_sel_hi:[1,0]
	v_pk_mul_f32 v[146:147], v[146:147], v[158:159] op_sel_hi:[1,0]
	v_pk_mul_f32 v[218:219], v[140:141], v[158:159] op_sel_hi:[1,0]
	v_lshl_add_u64 v[160:161], v[160:161], 0, v[114:115]
	v_pk_mul_f32 v[140:141], v[142:143], v[158:159] op_sel_hi:[1,0]
	s_lshl_b32 s14, s14, 5
	s_add_i32 s15, s15, s8
	s_add_i32 s28, s15, s14
	s_ashr_i32 s29, s28, 31
	s_lshl_b64 s[14:15], s[28:29], 9
	s_waitcnt vmcnt(0)
	v_pk_mul_f32 v[142:143], v[94:95], v[218:219]
	v_pk_mul_f32 v[214:215], v[92:93], v[146:147]
	v_pk_mul_f32 v[216:217], v[90:91], v[144:145]
	v_pk_fma_f32 v[218:219], v[90:91], v[144:145], 0 op_sel_hi:[1,1,0]
	v_cvt_pk_bf16_f32 v144, v216, v217
	v_cvt_pk_bf16_f32 v145, v214, v215
	v_pk_mul_f32 v[140:141], v[96:97], v[140:141]
	v_pk_fma_f32 v[220:221], v[92:93], v[146:147], 0 op_sel_hi:[1,1,0]
	v_cvt_pk_bf16_f32 v146, v142, v143
	v_cvt_pk_bf16_f32 v147, v140, v141
	ds_bpermute_b32 v232, v244, v144
	ds_bpermute_b32 v233, v244, v145
	ds_bpermute_b32 v234, v244, v146
	ds_bpermute_b32 v235, v244, v147
	ds_bpermute_b32 v236, v244, v160
	ds_bpermute_b32 v237, v244, v161
	s_waitcnt lgkmcnt(0)
	global_store_dwordx4 v[236:237], v[232:235], off
	s_nop 1
	v_pk_mul_f32 v[144:145], v[136:137], v[158:159] op_sel_hi:[1,0]
	v_pk_mul_f32 v[136:137], v[138:139], v[158:159] op_sel_hi:[1,0]
	v_pk_mul_f32 v[138:139], v[86:87], v[144:145]
	v_pk_mul_f32 v[144:145], v[132:133], v[158:159] op_sel_hi:[1,0]
	v_pk_mul_f32 v[132:133], v[134:135], v[158:159] op_sel_hi:[1,0]
	v_pk_mul_f32 v[136:137], v[88:89], v[136:137]
	v_pk_mul_f32 v[132:133], v[84:85], v[132:133]
	v_pk_mul_f32 v[134:135], v[82:83], v[144:145]
	v_cvt_pk_bf16_f32 v144, v138, v139
	v_cvt_pk_bf16_f32 v145, v136, v137
	v_cvt_pk_bf16_f32 v147, v132, v133
	s_nop 0
	v_cvt_pk_bf16_f32 v146, v134, v135
	ds_bpermute_b32 v238, v244, v144
	ds_bpermute_b32 v239, v244, v145
	ds_bpermute_b32 v240, v244, v146
	ds_bpermute_b32 v241, v244, v147
	ds_bpermute_b32 v242, v244, v160
	ds_bpermute_b32 v243, v244, v161
	s_waitcnt lgkmcnt(0)
	global_store_dwordx4 v[242:243], v[238:241], off offset:64
	ds_read_b32 v144, v195
	ds_read_b32 v145, v196
	v_lshlrev_b64 v[146:147], 12, v[180:181]
	v_lshl_add_u64 v[146:147], s[46:47], 0, v[146:147]
	v_lshl_add_u64 v[146:147], v[146:147], 0, v[114:115]
	s_waitcnt lgkmcnt(0)
	v_add_f32_e32 v144, v144, v145
	v_fmamk_f32 v144, v144, 0x3c000000, v185
	v_rsq_f32_e32 v144, v144
	s_nop 0
	v_mul_f32_e32 v144, v159, v144
	v_pk_mul_f32 v[128:129], v[128:129], v[144:145] op_sel_hi:[1,0]
	v_pk_mul_f32 v[130:131], v[130:131], v[144:145] op_sel_hi:[1,0]
	v_pk_mul_f32 v[160:161], v[90:91], v[128:129]
	v_pk_mul_f32 v[158:159], v[92:93], v[130:131]
	v_pk_mul_f32 v[180:181], v[124:125], v[144:145] op_sel_hi:[1,0]
	v_pk_mul_f32 v[124:125], v[126:127], v[144:145] op_sel_hi:[1,0]
	v_pk_fma_f32 v[214:215], v[90:91], v[128:129], v[218:219]
	v_cvt_pk_bf16_f32 v128, v160, v161
	v_cvt_pk_bf16_f32 v129, v158, v159
	v_pk_mul_f32 v[124:125], v[96:97], v[124:125]
	v_pk_mul_f32 v[126:127], v[94:95], v[180:181]
	v_pk_fma_f32 v[180:181], v[92:93], v[130:131], v[220:221]
	v_cvt_pk_bf16_f32 v130, v126, v127
	v_cvt_pk_bf16_f32 v131, v124, v125
	ds_bpermute_b32 v232, v244, v128
	ds_bpermute_b32 v233, v244, v129
	ds_bpermute_b32 v234, v244, v130
	ds_bpermute_b32 v235, v244, v131
	ds_bpermute_b32 v236, v244, v146
	ds_bpermute_b32 v237, v244, v147
	s_waitcnt lgkmcnt(0)
	global_store_dwordx4 v[236:237], v[232:235], off
	s_nop 1
	v_pk_mul_f32 v[128:129], v[120:121], v[144:145] op_sel_hi:[1,0]
	v_pk_mul_f32 v[120:121], v[122:123], v[144:145] op_sel_hi:[1,0]
	v_pk_mul_f32 v[122:123], v[86:87], v[128:129]
	v_pk_mul_f32 v[128:129], v[116:117], v[144:145] op_sel_hi:[1,0]
	v_pk_mul_f32 v[116:117], v[118:119], v[144:145] op_sel_hi:[1,0]
	v_pk_mul_f32 v[120:121], v[88:89], v[120:121]
	v_pk_mul_f32 v[116:117], v[84:85], v[116:117]
	v_pk_mul_f32 v[118:119], v[82:83], v[128:129]
	v_cvt_pk_bf16_f32 v128, v122, v123
	v_cvt_pk_bf16_f32 v129, v120, v121
	v_cvt_pk_bf16_f32 v131, v116, v117
	s_nop 0
	v_cvt_pk_bf16_f32 v130, v118, v119
	ds_bpermute_b32 v238, v244, v128
	ds_bpermute_b32 v239, v244, v129
	ds_bpermute_b32 v240, v244, v130
	ds_bpermute_b32 v241, v244, v131
	ds_bpermute_b32 v242, v244, v146
	ds_bpermute_b32 v243, v244, v147
	s_waitcnt lgkmcnt(0)
	global_store_dwordx4 v[242:243], v[238:241], off offset:64
	ds_read_b32 v128, v197
	ds_read_b32 v129, v198
	s_waitcnt lgkmcnt(0)
	v_add_f32_e32 v128, v128, v129
	v_fmamk_f32 v128, v128, 0x3c000000, v185
	v_rsq_f32_e32 v130, v128
	ds_read2_b32 v[128:129], v213 offset0:32 offset1:48
	s_waitcnt lgkmcnt(0)
	v_mul_f32_e32 v128, v128, v130
	v_lshlrev_b64 v[130:131], 12, v[178:179]
	v_pk_mul_f32 v[110:111], v[110:111], v[128:129] op_sel_hi:[1,0]
	v_lshl_add_u64 v[130:131], s[46:47], 0, v[130:131]
	v_pk_mul_f32 v[112:113], v[112:113], v[128:129] op_sel_hi:[1,0]
	v_pk_mul_f32 v[144:145], v[90:91], v[110:111]
	v_lshl_add_u64 v[130:131], v[130:131], 0, v[114:115]
	v_pk_mul_f32 v[146:147], v[92:93], v[112:113]
	v_pk_mul_f32 v[158:159], v[106:107], v[128:129] op_sel_hi:[1,0]
	v_pk_mul_f32 v[106:107], v[108:109], v[128:129] op_sel_hi:[1,0]
	v_cvt_pk_bf16_f32 v144, v144, v145
	v_cvt_pk_bf16_f32 v145, v146, v147
	v_pk_mul_f32 v[108:109], v[94:95], v[158:159]
	v_pk_mul_f32 v[106:107], v[96:97], v[106:107]
	v_cvt_pk_bf16_f32 v146, v108, v109
	v_pk_fma_f32 v[110:111], v[90:91], v[110:111], v[214:215]
	v_cvt_pk_bf16_f32 v147, v106, v107
	ds_bpermute_b32 v232, v244, v144
	ds_bpermute_b32 v233, v244, v145
	ds_bpermute_b32 v234, v244, v146
	ds_bpermute_b32 v235, v244, v147
	ds_bpermute_b32 v236, v244, v130
	ds_bpermute_b32 v237, v244, v131
	s_waitcnt lgkmcnt(0)
	global_store_dwordx4 v[236:237], v[232:235], off
	v_pk_fma_f32 v[112:113], v[92:93], v[112:113], v[180:181]
	s_nop 0
	v_pk_mul_f32 v[144:145], v[102:103], v[128:129] op_sel_hi:[1,0]
	v_pk_mul_f32 v[102:103], v[104:105], v[128:129] op_sel_hi:[1,0]
	v_pk_mul_f32 v[104:105], v[86:87], v[144:145]
	v_pk_mul_f32 v[144:145], v[98:99], v[128:129] op_sel_hi:[1,0]
	v_pk_mul_f32 v[98:99], v[100:101], v[128:129] op_sel_hi:[1,0]
	v_pk_mul_f32 v[102:103], v[88:89], v[102:103]
	v_pk_mul_f32 v[98:99], v[84:85], v[98:99]
	v_pk_mul_f32 v[100:101], v[82:83], v[144:145]
	v_cvt_pk_bf16_f32 v144, v104, v105
	v_cvt_pk_bf16_f32 v145, v102, v103
	v_cvt_pk_bf16_f32 v147, v98, v99
	s_nop 0
	v_cvt_pk_bf16_f32 v146, v100, v101
	ds_bpermute_b32 v238, v244, v144
	ds_bpermute_b32 v239, v244, v145
	ds_bpermute_b32 v240, v244, v146
	ds_bpermute_b32 v241, v244, v147
	ds_bpermute_b32 v242, v244, v130
	ds_bpermute_b32 v243, v244, v131
	s_waitcnt lgkmcnt(0)
	global_store_dwordx4 v[242:243], v[238:241], off offset:64
	ds_read_b32 v128, v199
	ds_read_b32 v130, v200
	s_waitcnt lgkmcnt(0)
	v_add_f32_e32 v128, v128, v130
	v_fmamk_f32 v128, v128, 0x3c000000, v185
	v_rsq_f32_e32 v128, v128
	v_lshlrev_b64 v[130:131], 12, v[176:177]
	v_lshl_add_u64 v[130:131], s[46:47], 0, v[130:131]
	v_lshl_add_u64 v[130:131], v[130:131], 0, v[114:115]
	v_mul_f32_e32 v128, v129, v128
	v_pk_mul_f32 v[144:145], v[78:79], v[128:129] op_sel_hi:[1,0]
	v_pk_mul_f32 v[80:81], v[80:81], v[128:129] op_sel_hi:[1,0]
	v_pk_mul_f32 v[74:75], v[74:75], v[128:129] op_sel_hi:[1,0]
	v_pk_mul_f32 v[76:77], v[76:77], v[128:129] op_sel_hi:[1,0]
	v_pk_mul_f32 v[146:147], v[92:93], v[80:81]
	v_pk_mul_f32 v[158:159], v[90:91], v[144:145]
	v_pk_mul_f32 v[76:77], v[96:97], v[76:77]
	v_pk_mul_f32 v[78:79], v[94:95], v[74:75]
	v_pk_fma_f32 v[160:161], v[92:93], v[80:81], v[112:113]
	v_pk_fma_f32 v[80:81], v[90:91], v[144:145], v[110:111]
	v_cvt_pk_bf16_f32 v110, v158, v159
	v_cvt_pk_bf16_f32 v111, v146, v147
	v_cvt_pk_bf16_f32 v112, v78, v79
	v_cvt_pk_bf16_f32 v113, v76, v77
	v_pk_mul_f32 v[70:71], v[70:71], v[128:129] op_sel_hi:[1,0]
	v_pk_mul_f32 v[72:73], v[72:73], v[128:129] op_sel_hi:[1,0]
	v_pk_mul_f32 v[66:67], v[66:67], v[128:129] op_sel_hi:[1,0]
	v_pk_mul_f32 v[68:69], v[68:69], v[128:129] op_sel_hi:[1,0]
	ds_bpermute_b32 v232, v244, v110
	ds_bpermute_b32 v233, v244, v111
	ds_bpermute_b32 v234, v244, v112
	ds_bpermute_b32 v235, v244, v113
	ds_bpermute_b32 v236, v244, v130
	ds_bpermute_b32 v237, v244, v131
	s_waitcnt lgkmcnt(0)
	global_store_dwordx4 v[236:237], v[232:235], off
	v_pk_mul_f32 v[72:73], v[88:89], v[72:73]
	v_pk_mul_f32 v[74:75], v[86:87], v[70:71]
	v_pk_mul_f32 v[68:69], v[84:85], v[68:69]
	v_pk_mul_f32 v[70:71], v[82:83], v[66:67]
	v_cvt_pk_bf16_f32 v110, v74, v75
	v_cvt_pk_bf16_f32 v111, v72, v73
	v_cvt_pk_bf16_f32 v113, v68, v69
	v_lshl_add_u64 v[66:67], v[166:167], 0, s[14:15]
	v_cvt_pk_bf16_f32 v112, v70, v71
	ds_bpermute_b32 v238, v244, v110
	ds_bpermute_b32 v239, v244, v111
	ds_bpermute_b32 v240, v244, v112
	ds_bpermute_b32 v241, v244, v113
	ds_bpermute_b32 v242, v244, v130
	ds_bpermute_b32 v243, v244, v131
	s_waitcnt lgkmcnt(0)
	global_store_dwordx4 v[242:243], v[238:241], off offset:64
	ds_swizzle_b32 v110, v80 offset:swizzle(SWAP,1)
	ds_swizzle_b32 v111, v81 offset:swizzle(SWAP,1)
	ds_swizzle_b32 v112, v160 offset:swizzle(SWAP,1)
	ds_swizzle_b32 v113, v161 offset:swizzle(SWAP,1)
	s_waitcnt lgkmcnt(2)
	v_pk_add_f32 v[80:81], v[80:81], v[110:111]
	ds_swizzle_b32 v110, v80 offset:swizzle(SWAP,2)
	s_waitcnt lgkmcnt(1)
	v_pk_add_f32 v[112:113], v[160:161], v[112:113]
	ds_swizzle_b32 v111, v81 offset:swizzle(SWAP,2)
	ds_swizzle_b32 v128, v112 offset:swizzle(SWAP,2)
	ds_swizzle_b32 v129, v113 offset:swizzle(SWAP,2)
	s_waitcnt lgkmcnt(2)
	v_pk_add_f32 v[80:81], v[80:81], v[110:111]
	ds_swizzle_b32 v110, v80 offset:swizzle(SWAP,4)
	s_waitcnt lgkmcnt(1)
	v_pk_add_f32 v[112:113], v[112:113], v[128:129]
	ds_swizzle_b32 v111, v81 offset:swizzle(SWAP,4)
	ds_swizzle_b32 v128, v112 offset:swizzle(SWAP,4)
	ds_swizzle_b32 v129, v113 offset:swizzle(SWAP,4)
	s_waitcnt lgkmcnt(2)
	v_pk_add_f32 v[80:81], v[80:81], v[110:111]
	ds_swizzle_b32 v110, v80 offset:swizzle(SWAP,8)
	s_waitcnt lgkmcnt(1)
	v_pk_add_f32 v[112:113], v[112:113], v[128:129]
	ds_swizzle_b32 v111, v81 offset:swizzle(SWAP,8)
	ds_swizzle_b32 v128, v112 offset:swizzle(SWAP,8)
	ds_swizzle_b32 v129, v113 offset:swizzle(SWAP,8)
	s_and_saveexec_b64 s[60:61], s[40:41]
	s_cbranch_execz .LBB0_196
	s_waitcnt lgkmcnt(0)
	v_pk_add_f32 v[112:113], v[112:113], v[128:129]
	v_pk_add_f32 v[110:111], v[80:81], v[110:111]
	global_store_dwordx4 v[66:67], v[110:113], off

.LBB0_202:
	s_or_b64 exec, exec, s[60:61]
	ds_read_b32 v66, v201
	ds_read_b32 v67, v202
	ds_read2_b32 v[68:69], v213 offset0:128 offset1:144
	s_mov_b64 s[14:15], 0x80000
	s_waitcnt lgkmcnt(1)
	v_add_f32_e32 v66, v66, v67
	v_fmamk_f32 v66, v66, 0x3c000000, v185
	v_rsq_f32_e32 v66, v66
	s_waitcnt lgkmcnt(0)
	v_mul_f32_e32 v68, v68, v66
	v_lshlrev_b64 v[66:67], 12, v[174:175]
	v_lshl_add_u64 v[66:67], s[46:47], 0, v[66:67]
	v_lshl_add_u64 v[66:67], v[66:67], 0, v[114:115]
	v_pk_mul_f32 v[64:65], v[64:65], v[68:69] op_sel_hi:[1,0]
	v_lshl_add_u64 v[70:71], v[66:67], 0, s[14:15]
	v_pk_mul_f32 v[62:63], v[62:63], v[68:69] op_sel_hi:[1,0]
	v_pk_mul_f32 v[72:73], v[92:93], v[64:65]
	v_pk_mul_f32 v[76:77], v[58:59], v[68:69] op_sel_hi:[1,0]
	s_mov_b32 s14, 0x80000
	v_pk_mul_f32 v[74:75], v[90:91], v[62:63]
	v_pk_mul_f32 v[58:59], v[60:61], v[68:69] op_sel_hi:[1,0]
	v_pk_mul_f32 v[60:61], v[94:95], v[76:77]
	v_pk_fma_f32 v[76:77], v[90:91], v[62:63], 0 op_sel_hi:[1,1,0]
	v_cvt_pk_bf16_f32 v63, v72, v73
	v_add_co_u32_e32 v72, vcc, s14, v66
	v_cvt_pk_bf16_f32 v62, v74, v75
	v_pk_mul_f32 v[58:59], v[96:97], v[58:59]
	s_nop 0
	v_addc_co_u32_e32 v73, vcc, 0, v67, vcc
	v_pk_fma_f32 v[78:79], v[92:93], v[64:65], 0 op_sel_hi:[1,1,0]
	v_cvt_pk_bf16_f32 v64, v60, v61
	v_cvt_pk_bf16_f32 v65, v58, v59
	ds_bpermute_b32 v232, v244, v62
	ds_bpermute_b32 v233, v244, v63
	ds_bpermute_b32 v234, v244, v64
	ds_bpermute_b32 v235, v244, v65
	ds_bpermute_b32 v236, v244, v72
	ds_bpermute_b32 v237, v244, v73
	s_waitcnt lgkmcnt(0)
	global_store_dwordx4 v[236:237], v[232:235], off
	s_mov_b64 s[14:15], 0x90000
	s_nop 0
	v_pk_mul_f32 v[62:63], v[54:55], v[68:69] op_sel_hi:[1,0]
	v_pk_mul_f32 v[54:55], v[56:57], v[68:69] op_sel_hi:[1,0]
	v_pk_mul_f32 v[56:57], v[86:87], v[62:63]
	v_pk_mul_f32 v[62:63], v[50:51], v[68:69] op_sel_hi:[1,0]
	v_pk_mul_f32 v[50:51], v[52:53], v[68:69] op_sel_hi:[1,0]
	v_pk_mul_f32 v[54:55], v[88:89], v[54:55]
	v_pk_mul_f32 v[50:51], v[84:85], v[50:51]
	v_pk_mul_f32 v[52:53], v[82:83], v[62:63]
	v_cvt_pk_bf16_f32 v62, v56, v57
	v_cvt_pk_bf16_f32 v63, v54, v55
	v_cvt_pk_bf16_f32 v65, v50, v51
	s_nop 0
	v_cvt_pk_bf16_f32 v64, v52, v53
	ds_bpermute_b32 v238, v244, v62
	ds_bpermute_b32 v239, v244, v63
	ds_bpermute_b32 v240, v244, v64
	ds_bpermute_b32 v241, v244, v65
	ds_bpermute_b32 v242, v244, v70
	ds_bpermute_b32 v243, v244, v71
	s_waitcnt lgkmcnt(0)
	global_store_dwordx4 v[242:243], v[238:241], off offset:64
	ds_read_b32 v62, v203
	ds_read_b32 v63, v204
	v_lshl_add_u64 v[64:65], v[66:67], 0, s[14:15]
	s_mov_b32 s14, 0x90000
	s_waitcnt lgkmcnt(0)
	v_add_f32_e32 v62, v62, v63
	v_fmamk_f32 v62, v62, 0x3c000000, v185
	v_rsq_f32_e32 v62, v62
	s_nop 0
	v_mul_f32_e32 v62, v69, v62
	v_pk_mul_f32 v[48:49], v[48:49], v[62:63] op_sel_hi:[1,0]
	v_pk_mul_f32 v[46:47], v[46:47], v[62:63] op_sel_hi:[1,0]
	v_pk_mul_f32 v[68:69], v[92:93], v[48:49]
	v_pk_mul_f32 v[70:71], v[90:91], v[46:47]
	v_pk_fma_f32 v[74:75], v[90:91], v[46:47], v[76:77]
	v_cvt_pk_bf16_f32 v47, v68, v69
	v_add_co_u32_e32 v68, vcc, s14, v66
	v_pk_mul_f32 v[72:73], v[42:43], v[62:63] op_sel_hi:[1,0]
	v_pk_mul_f32 v[42:43], v[44:45], v[62:63] op_sel_hi:[1,0]
	v_cvt_pk_bf16_f32 v46, v70, v71
	v_addc_co_u32_e32 v69, vcc, 0, v67, vcc
	v_pk_mul_f32 v[42:43], v[96:97], v[42:43]
	v_pk_mul_f32 v[44:45], v[94:95], v[72:73]
	v_pk_fma_f32 v[72:73], v[92:93], v[48:49], v[78:79]
	v_cvt_pk_bf16_f32 v48, v44, v45
	v_cvt_pk_bf16_f32 v49, v42, v43
	ds_bpermute_b32 v232, v244, v46
	ds_bpermute_b32 v233, v244, v47
	ds_bpermute_b32 v234, v244, v48
	ds_bpermute_b32 v235, v244, v49
	ds_bpermute_b32 v236, v244, v68
	ds_bpermute_b32 v237, v244, v69
	s_waitcnt lgkmcnt(0)
	global_store_dwordx4 v[236:237], v[232:235], off
	s_mov_b64 s[14:15], 0xa0000
	s_nop 0
	v_pk_mul_f32 v[46:47], v[38:39], v[62:63] op_sel_hi:[1,0]
	v_pk_mul_f32 v[38:39], v[40:41], v[62:63] op_sel_hi:[1,0]
	v_pk_mul_f32 v[40:41], v[86:87], v[46:47]
	v_pk_mul_f32 v[46:47], v[34:35], v[62:63] op_sel_hi:[1,0]
	v_pk_mul_f32 v[34:35], v[36:37], v[62:63] op_sel_hi:[1,0]
	v_pk_mul_f32 v[38:39], v[88:89], v[38:39]
	v_pk_mul_f32 v[34:35], v[84:85], v[34:35]
	v_pk_mul_f32 v[36:37], v[82:83], v[46:47]
	v_cvt_pk_bf16_f32 v46, v40, v41
	v_cvt_pk_bf16_f32 v47, v38, v39
	v_cvt_pk_bf16_f32 v49, v34, v35
	s_nop 0
	v_cvt_pk_bf16_f32 v48, v36, v37
	ds_bpermute_b32 v238, v244, v46
	ds_bpermute_b32 v239, v244, v47
	ds_bpermute_b32 v240, v244, v48
	ds_bpermute_b32 v241, v244, v49
	ds_bpermute_b32 v242, v244, v64
	ds_bpermute_b32 v243, v244, v65
	s_waitcnt lgkmcnt(0)
	global_store_dwordx4 v[242:243], v[238:241], off offset:64
	ds_read_b32 v46, v205
	ds_read_b32 v47, v206
	s_waitcnt lgkmcnt(0)
	v_add_f32_e32 v46, v46, v47
	v_fmamk_f32 v46, v46, 0x3c000000, v185
	v_rsq_f32_e32 v48, v46
	ds_read2_b32 v[46:47], v213 offset0:160 offset1:176
	s_waitcnt lgkmcnt(0)
	v_mul_f32_e32 v46, v46, v48
	v_lshl_add_u64 v[48:49], v[66:67], 0, s[14:15]
	v_pk_mul_f32 v[30:31], v[30:31], v[46:47] op_sel_hi:[1,0]
	v_pk_mul_f32 v[68:69], v[26:27], v[46:47] op_sel_hi:[1,0]
	s_mov_b32 s14, 0xa0000
	v_pk_mul_f32 v[32:33], v[32:33], v[46:47] op_sel_hi:[1,0]
	v_pk_mul_f32 v[62:63], v[90:91], v[30:31]
	v_pk_mul_f32 v[26:27], v[28:29], v[46:47] op_sel_hi:[1,0]
	v_pk_mul_f32 v[28:29], v[94:95], v[68:69]
	v_add_co_u32_e32 v68, vcc, s14, v66
	v_pk_mul_f32 v[64:65], v[92:93], v[32:33]
	v_cvt_pk_bf16_f32 v62, v62, v63
	s_nop 0
	v_addc_co_u32_e32 v69, vcc, 0, v67, vcc
	v_cvt_pk_bf16_f32 v63, v64, v65
	v_pk_mul_f32 v[26:27], v[96:97], v[26:27]
	v_cvt_pk_bf16_f32 v64, v28, v29
	s_mov_b64 s[14:15], 0xb0000
	v_cvt_pk_bf16_f32 v65, v26, v27
	ds_bpermute_b32 v232, v244, v62
	ds_bpermute_b32 v233, v244, v63
	ds_bpermute_b32 v234, v244, v64
	ds_bpermute_b32 v235, v244, v65
	ds_bpermute_b32 v236, v244, v68
	ds_bpermute_b32 v237, v244, v69
	s_waitcnt lgkmcnt(0)
	global_store_dwordx4 v[236:237], v[232:235], off
	v_pk_fma_f32 v[30:31], v[90:91], v[30:31], v[74:75]
	v_pk_fma_f32 v[32:33], v[92:93], v[32:33], v[72:73]
	v_pk_mul_f32 v[62:63], v[22:23], v[46:47] op_sel_hi:[1,0]
	v_pk_mul_f32 v[22:23], v[24:25], v[46:47] op_sel_hi:[1,0]
	v_pk_mul_f32 v[24:25], v[86:87], v[62:63]
	v_pk_mul_f32 v[62:63], v[18:19], v[46:47] op_sel_hi:[1,0]
	v_pk_mul_f32 v[18:19], v[20:21], v[46:47] op_sel_hi:[1,0]
	v_pk_mul_f32 v[22:23], v[88:89], v[22:23]
	v_pk_mul_f32 v[18:19], v[84:85], v[18:19]
	v_pk_mul_f32 v[20:21], v[82:83], v[62:63]
	v_cvt_pk_bf16_f32 v62, v24, v25
	v_cvt_pk_bf16_f32 v63, v22, v23
	v_cvt_pk_bf16_f32 v65, v18, v19
	s_nop 0
	v_cvt_pk_bf16_f32 v64, v20, v21
	ds_bpermute_b32 v238, v244, v62
	ds_bpermute_b32 v239, v244, v63
	ds_bpermute_b32 v240, v244, v64
	ds_bpermute_b32 v241, v244, v65
	ds_bpermute_b32 v242, v244, v48
	ds_bpermute_b32 v243, v244, v49
	s_waitcnt lgkmcnt(0)
	global_store_dwordx4 v[242:243], v[238:241], off offset:64
	ds_read_b32 v46, v207
	ds_read_b32 v48, v208
	s_waitcnt lgkmcnt(0)
	v_add_f32_e32 v46, v46, v48
	v_fmamk_f32 v46, v46, 0x3c000000, v185
	v_rsq_f32_e32 v46, v46
	v_lshl_add_u64 v[48:49], v[66:67], 0, s[14:15]
	s_mov_b32 s14, 0xb0000
	v_mul_f32_e32 v46, v47, v46
	v_pk_mul_f32 v[10:11], v[10:11], v[46:47] op_sel_hi:[1,0]
	v_pk_mul_f32 v[62:63], v[14:15], v[46:47] op_sel_hi:[1,0]
	v_pk_mul_f32 v[16:17], v[16:17], v[46:47] op_sel_hi:[1,0]
	v_pk_mul_f32 v[12:13], v[12:13], v[46:47] op_sel_hi:[1,0]
	v_pk_mul_f32 v[14:15], v[94:95], v[10:11]
	v_add_co_u32_e32 v10, vcc, s14, v66
	v_pk_mul_f32 v[64:65], v[92:93], v[16:17]
	v_pk_mul_f32 v[68:69], v[90:91], v[62:63]
	v_pk_mul_f32 v[12:13], v[96:97], v[12:13]
	v_pk_fma_f32 v[70:71], v[92:93], v[16:17], v[32:33]
	v_pk_fma_f32 v[16:17], v[90:91], v[62:63], v[30:31]
	v_cvt_pk_bf16_f32 v30, v68, v69
	v_cvt_pk_bf16_f32 v31, v64, v65
	v_cvt_pk_bf16_f32 v32, v14, v15
	v_cvt_pk_bf16_f32 v33, v12, v13
	v_addc_co_u32_e32 v11, vcc, 0, v67, vcc
	v_pk_mul_f32 v[6:7], v[6:7], v[46:47] op_sel_hi:[1,0]
	v_pk_mul_f32 v[8:9], v[8:9], v[46:47] op_sel_hi:[1,0]
	v_pk_mul_f32 v[2:3], v[2:3], v[46:47] op_sel_hi:[1,0]
	v_pk_mul_f32 v[4:5], v[4:5], v[46:47] op_sel_hi:[1,0]
	ds_bpermute_b32 v232, v244, v30
	ds_bpermute_b32 v233, v244, v31
	ds_bpermute_b32 v234, v244, v32
	ds_bpermute_b32 v235, v244, v33
	ds_bpermute_b32 v236, v244, v10
	ds_bpermute_b32 v237, v244, v11
	s_waitcnt lgkmcnt(0)
	global_store_dwordx4 v[236:237], v[232:235], off
	v_pk_mul_f32 v[8:9], v[88:89], v[8:9]
	v_pk_mul_f32 v[10:11], v[86:87], v[6:7]
	v_pk_mul_f32 v[4:5], v[84:85], v[4:5]
	v_pk_mul_f32 v[6:7], v[82:83], v[2:3]
	v_cvt_pk_bf16_f32 v30, v10, v11
	v_cvt_pk_bf16_f32 v31, v8, v9
	v_cvt_pk_bf16_f32 v33, v4, v5
	s_add_i32 s14, s28, 2
	v_cvt_pk_bf16_f32 v32, v6, v7
	ds_bpermute_b32 v238, v244, v30
	ds_bpermute_b32 v239, v244, v31
	ds_bpermute_b32 v240, v244, v32
	ds_bpermute_b32 v241, v244, v33
	ds_bpermute_b32 v242, v244, v48
	ds_bpermute_b32 v243, v244, v49
	s_waitcnt lgkmcnt(0)
	global_store_dwordx4 v[242:243], v[238:241], off offset:64
	ds_swizzle_b32 v30, v16 offset:swizzle(SWAP,1)
	ds_swizzle_b32 v31, v17 offset:swizzle(SWAP,1)
	ds_swizzle_b32 v32, v70 offset:swizzle(SWAP,1)
	ds_swizzle_b32 v33, v71 offset:swizzle(SWAP,1)
	s_ashr_i32 s15, s14, 31
	s_lshl_b64 s[14:15], s[14:15], 9
	s_waitcnt lgkmcnt(2)
	v_pk_add_f32 v[16:17], v[16:17], v[30:31]
	ds_swizzle_b32 v30, v16 offset:swizzle(SWAP,2)
	s_waitcnt lgkmcnt(1)
	v_pk_add_f32 v[32:33], v[70:71], v[32:33]
	ds_swizzle_b32 v31, v17 offset:swizzle(SWAP,2)
	ds_swizzle_b32 v46, v32 offset:swizzle(SWAP,2)
	ds_swizzle_b32 v47, v33 offset:swizzle(SWAP,2)
	v_lshl_add_u64 v[2:3], v[166:167], 0, s[14:15]
	s_waitcnt lgkmcnt(2)
	v_pk_add_f32 v[16:17], v[16:17], v[30:31]
	ds_swizzle_b32 v30, v16 offset:swizzle(SWAP,4)
	s_waitcnt lgkmcnt(1)
	v_pk_add_f32 v[32:33], v[32:33], v[46:47]
	ds_swizzle_b32 v31, v17 offset:swizzle(SWAP,4)
	ds_swizzle_b32 v46, v32 offset:swizzle(SWAP,4)
	ds_swizzle_b32 v47, v33 offset:swizzle(SWAP,4)
	s_waitcnt lgkmcnt(2)
	v_pk_add_f32 v[16:17], v[16:17], v[30:31]
	ds_swizzle_b32 v30, v16 offset:swizzle(SWAP,8)
	s_waitcnt lgkmcnt(1)
	v_pk_add_f32 v[32:33], v[32:33], v[46:47]
	ds_swizzle_b32 v31, v17 offset:swizzle(SWAP,8)
	ds_swizzle_b32 v46, v32 offset:swizzle(SWAP,8)
	ds_swizzle_b32 v47, v33 offset:swizzle(SWAP,8)
	s_and_saveexec_b64 s[28:29], s[40:41]
	s_cbranch_execz .LBB0_204
	s_waitcnt lgkmcnt(0)
	v_pk_add_f32 v[32:33], v[32:33], v[46:47]
	v_pk_add_f32 v[30:31], v[16:17], v[30:31]
	global_store_dwordx4 v[2:3], v[30:33], off

.LBB0_349:
	v_mbcnt_lo_u32_b32 v244, -1, 0
	v_mbcnt_hi_u32_b32 v244, -1, v244
	v_lshrrev_b32_e32 v245, 2, v244
	v_and_b32_e32 v244, 3, v244
	v_lshl_add_u32 v244, v244, 4, v245
	v_lshlrev_b32_e32 v244, 2, v244
	s_lshl_b32 s14, s14, 10
	v_add_u32_e32 v176, s14, v174
	ds_read_b32 v154, v176
	s_lshl_b32 s15, s28, 8
	s_ashr_i32 s58, s28, 3
	s_and_b32 s14, s15, 0x700
	v_readlane_b32 s70, v255, 13
	v_readlane_b32 s74, v255, 15
	v_lshl_add_u32 v152, s40, 8, v1
	v_or_b32_e32 v177, s14, v173
	s_cmp_lg_u32 s58, 1
	s_mov_b64 s[40:41], -1
	v_readlane_b32 s71, v255, 14
	v_readlane_b32 s75, v255, 16
	s_cbranch_scc0 .LBB0_384
	s_cmp_lt_u32 s28, 8
	s_cselect_b64 s[56:57], -1, 0
	s_cmp_gt_u32 s28, 7
	s_waitcnt lgkmcnt(0)
	v_pk_mul_f32 v[134:135], v[130:131], v[154:155] op_sel_hi:[1,0]
	v_pk_mul_f32 v[166:167], v[128:129], v[154:155] op_sel_hi:[1,0]
	v_pk_mul_f32 v[138:139], v[126:127], v[154:155] op_sel_hi:[1,0]
	v_pk_mul_f32 v[168:169], v[124:125], v[154:155] op_sel_hi:[1,0]
	s_cbranch_scc1 .LBB0_352
	v_max_f32_e32 v114, v166, v166
	v_max_f32_e32 v132, 0xc2a00000, v114
	v_max_f32_e32 v114, v168, v168
	v_max_f32_e32 v136, 0xc2a00000, v114
	v_mul_f32_e32 v114, 0xbfb8aa3b, v132
	v_exp_f32_e32 v114, v114
	v_mul_f32_e32 v133, 0xbfb8aa3b, v136
	v_exp_f32_e32 v133, v133
	v_max_f32_e32 v137, v169, v169
	v_add_f32_e32 v114, 1.0, v114
	v_rcp_f32_e32 v158, v114
	v_add_f32_e32 v114, 1.0, v133
	v_max_f32_e32 v133, v167, v167
	v_max_f32_e32 v133, 0xc2a00000, v133
	v_max_f32_e32 v137, 0xc2a00000, v137
	v_mul_f32_e32 v153, 0xbfb8aa3b, v133
	v_exp_f32_e32 v153, v153
	v_mul_f32_e32 v155, 0xbfb8aa3b, v137
	v_exp_f32_e32 v155, v155
	v_max_f32_e32 v134, v134, v134
	v_max_f32_e32 v134, 0xc2a00000, v134
	v_max_f32_e32 v138, v138, v138
	v_rcp_f32_e32 v160, v114
	v_add_f32_e32 v114, 1.0, v153
	v_max_f32_e32 v138, 0xc2a00000, v138
	v_mul_f32_e32 v153, 0xbfb8aa3b, v134
	v_rcp_f32_e32 v159, v114
	v_add_f32_e32 v114, 1.0, v155
	v_exp_f32_e32 v153, v153
	v_mul_f32_e32 v155, 0xbfb8aa3b, v138
	v_exp_f32_e32 v155, v155
	v_max_f32_e32 v135, v135, v135
	v_max_f32_e32 v135, 0xc2a00000, v135
	v_max_f32_e32 v139, v139, v139
	v_rcp_f32_e32 v161, v114
	v_add_f32_e32 v114, 1.0, v153
	v_max_f32_e32 v139, 0xc2a00000, v139
	v_mul_f32_e32 v153, 0xbfb8aa3b, v135
	v_rcp_f32_e32 v168, v114
	v_add_f32_e32 v114, 1.0, v155
	v_exp_f32_e32 v153, v153
	v_mul_f32_e32 v155, 0xbfb8aa3b, v139
	v_exp_f32_e32 v155, v155
	v_rcp_f32_e32 v170, v114
	v_add_f32_e32 v114, 1.0, v153
	v_rcp_f32_e32 v169, v114
	v_add_f32_e32 v114, 1.0, v155
	v_rcp_f32_e32 v171, v114
	v_pk_mul_f32 v[166:167], v[132:133], v[158:159]
	v_pk_mul_f32 v[134:135], v[134:135], v[168:169]
	v_pk_mul_f32 v[168:169], v[136:137], v[160:161]
	v_pk_mul_f32 v[138:139], v[138:139], v[170:171]
.LBB0_352:
	s_ashr_i32 s59, s58, 31
	s_lshl_b64 s[14:15], s[58:59], 25
	s_add_u32 s14, s37, s14
	s_addc_u32 s15, s64, s15
	v_lshlrev_b32_e32 v114, 1, v177
	v_ashrrev_i32_e32 v153, 31, v152
	v_lshl_add_u64 v[132:133], s[14:15], 0, v[114:115]
	v_lshlrev_b64 v[136:137], 12, v[152:153]
	v_mov_b32_e32 v155, v154
	v_lshl_add_u64 v[136:137], v[132:133], 0, v[136:137]
	v_cvt_pk_bf16_f32 v166, v166, v167
	v_cvt_pk_bf16_f32 v167, v134, v135
	v_cvt_pk_bf16_f32 v168, v168, v169
	v_cvt_pk_bf16_f32 v169, v138, v139
	v_mov_b32_e32 v158, v154
	v_mov_b32_e32 v159, v154
	v_cndmask_b32_e64 v114, 0, 1, s[56:57]
	ds_bpermute_b32 v232, v244, v166
	ds_bpermute_b32 v233, v244, v167
	ds_bpermute_b32 v234, v244, v168
	ds_bpermute_b32 v235, v244, v169
	ds_bpermute_b32 v236, v244, v136
	ds_bpermute_b32 v237, v244, v137
	s_waitcnt lgkmcnt(0)
	global_store_dwordx4 v[236:237], v[232:235], off
	v_pk_mul_f32 v[138:139], v[122:123], v[158:159]
	v_pk_mul_f32 v[134:135], v[120:121], v[154:155]
	v_pk_mul_f32 v[166:167], v[118:119], v[158:159]
	v_cmp_ne_u32_e64 s[40:41], 1, v114
	s_andn2_b64 vcc, exec, s[56:57]
	v_pk_mul_f32 v[168:169], v[116:117], v[154:155]
	s_cbranch_vccnz .LBB0_354
	v_max_f32_e32 v114, v134, v134
	v_max_f32_e32 v134, 0xc2a00000, v114
	v_max_f32_e32 v114, v168, v168
	v_max_f32_e32 v158, 0xc2a00000, v114
	v_mul_f32_e32 v114, 0xbfb8aa3b, v134
	v_exp_f32_e32 v114, v114
	v_mul_f32_e32 v155, 0xbfb8aa3b, v158
	v_exp_f32_e32 v155, v155
	v_max_f32_e32 v135, v135, v135
	v_add_f32_e32 v114, 1.0, v114
	v_rcp_f32_e32 v160, v114
	v_add_f32_e32 v114, 1.0, v155
	v_max_f32_e32 v135, 0xc2a00000, v135
	v_max_f32_e32 v155, v169, v169
	v_max_f32_e32 v159, 0xc2a00000, v155
	v_mul_f32_e32 v155, 0xbfb8aa3b, v135
	v_exp_f32_e32 v155, v155
	v_mul_f32_e32 v161, 0xbfb8aa3b, v159
	v_exp_f32_e32 v169, v161
	v_max_f32_e32 v138, v138, v138
	v_rcp_f32_e32 v168, v114
	v_add_f32_e32 v114, 1.0, v155
	v_max_f32_e32 v138, 0xc2a00000, v138
	v_max_f32_e32 v155, v166, v166
	v_max_f32_e32 v166, 0xc2a00000, v155
	v_mul_f32_e32 v155, 0xbfb8aa3b, v138
	v_exp_f32_e32 v155, v155
	v_rcp_f32_e32 v161, v114
	v_add_f32_e32 v114, 1.0, v169
	v_mul_f32_e32 v169, 0xbfb8aa3b, v166
	v_exp_f32_e32 v171, v169
	v_max_f32_e32 v139, v139, v139
	v_rcp_f32_e32 v169, v114
	v_add_f32_e32 v114, 1.0, v155
	v_max_f32_e32 v139, 0xc2a00000, v139
	v_max_f32_e32 v155, v167, v167
	v_max_f32_e32 v167, 0xc2a00000, v155
	v_mul_f32_e32 v155, 0xbfb8aa3b, v139
	v_rcp_f32_e32 v170, v114
	v_add_f32_e32 v114, 1.0, v171
	v_exp_f32_e32 v155, v155
	v_mul_f32_e32 v171, 0xbfb8aa3b, v167
	v_exp_f32_e32 v179, v171
	v_rcp_f32_e32 v178, v114
	v_add_f32_e32 v114, 1.0, v155
	v_rcp_f32_e32 v171, v114
	v_add_f32_e32 v114, 1.0, v179
	v_rcp_f32_e32 v179, v114
	v_pk_mul_f32 v[134:135], v[134:135], v[160:161]
	v_pk_mul_f32 v[138:139], v[138:139], v[170:171]
	v_pk_mul_f32 v[168:169], v[158:159], v[168:169]
	v_pk_mul_f32 v[166:167], v[166:167], v[178:179]
.LBB0_354:
	v_cvt_pk_bf16_f32 v178, v134, v135
	ds_read_b32 v134, v176 offset:64
	v_cvt_pk_bf16_f32 v179, v138, v139
	v_cvt_pk_bf16_f32 v180, v168, v169
	v_cvt_pk_bf16_f32 v181, v166, v167
	s_and_b64 vcc, exec, s[40:41]
	s_waitcnt lgkmcnt(0)
	v_pk_mul_f32 v[138:139], v[112:113], v[134:135] op_sel_hi:[1,0]
	v_pk_mul_f32 v[168:169], v[110:111], v[134:135] op_sel_hi:[1,0]
	v_pk_mul_f32 v[166:167], v[108:109], v[134:135] op_sel_hi:[1,0]
	v_pk_mul_f32 v[170:171], v[106:107], v[134:135] op_sel_hi:[1,0]
	ds_bpermute_b32 v238, v244, v178
	ds_bpermute_b32 v239, v244, v179
	ds_bpermute_b32 v240, v244, v180
	ds_bpermute_b32 v241, v244, v181
	ds_bpermute_b32 v242, v244, v136
	ds_bpermute_b32 v243, v244, v137
	s_waitcnt lgkmcnt(0)
	global_store_dwordx4 v[242:243], v[238:241], off offset:64
	s_cbranch_vccnz .LBB0_356
	v_max_f32_e32 v114, v168, v168
	v_max_f32_e32 v136, 0xc2a00000, v114
	v_max_f32_e32 v114, v170, v170
	v_max_f32_e32 v158, 0xc2a00000, v114
	v_mul_f32_e32 v114, 0xbfb8aa3b, v136
	v_exp_f32_e32 v114, v114
	v_mul_f32_e32 v135, 0xbfb8aa3b, v158
	v_exp_f32_e32 v135, v135
	v_add_f32_e32 v114, 1.0, v114
	v_rcp_f32_e32 v160, v114
	v_add_f32_e32 v114, 1.0, v135
	v_max_f32_e32 v135, v169, v169
	v_max_f32_e32 v137, 0xc2a00000, v135
	v_max_f32_e32 v135, v171, v171
	v_max_f32_e32 v159, 0xc2a00000, v135
	v_mul_f32_e32 v135, 0xbfb8aa3b, v137
	v_exp_f32_e32 v135, v135
	v_mul_f32_e32 v155, 0xbfb8aa3b, v159
	v_rcp_f32_e32 v170, v114
	v_exp_f32_e32 v155, v155
	v_add_f32_e32 v114, 1.0, v135
	v_max_f32_e32 v135, v138, v138
	v_max_f32_e32 v138, 0xc2a00000, v135
	v_max_f32_e32 v135, v166, v166
	v_max_f32_e32 v166, 0xc2a00000, v135
	v_mul_f32_e32 v135, 0xbfb8aa3b, v138
	v_exp_f32_e32 v135, v135
	v_rcp_f32_e32 v161, v114
	v_add_f32_e32 v114, 1.0, v155
	v_mul_f32_e32 v155, 0xbfb8aa3b, v166
	v_exp_f32_e32 v155, v155
	v_rcp_f32_e32 v171, v114
	v_add_f32_e32 v114, 1.0, v135
	v_max_f32_e32 v135, v139, v139
	v_max_f32_e32 v139, 0xc2a00000, v135
	v_max_f32_e32 v135, v167, v167
	v_max_f32_e32 v167, 0xc2a00000, v135
	v_mul_f32_e32 v135, 0xbfb8aa3b, v139
	v_rcp_f32_e32 v178, v114
	v_add_f32_e32 v114, 1.0, v155
	v_exp_f32_e32 v135, v135
	v_mul_f32_e32 v155, 0xbfb8aa3b, v167
	v_exp_f32_e32 v155, v155
	v_rcp_f32_e32 v180, v114
	v_add_f32_e32 v114, 1.0, v135
	v_rcp_f32_e32 v179, v114
	v_add_f32_e32 v114, 1.0, v155
	v_rcp_f32_e32 v181, v114
	v_pk_mul_f32 v[168:169], v[136:137], v[160:161]
	v_pk_mul_f32 v[138:139], v[138:139], v[178:179]
	v_pk_mul_f32 v[170:171], v[158:159], v[170:171]
	v_pk_mul_f32 v[166:167], v[166:167], v[180:181]
.LBB0_356:
	v_or_b32_e32 v136, 16, v152
	v_ashrrev_i32_e32 v137, 31, v136
	v_lshlrev_b64 v[136:137], 12, v[136:137]
	v_mov_b32_e32 v135, v134
	v_lshl_add_u64 v[136:137], v[132:133], 0, v[136:137]
	v_cvt_pk_bf16_f32 v168, v168, v169
	v_cvt_pk_bf16_f32 v169, v138, v139
	v_cvt_pk_bf16_f32 v170, v170, v171
	v_cvt_pk_bf16_f32 v171, v166, v167
	v_mov_b32_e32 v158, v134
	v_mov_b32_e32 v159, v134
	ds_bpermute_b32 v232, v244, v168
	ds_bpermute_b32 v233, v244, v169
	ds_bpermute_b32 v234, v244, v170
	ds_bpermute_b32 v235, v244, v171
	ds_bpermute_b32 v236, v244, v136
	ds_bpermute_b32 v237, v244, v137
	s_waitcnt lgkmcnt(0)
	global_store_dwordx4 v[236:237], v[232:235], off
	v_pk_mul_f32 v[138:139], v[104:105], v[158:159]
	v_pk_mul_f32 v[166:167], v[100:101], v[158:159]
	v_pk_mul_f32 v[168:169], v[102:103], v[134:135]
	s_and_b64 vcc, exec, s[40:41]
	v_pk_mul_f32 v[170:171], v[98:99], v[134:135]
	s_cbranch_vccnz .LBB0_358
	v_max_f32_e32 v114, v168, v168
	v_max_f32_e32 v134, 0xc2a00000, v114
	v_max_f32_e32 v114, v170, v170
	v_max_f32_e32 v158, 0xc2a00000, v114
	v_mul_f32_e32 v114, 0xbfb8aa3b, v134
	v_exp_f32_e32 v114, v114
	v_mul_f32_e32 v135, 0xbfb8aa3b, v158
	v_exp_f32_e32 v135, v135
	v_max_f32_e32 v155, v171, v171
	v_add_f32_e32 v114, 1.0, v114
	v_rcp_f32_e32 v160, v114
	v_add_f32_e32 v114, 1.0, v135
	v_max_f32_e32 v135, v169, v169
	v_max_f32_e32 v135, 0xc2a00000, v135
	v_max_f32_e32 v159, 0xc2a00000, v155
	v_mul_f32_e32 v155, 0xbfb8aa3b, v135
	v_exp_f32_e32 v155, v155
	v_mul_f32_e32 v161, 0xbfb8aa3b, v159
	v_exp_f32_e32 v168, v161
	v_max_f32_e32 v138, v138, v138
	v_rcp_f32_e32 v170, v114
	v_add_f32_e32 v114, 1.0, v155
	v_max_f32_e32 v138, 0xc2a00000, v138
	v_max_f32_e32 v155, v166, v166
	v_max_f32_e32 v166, 0xc2a00000, v155
	v_mul_f32_e32 v155, 0xbfb8aa3b, v138
	v_exp_f32_e32 v155, v155
	v_rcp_f32_e32 v161, v114
	v_add_f32_e32 v114, 1.0, v168
	v_mul_f32_e32 v168, 0xbfb8aa3b, v166
	v_exp_f32_e32 v168, v168
	v_max_f32_e32 v139, v139, v139
	v_rcp_f32_e32 v171, v114
	v_add_f32_e32 v114, 1.0, v155
	v_max_f32_e32 v139, 0xc2a00000, v139
	v_max_f32_e32 v155, v167, v167
	v_max_f32_e32 v167, 0xc2a00000, v155
	v_mul_f32_e32 v155, 0xbfb8aa3b, v139
	v_rcp_f32_e32 v178, v114
	v_add_f32_e32 v114, 1.0, v168
	v_exp_f32_e32 v155, v155
	v_mul_f32_e32 v168, 0xbfb8aa3b, v167
	v_exp_f32_e32 v168, v168
	v_rcp_f32_e32 v180, v114
	v_add_f32_e32 v114, 1.0, v155
	v_rcp_f32_e32 v179, v114
	v_add_f32_e32 v114, 1.0, v168
	v_rcp_f32_e32 v181, v114
	v_pk_mul_f32 v[168:169], v[134:135], v[160:161]
	v_pk_mul_f32 v[138:139], v[138:139], v[178:179]
	v_pk_mul_f32 v[170:171], v[158:159], v[170:171]
	v_pk_mul_f32 v[166:167], v[166:167], v[180:181]
.LBB0_358:
	ds_read_b32 v134, v176 offset:128
	v_cvt_pk_bf16_f32 v168, v168, v169
	v_cvt_pk_bf16_f32 v169, v138, v139
	v_cvt_pk_bf16_f32 v170, v170, v171
	v_cvt_pk_bf16_f32 v171, v166, v167
	ds_bpermute_b32 v238, v244, v168
	ds_bpermute_b32 v239, v244, v169
	ds_bpermute_b32 v240, v244, v170
	ds_bpermute_b32 v241, v244, v171
	ds_bpermute_b32 v242, v244, v136
	ds_bpermute_b32 v243, v244, v137
	s_waitcnt lgkmcnt(0)
	global_store_dwordx4 v[242:243], v[238:241], off offset:64
	s_waitcnt lgkmcnt(0)
	v_pk_mul_f32 v[138:139], v[96:97], v[134:135] op_sel_hi:[1,0]
	v_pk_mul_f32 v[166:167], v[92:93], v[134:135] op_sel_hi:[1,0]
	v_pk_mul_f32 v[168:169], v[94:95], v[134:135] op_sel_hi:[1,0]
	s_and_b64 vcc, exec, s[40:41]
	v_pk_mul_f32 v[170:171], v[90:91], v[134:135] op_sel_hi:[1,0]
	s_cbranch_vccnz .LBB0_360
	v_max_f32_e32 v114, v168, v168
	v_max_f32_e32 v136, 0xc2a00000, v114
	v_max_f32_e32 v114, v170, v170
	v_max_f32_e32 v158, 0xc2a00000, v114
	v_mul_f32_e32 v114, 0xbfb8aa3b, v136
	v_exp_f32_e32 v114, v114
	v_mul_f32_e32 v135, 0xbfb8aa3b, v158
	v_exp_f32_e32 v135, v135
	v_add_f32_e32 v114, 1.0, v114
	v_rcp_f32_e32 v160, v114
	v_add_f32_e32 v114, 1.0, v135
	v_max_f32_e32 v135, v169, v169
	v_max_f32_e32 v137, 0xc2a00000, v135
	v_max_f32_e32 v135, v171, v171
	v_max_f32_e32 v159, 0xc2a00000, v135
	v_mul_f32_e32 v135, 0xbfb8aa3b, v137
	v_exp_f32_e32 v135, v135
	v_mul_f32_e32 v155, 0xbfb8aa3b, v159
	v_rcp_f32_e32 v170, v114
	v_exp_f32_e32 v155, v155
	v_add_f32_e32 v114, 1.0, v135
	v_max_f32_e32 v135, v138, v138
	v_max_f32_e32 v138, 0xc2a00000, v135
	v_max_f32_e32 v135, v166, v166
	v_max_f32_e32 v166, 0xc2a00000, v135
	v_mul_f32_e32 v135, 0xbfb8aa3b, v138
	v_exp_f32_e32 v135, v135
	v_rcp_f32_e32 v161, v114
	v_add_f32_e32 v114, 1.0, v155
	v_mul_f32_e32 v155, 0xbfb8aa3b, v166
	v_exp_f32_e32 v155, v155
	v_rcp_f32_e32 v171, v114
	v_add_f32_e32 v114, 1.0, v135
	v_max_f32_e32 v135, v139, v139
	v_max_f32_e32 v139, 0xc2a00000, v135
	v_max_f32_e32 v135, v167, v167
	v_max_f32_e32 v167, 0xc2a00000, v135
	v_mul_f32_e32 v135, 0xbfb8aa3b, v139
	v_rcp_f32_e32 v178, v114
	v_add_f32_e32 v114, 1.0, v155
	v_exp_f32_e32 v135, v135
	v_mul_f32_e32 v155, 0xbfb8aa3b, v167
	v_exp_f32_e32 v155, v155
	v_rcp_f32_e32 v180, v114
	v_add_f32_e32 v114, 1.0, v135
	v_rcp_f32_e32 v179, v114
	v_add_f32_e32 v114, 1.0, v155
	v_rcp_f32_e32 v181, v114
	v_pk_mul_f32 v[168:169], v[136:137], v[160:161]
	v_pk_mul_f32 v[138:139], v[138:139], v[178:179]
	v_pk_mul_f32 v[170:171], v[158:159], v[170:171]
	v_pk_mul_f32 v[166:167], v[166:167], v[180:181]
.LBB0_360:
	v_or_b32_e32 v136, 32, v152
	v_ashrrev_i32_e32 v137, 31, v136
	v_lshlrev_b64 v[136:137], 12, v[136:137]
	v_mov_b32_e32 v135, v134
	v_lshl_add_u64 v[136:137], v[132:133], 0, v[136:137]
	v_cvt_pk_bf16_f32 v168, v168, v169
	v_cvt_pk_bf16_f32 v169, v138, v139
	v_cvt_pk_bf16_f32 v170, v170, v171
	v_cvt_pk_bf16_f32 v171, v166, v167
	v_mov_b32_e32 v158, v134
	v_mov_b32_e32 v159, v134
	ds_bpermute_b32 v232, v244, v168
	ds_bpermute_b32 v233, v244, v169
	ds_bpermute_b32 v234, v244, v170
	ds_bpermute_b32 v235, v244, v171
	ds_bpermute_b32 v236, v244, v136
	ds_bpermute_b32 v237, v244, v137
	s_waitcnt lgkmcnt(0)
	global_store_dwordx4 v[236:237], v[232:235], off
	v_pk_mul_f32 v[138:139], v[88:89], v[158:159]
	v_pk_mul_f32 v[166:167], v[84:85], v[158:159]
	v_pk_mul_f32 v[168:169], v[86:87], v[134:135]
	s_and_b64 vcc, exec, s[40:41]
	v_pk_mul_f32 v[170:171], v[82:83], v[134:135]
	s_cbranch_vccnz .LBB0_362
	v_max_f32_e32 v114, v168, v168
	v_max_f32_e32 v134, 0xc2a00000, v114
	v_max_f32_e32 v114, v170, v170
	v_max_f32_e32 v158, 0xc2a00000, v114
	v_mul_f32_e32 v114, 0xbfb8aa3b, v134
	v_exp_f32_e32 v114, v114
	v_mul_f32_e32 v135, 0xbfb8aa3b, v158
	v_exp_f32_e32 v135, v135
	v_max_f32_e32 v155, v171, v171
	v_add_f32_e32 v114, 1.0, v114
	v_rcp_f32_e32 v160, v114
	v_add_f32_e32 v114, 1.0, v135
	v_max_f32_e32 v135, v169, v169
	v_max_f32_e32 v135, 0xc2a00000, v135
	v_max_f32_e32 v159, 0xc2a00000, v155
	v_mul_f32_e32 v155, 0xbfb8aa3b, v135
	v_exp_f32_e32 v155, v155
	v_mul_f32_e32 v161, 0xbfb8aa3b, v159
	v_exp_f32_e32 v168, v161
	v_max_f32_e32 v138, v138, v138
	v_rcp_f32_e32 v170, v114
	v_add_f32_e32 v114, 1.0, v155
	v_max_f32_e32 v138, 0xc2a00000, v138
	v_max_f32_e32 v155, v166, v166
	v_max_f32_e32 v166, 0xc2a00000, v155
	v_mul_f32_e32 v155, 0xbfb8aa3b, v138
	v_exp_f32_e32 v155, v155
	v_rcp_f32_e32 v161, v114
	v_add_f32_e32 v114, 1.0, v168
	v_mul_f32_e32 v168, 0xbfb8aa3b, v166
	v_exp_f32_e32 v168, v168
	v_max_f32_e32 v139, v139, v139
	v_rcp_f32_e32 v171, v114
	v_add_f32_e32 v114, 1.0, v155
	v_max_f32_e32 v139, 0xc2a00000, v139
	v_max_f32_e32 v155, v167, v167
	v_max_f32_e32 v167, 0xc2a00000, v155
	v_mul_f32_e32 v155, 0xbfb8aa3b, v139
	v_rcp_f32_e32 v178, v114
	v_add_f32_e32 v114, 1.0, v168
	v_exp_f32_e32 v155, v155
	v_mul_f32_e32 v168, 0xbfb8aa3b, v167
	v_exp_f32_e32 v168, v168
	v_rcp_f32_e32 v180, v114
	v_add_f32_e32 v114, 1.0, v155
	v_rcp_f32_e32 v179, v114
	v_add_f32_e32 v114, 1.0, v168
	v_rcp_f32_e32 v181, v114
	v_pk_mul_f32 v[168:169], v[134:135], v[160:161]
	v_pk_mul_f32 v[138:139], v[138:139], v[178:179]
	v_pk_mul_f32 v[170:171], v[158:159], v[170:171]
	v_pk_mul_f32 v[166:167], v[166:167], v[180:181]
.LBB0_362:
	ds_read_b32 v134, v176 offset:192
	v_cvt_pk_bf16_f32 v168, v168, v169
	v_cvt_pk_bf16_f32 v169, v138, v139
	v_cvt_pk_bf16_f32 v170, v170, v171
	v_cvt_pk_bf16_f32 v171, v166, v167
	ds_bpermute_b32 v238, v244, v168
	ds_bpermute_b32 v239, v244, v169
	ds_bpermute_b32 v240, v244, v170
	ds_bpermute_b32 v241, v244, v171
	ds_bpermute_b32 v242, v244, v136
	ds_bpermute_b32 v243, v244, v137
	s_waitcnt lgkmcnt(0)
	global_store_dwordx4 v[242:243], v[238:241], off offset:64
	s_waitcnt lgkmcnt(0)
	v_pk_mul_f32 v[138:139], v[80:81], v[134:135] op_sel_hi:[1,0]
	v_pk_mul_f32 v[166:167], v[76:77], v[134:135] op_sel_hi:[1,0]
	v_pk_mul_f32 v[168:169], v[78:79], v[134:135] op_sel_hi:[1,0]
	s_and_b64 vcc, exec, s[40:41]
	v_pk_mul_f32 v[170:171], v[74:75], v[134:135] op_sel_hi:[1,0]
	s_cbranch_vccnz .LBB0_364
	v_max_f32_e32 v114, v168, v168
	v_max_f32_e32 v136, 0xc2a00000, v114
	v_max_f32_e32 v114, v170, v170
	v_max_f32_e32 v158, 0xc2a00000, v114
	v_mul_f32_e32 v114, 0xbfb8aa3b, v136
	v_exp_f32_e32 v114, v114
	v_mul_f32_e32 v135, 0xbfb8aa3b, v158
	v_exp_f32_e32 v135, v135
	v_add_f32_e32 v114, 1.0, v114
	v_rcp_f32_e32 v160, v114
	v_add_f32_e32 v114, 1.0, v135
	v_max_f32_e32 v135, v169, v169
	v_max_f32_e32 v137, 0xc2a00000, v135
	v_max_f32_e32 v135, v171, v171
	v_max_f32_e32 v159, 0xc2a00000, v135
	v_mul_f32_e32 v135, 0xbfb8aa3b, v137
	v_exp_f32_e32 v135, v135
	v_mul_f32_e32 v155, 0xbfb8aa3b, v159
	v_rcp_f32_e32 v170, v114
	v_exp_f32_e32 v155, v155
	v_add_f32_e32 v114, 1.0, v135
	v_max_f32_e32 v135, v138, v138
	v_max_f32_e32 v138, 0xc2a00000, v135
	v_max_f32_e32 v135, v166, v166
	v_max_f32_e32 v166, 0xc2a00000, v135
	v_mul_f32_e32 v135, 0xbfb8aa3b, v138
	v_exp_f32_e32 v135, v135
	v_rcp_f32_e32 v161, v114
	v_add_f32_e32 v114, 1.0, v155
	v_mul_f32_e32 v155, 0xbfb8aa3b, v166
	v_exp_f32_e32 v155, v155
	v_rcp_f32_e32 v171, v114
	v_add_f32_e32 v114, 1.0, v135
	v_max_f32_e32 v135, v139, v139
	v_max_f32_e32 v139, 0xc2a00000, v135
	v_max_f32_e32 v135, v167, v167
	v_max_f32_e32 v167, 0xc2a00000, v135
	v_mul_f32_e32 v135, 0xbfb8aa3b, v139
	v_rcp_f32_e32 v178, v114
	v_add_f32_e32 v114, 1.0, v155
	v_exp_f32_e32 v135, v135
	v_mul_f32_e32 v155, 0xbfb8aa3b, v167
	v_exp_f32_e32 v155, v155
	v_rcp_f32_e32 v180, v114
	v_add_f32_e32 v114, 1.0, v135
	v_rcp_f32_e32 v179, v114
	v_add_f32_e32 v114, 1.0, v155
	v_rcp_f32_e32 v181, v114
	v_pk_mul_f32 v[168:169], v[136:137], v[160:161]
	v_pk_mul_f32 v[138:139], v[138:139], v[178:179]
	v_pk_mul_f32 v[170:171], v[158:159], v[170:171]
	v_pk_mul_f32 v[166:167], v[166:167], v[180:181]
.LBB0_364:
	v_or_b32_e32 v136, 48, v152
	v_ashrrev_i32_e32 v137, 31, v136
	v_lshlrev_b64 v[136:137], 12, v[136:137]
	v_mov_b32_e32 v135, v134
	v_lshl_add_u64 v[136:137], v[132:133], 0, v[136:137]
	v_cvt_pk_bf16_f32 v168, v168, v169
	v_cvt_pk_bf16_f32 v169, v138, v139
	v_cvt_pk_bf16_f32 v170, v170, v171
	v_cvt_pk_bf16_f32 v171, v166, v167
	v_mov_b32_e32 v158, v134
	v_mov_b32_e32 v159, v134
	ds_bpermute_b32 v232, v244, v168
	ds_bpermute_b32 v233, v244, v169
	ds_bpermute_b32 v234, v244, v170
	ds_bpermute_b32 v235, v244, v171
	ds_bpermute_b32 v236, v244, v136
	ds_bpermute_b32 v237, v244, v137
	s_waitcnt lgkmcnt(0)
	global_store_dwordx4 v[236:237], v[232:235], off
	v_pk_mul_f32 v[138:139], v[72:73], v[158:159]
	v_pk_mul_f32 v[166:167], v[68:69], v[158:159]
	v_pk_mul_f32 v[168:169], v[70:71], v[134:135]
	s_and_b64 vcc, exec, s[40:41]
	v_pk_mul_f32 v[170:171], v[66:67], v[134:135]
	s_cbranch_vccnz .LBB0_366
	v_max_f32_e32 v114, v168, v168
	v_max_f32_e32 v134, 0xc2a00000, v114
	v_max_f32_e32 v114, v170, v170
	v_max_f32_e32 v158, 0xc2a00000, v114
	v_mul_f32_e32 v114, 0xbfb8aa3b, v134
	v_exp_f32_e32 v114, v114
	v_mul_f32_e32 v135, 0xbfb8aa3b, v158
	v_exp_f32_e32 v135, v135
	v_max_f32_e32 v155, v171, v171
	v_add_f32_e32 v114, 1.0, v114
	v_rcp_f32_e32 v160, v114
	v_add_f32_e32 v114, 1.0, v135
	v_max_f32_e32 v135, v169, v169
	v_max_f32_e32 v135, 0xc2a00000, v135
	v_max_f32_e32 v159, 0xc2a00000, v155
	v_mul_f32_e32 v155, 0xbfb8aa3b, v135
	v_exp_f32_e32 v155, v155
	v_mul_f32_e32 v161, 0xbfb8aa3b, v159
	v_exp_f32_e32 v168, v161
	v_max_f32_e32 v138, v138, v138
	v_rcp_f32_e32 v170, v114
	v_add_f32_e32 v114, 1.0, v155
	v_max_f32_e32 v138, 0xc2a00000, v138
	v_max_f32_e32 v155, v166, v166
	v_max_f32_e32 v166, 0xc2a00000, v155
	v_mul_f32_e32 v155, 0xbfb8aa3b, v138
	v_exp_f32_e32 v155, v155
	v_rcp_f32_e32 v161, v114
	v_add_f32_e32 v114, 1.0, v168
	v_mul_f32_e32 v168, 0xbfb8aa3b, v166
	v_exp_f32_e32 v168, v168
	v_max_f32_e32 v139, v139, v139
	v_rcp_f32_e32 v171, v114
	v_add_f32_e32 v114, 1.0, v155
	v_max_f32_e32 v139, 0xc2a00000, v139
	v_max_f32_e32 v155, v167, v167
	v_max_f32_e32 v167, 0xc2a00000, v155
	v_mul_f32_e32 v155, 0xbfb8aa3b, v139
	v_rcp_f32_e32 v178, v114
	v_add_f32_e32 v114, 1.0, v168
	v_exp_f32_e32 v155, v155
	v_mul_f32_e32 v168, 0xbfb8aa3b, v167
	v_exp_f32_e32 v168, v168
	v_rcp_f32_e32 v180, v114
	v_add_f32_e32 v114, 1.0, v155
	v_rcp_f32_e32 v179, v114
	v_add_f32_e32 v114, 1.0, v168
	v_rcp_f32_e32 v181, v114
	v_pk_mul_f32 v[168:169], v[134:135], v[160:161]
	v_pk_mul_f32 v[138:139], v[138:139], v[178:179]
	v_pk_mul_f32 v[170:171], v[158:159], v[170:171]
	v_pk_mul_f32 v[166:167], v[166:167], v[180:181]
.LBB0_366:
	ds_read_b32 v134, v176 offset:512
	v_cvt_pk_bf16_f32 v168, v168, v169
	v_cvt_pk_bf16_f32 v169, v138, v139
	v_cvt_pk_bf16_f32 v170, v170, v171
	v_cvt_pk_bf16_f32 v171, v166, v167
	ds_bpermute_b32 v238, v244, v168
	ds_bpermute_b32 v239, v244, v169
	ds_bpermute_b32 v240, v244, v170
	ds_bpermute_b32 v241, v244, v171
	ds_bpermute_b32 v242, v244, v136
	ds_bpermute_b32 v243, v244, v137
	s_waitcnt lgkmcnt(0)
	global_store_dwordx4 v[242:243], v[238:241], off offset:64
	s_waitcnt lgkmcnt(0)
	v_pk_mul_f32 v[138:139], v[64:65], v[134:135] op_sel_hi:[1,0]
	v_pk_mul_f32 v[166:167], v[60:61], v[134:135] op_sel_hi:[1,0]
	v_pk_mul_f32 v[168:169], v[62:63], v[134:135] op_sel_hi:[1,0]
	s_and_b64 vcc, exec, s[40:41]
	v_pk_mul_f32 v[170:171], v[58:59], v[134:135] op_sel_hi:[1,0]
	s_cbranch_vccnz .LBB0_368
	v_max_f32_e32 v114, v168, v168
	v_max_f32_e32 v136, 0xc2a00000, v114
	v_max_f32_e32 v114, v170, v170
	v_max_f32_e32 v158, 0xc2a00000, v114
	v_mul_f32_e32 v114, 0xbfb8aa3b, v136
	v_exp_f32_e32 v114, v114
	v_mul_f32_e32 v135, 0xbfb8aa3b, v158
	v_exp_f32_e32 v135, v135
	v_add_f32_e32 v114, 1.0, v114
	v_rcp_f32_e32 v160, v114
	v_add_f32_e32 v114, 1.0, v135
	v_max_f32_e32 v135, v169, v169
	v_max_f32_e32 v137, 0xc2a00000, v135
	v_max_f32_e32 v135, v171, v171
	v_max_f32_e32 v159, 0xc2a00000, v135
	v_mul_f32_e32 v135, 0xbfb8aa3b, v137
	v_exp_f32_e32 v135, v135
	v_mul_f32_e32 v155, 0xbfb8aa3b, v159
	v_rcp_f32_e32 v170, v114
	v_exp_f32_e32 v155, v155
	v_add_f32_e32 v114, 1.0, v135
	v_max_f32_e32 v135, v138, v138
	v_max_f32_e32 v138, 0xc2a00000, v135
	v_max_f32_e32 v135, v166, v166
	v_max_f32_e32 v166, 0xc2a00000, v135
	v_mul_f32_e32 v135, 0xbfb8aa3b, v138
	v_exp_f32_e32 v135, v135
	v_rcp_f32_e32 v161, v114
	v_add_f32_e32 v114, 1.0, v155
	v_mul_f32_e32 v155, 0xbfb8aa3b, v166
	v_exp_f32_e32 v155, v155
	v_rcp_f32_e32 v171, v114
	v_add_f32_e32 v114, 1.0, v135
	v_max_f32_e32 v135, v139, v139
	v_max_f32_e32 v139, 0xc2a00000, v135
	v_max_f32_e32 v135, v167, v167
	v_max_f32_e32 v167, 0xc2a00000, v135
	v_mul_f32_e32 v135, 0xbfb8aa3b, v139
	v_rcp_f32_e32 v178, v114
	v_add_f32_e32 v114, 1.0, v155
	v_exp_f32_e32 v135, v135
	v_mul_f32_e32 v155, 0xbfb8aa3b, v167
	v_exp_f32_e32 v155, v155
	v_rcp_f32_e32 v180, v114
	v_add_f32_e32 v114, 1.0, v135
	v_rcp_f32_e32 v179, v114
	v_add_f32_e32 v114, 1.0, v155
	v_rcp_f32_e32 v181, v114
	v_pk_mul_f32 v[168:169], v[136:137], v[160:161]
	v_pk_mul_f32 v[138:139], v[138:139], v[178:179]
	v_pk_mul_f32 v[170:171], v[158:159], v[170:171]
	v_pk_mul_f32 v[166:167], v[166:167], v[180:181]
.LBB0_368:
	v_lshlrev_b64 v[136:137], 12, v[152:153]
	v_lshl_add_u64 v[136:137], v[132:133], 0, v[136:137]
	s_mov_b32 s14, 0x80000
	v_cvt_pk_bf16_f32 v168, v168, v169
	v_cvt_pk_bf16_f32 v169, v138, v139
	v_add_co_u32_e32 v138, vcc, s14, v136
	v_mov_b32_e32 v135, v134
	v_cvt_pk_bf16_f32 v170, v170, v171
	v_cvt_pk_bf16_f32 v171, v166, v167
	s_nop 0
	v_addc_co_u32_e32 v139, vcc, 0, v137, vcc
	v_mov_b32_e32 v158, v134
	v_mov_b32_e32 v159, v134
	ds_bpermute_b32 v232, v244, v168
	ds_bpermute_b32 v233, v244, v169
	ds_bpermute_b32 v234, v244, v170
	ds_bpermute_b32 v235, v244, v171
	ds_bpermute_b32 v236, v244, v138
	ds_bpermute_b32 v237, v244, v139
	s_waitcnt lgkmcnt(0)
	global_store_dwordx4 v[236:237], v[232:235], off
	v_pk_mul_f32 v[138:139], v[56:57], v[158:159]
	v_pk_mul_f32 v[166:167], v[52:53], v[158:159]
	v_pk_mul_f32 v[168:169], v[54:55], v[134:135]
	s_and_b64 vcc, exec, s[40:41]
	v_pk_mul_f32 v[170:171], v[50:51], v[134:135]
	s_cbranch_vccnz .LBB0_370
	v_max_f32_e32 v114, v168, v168
	v_max_f32_e32 v134, 0xc2a00000, v114
	v_max_f32_e32 v114, v170, v170
	v_max_f32_e32 v158, 0xc2a00000, v114
	v_mul_f32_e32 v114, 0xbfb8aa3b, v134
	v_exp_f32_e32 v114, v114
	v_mul_f32_e32 v135, 0xbfb8aa3b, v158
	v_exp_f32_e32 v135, v135
	v_max_f32_e32 v155, v171, v171
	v_add_f32_e32 v114, 1.0, v114
	v_rcp_f32_e32 v160, v114
	v_add_f32_e32 v114, 1.0, v135
	v_max_f32_e32 v135, v169, v169
	v_max_f32_e32 v135, 0xc2a00000, v135
	v_max_f32_e32 v159, 0xc2a00000, v155
	v_mul_f32_e32 v155, 0xbfb8aa3b, v135
	v_exp_f32_e32 v155, v155
	v_mul_f32_e32 v161, 0xbfb8aa3b, v159
	v_exp_f32_e32 v168, v161
	v_max_f32_e32 v138, v138, v138
	v_rcp_f32_e32 v170, v114
	v_add_f32_e32 v114, 1.0, v155
	v_max_f32_e32 v138, 0xc2a00000, v138
	v_max_f32_e32 v155, v166, v166
	v_max_f32_e32 v166, 0xc2a00000, v155
	v_mul_f32_e32 v155, 0xbfb8aa3b, v138
	v_exp_f32_e32 v155, v155
	v_rcp_f32_e32 v161, v114
	v_add_f32_e32 v114, 1.0, v168
	v_mul_f32_e32 v168, 0xbfb8aa3b, v166
	v_exp_f32_e32 v168, v168
	v_max_f32_e32 v139, v139, v139
	v_rcp_f32_e32 v171, v114
	v_add_f32_e32 v114, 1.0, v155
	v_max_f32_e32 v139, 0xc2a00000, v139
	v_max_f32_e32 v155, v167, v167
	v_max_f32_e32 v167, 0xc2a00000, v155
	v_mul_f32_e32 v155, 0xbfb8aa3b, v139
	v_rcp_f32_e32 v178, v114
	v_add_f32_e32 v114, 1.0, v168
	v_exp_f32_e32 v155, v155
	v_mul_f32_e32 v168, 0xbfb8aa3b, v167
	v_exp_f32_e32 v168, v168
	v_rcp_f32_e32 v180, v114
	v_add_f32_e32 v114, 1.0, v155
	v_rcp_f32_e32 v179, v114
	v_add_f32_e32 v114, 1.0, v168
	v_rcp_f32_e32 v181, v114
	v_pk_mul_f32 v[168:169], v[134:135], v[160:161]
	v_pk_mul_f32 v[138:139], v[138:139], v[178:179]
	v_pk_mul_f32 v[170:171], v[158:159], v[170:171]
	v_pk_mul_f32 v[166:167], v[166:167], v[180:181]
.LBB0_370:
	ds_read_b32 v134, v176 offset:576
	s_mov_b64 s[14:15], 0x80000
	v_lshl_add_u64 v[158:159], v[136:137], 0, s[14:15]
	v_cvt_pk_bf16_f32 v137, v138, v139
	v_cvt_pk_bf16_f32 v138, v170, v171
	v_cvt_pk_bf16_f32 v139, v166, v167
	v_cvt_pk_bf16_f32 v136, v168, v169
	ds_bpermute_b32 v238, v244, v136
	ds_bpermute_b32 v239, v244, v137
	ds_bpermute_b32 v240, v244, v138
	ds_bpermute_b32 v241, v244, v139
	ds_bpermute_b32 v242, v244, v158
	ds_bpermute_b32 v243, v244, v159
	s_waitcnt lgkmcnt(0)
	global_store_dwordx4 v[242:243], v[238:241], off offset:64
	s_waitcnt lgkmcnt(0)
	v_pk_mul_f32 v[168:169], v[46:47], v[134:135] op_sel_hi:[1,0]
	v_pk_mul_f32 v[166:167], v[44:45], v[134:135] op_sel_hi:[1,0]
	v_pk_mul_f32 v[138:139], v[48:49], v[134:135] op_sel_hi:[1,0]
	s_and_b64 vcc, exec, s[40:41]
	v_pk_mul_f32 v[170:171], v[42:43], v[134:135] op_sel_hi:[1,0]
	s_cbranch_vccnz .LBB0_372
	v_max_f32_e32 v114, v168, v168
	v_max_f32_e32 v136, 0xc2a00000, v114
	v_max_f32_e32 v114, v170, v170
	v_max_f32_e32 v158, 0xc2a00000, v114
	v_mul_f32_e32 v114, 0xbfb8aa3b, v136
	v_exp_f32_e32 v114, v114
	v_mul_f32_e32 v135, 0xbfb8aa3b, v158
	v_exp_f32_e32 v135, v135
	v_add_f32_e32 v114, 1.0, v114
	v_rcp_f32_e32 v160, v114
	v_add_f32_e32 v114, 1.0, v135
	v_max_f32_e32 v135, v169, v169
	v_max_f32_e32 v137, 0xc2a00000, v135
	v_max_f32_e32 v135, v171, v171
	v_max_f32_e32 v159, 0xc2a00000, v135
	v_mul_f32_e32 v135, 0xbfb8aa3b, v137
	v_exp_f32_e32 v135, v135
	v_mul_f32_e32 v155, 0xbfb8aa3b, v159
	v_rcp_f32_e32 v170, v114
	v_exp_f32_e32 v155, v155
	v_add_f32_e32 v114, 1.0, v135
	v_max_f32_e32 v135, v138, v138
	v_max_f32_e32 v138, 0xc2a00000, v135
	v_max_f32_e32 v135, v166, v166
	v_max_f32_e32 v166, 0xc2a00000, v135
	v_mul_f32_e32 v135, 0xbfb8aa3b, v138
	v_exp_f32_e32 v135, v135
	v_rcp_f32_e32 v161, v114
	v_add_f32_e32 v114, 1.0, v155
	v_mul_f32_e32 v155, 0xbfb8aa3b, v166
	v_exp_f32_e32 v155, v155
	v_rcp_f32_e32 v171, v114
	v_add_f32_e32 v114, 1.0, v135
	v_max_f32_e32 v135, v139, v139
	v_max_f32_e32 v139, 0xc2a00000, v135
	v_max_f32_e32 v135, v167, v167
	v_max_f32_e32 v167, 0xc2a00000, v135
	v_mul_f32_e32 v135, 0xbfb8aa3b, v139
	v_rcp_f32_e32 v178, v114
	v_add_f32_e32 v114, 1.0, v155
	v_exp_f32_e32 v135, v135
	v_mul_f32_e32 v155, 0xbfb8aa3b, v167
	v_exp_f32_e32 v155, v155
	v_rcp_f32_e32 v180, v114
	v_add_f32_e32 v114, 1.0, v135
	v_rcp_f32_e32 v179, v114
	v_add_f32_e32 v114, 1.0, v155
	v_rcp_f32_e32 v181, v114
	v_pk_mul_f32 v[168:169], v[136:137], v[160:161]
	v_pk_mul_f32 v[138:139], v[138:139], v[178:179]
	v_pk_mul_f32 v[170:171], v[158:159], v[170:171]
	v_pk_mul_f32 v[166:167], v[166:167], v[180:181]
.LBB0_372:
	v_lshlrev_b64 v[136:137], 12, v[152:153]
	v_lshl_add_u64 v[136:137], v[132:133], 0, v[136:137]
	s_mov_b32 s14, 0x90000
	v_cvt_pk_bf16_f32 v168, v168, v169
	v_cvt_pk_bf16_f32 v169, v138, v139
	v_add_co_u32_e32 v138, vcc, s14, v136
	v_mov_b32_e32 v135, v134
	v_cvt_pk_bf16_f32 v170, v170, v171
	v_cvt_pk_bf16_f32 v171, v166, v167
	s_nop 0
	v_addc_co_u32_e32 v139, vcc, 0, v137, vcc
	v_mov_b32_e32 v158, v134
	v_mov_b32_e32 v159, v134
	ds_bpermute_b32 v232, v244, v168
	ds_bpermute_b32 v233, v244, v169
	ds_bpermute_b32 v234, v244, v170
	ds_bpermute_b32 v235, v244, v171
	ds_bpermute_b32 v236, v244, v138
	ds_bpermute_b32 v237, v244, v139
	s_waitcnt lgkmcnt(0)
	global_store_dwordx4 v[236:237], v[232:235], off
	v_pk_mul_f32 v[138:139], v[40:41], v[158:159]
	v_pk_mul_f32 v[166:167], v[36:37], v[158:159]
	v_pk_mul_f32 v[168:169], v[38:39], v[134:135]
	s_and_b64 vcc, exec, s[40:41]
	v_pk_mul_f32 v[170:171], v[34:35], v[134:135]
	s_cbranch_vccnz .LBB0_374
	v_max_f32_e32 v114, v168, v168
	v_max_f32_e32 v134, 0xc2a00000, v114
	v_max_f32_e32 v114, v170, v170
	v_max_f32_e32 v158, 0xc2a00000, v114
	v_mul_f32_e32 v114, 0xbfb8aa3b, v134
	v_exp_f32_e32 v114, v114
	v_mul_f32_e32 v135, 0xbfb8aa3b, v158
	v_exp_f32_e32 v135, v135
	v_max_f32_e32 v155, v171, v171
	v_add_f32_e32 v114, 1.0, v114
	v_rcp_f32_e32 v160, v114
	v_add_f32_e32 v114, 1.0, v135
	v_max_f32_e32 v135, v169, v169
	v_max_f32_e32 v135, 0xc2a00000, v135
	v_max_f32_e32 v159, 0xc2a00000, v155
	v_mul_f32_e32 v155, 0xbfb8aa3b, v135
	v_exp_f32_e32 v155, v155
	v_mul_f32_e32 v161, 0xbfb8aa3b, v159
	v_exp_f32_e32 v168, v161
	v_max_f32_e32 v138, v138, v138
	v_rcp_f32_e32 v170, v114
	v_add_f32_e32 v114, 1.0, v155
	v_max_f32_e32 v138, 0xc2a00000, v138
	v_max_f32_e32 v155, v166, v166
	v_max_f32_e32 v166, 0xc2a00000, v155
	v_mul_f32_e32 v155, 0xbfb8aa3b, v138
	v_exp_f32_e32 v155, v155
	v_rcp_f32_e32 v161, v114
	v_add_f32_e32 v114, 1.0, v168
	v_mul_f32_e32 v168, 0xbfb8aa3b, v166
	v_exp_f32_e32 v168, v168
	v_max_f32_e32 v139, v139, v139
	v_rcp_f32_e32 v171, v114
	v_add_f32_e32 v114, 1.0, v155
	v_max_f32_e32 v139, 0xc2a00000, v139
	v_max_f32_e32 v155, v167, v167
	v_max_f32_e32 v167, 0xc2a00000, v155
	v_mul_f32_e32 v155, 0xbfb8aa3b, v139
	v_rcp_f32_e32 v178, v114
	v_add_f32_e32 v114, 1.0, v168
	v_exp_f32_e32 v155, v155
	v_mul_f32_e32 v168, 0xbfb8aa3b, v167
	v_exp_f32_e32 v168, v168
	v_rcp_f32_e32 v180, v114
	v_add_f32_e32 v114, 1.0, v155
	v_rcp_f32_e32 v179, v114
	v_add_f32_e32 v114, 1.0, v168
	v_rcp_f32_e32 v181, v114
	v_pk_mul_f32 v[168:169], v[134:135], v[160:161]
	v_pk_mul_f32 v[138:139], v[138:139], v[178:179]
	v_pk_mul_f32 v[170:171], v[158:159], v[170:171]
	v_pk_mul_f32 v[166:167], v[166:167], v[180:181]
.LBB0_374:
	ds_read_b32 v134, v176 offset:640
	s_mov_b64 s[14:15], 0x90000
	v_lshl_add_u64 v[158:159], v[136:137], 0, s[14:15]
	v_cvt_pk_bf16_f32 v137, v138, v139
	v_cvt_pk_bf16_f32 v138, v170, v171
	v_cvt_pk_bf16_f32 v139, v166, v167
	v_cvt_pk_bf16_f32 v136, v168, v169
	ds_bpermute_b32 v238, v244, v136
	ds_bpermute_b32 v239, v244, v137
	ds_bpermute_b32 v240, v244, v138
	ds_bpermute_b32 v241, v244, v139
	ds_bpermute_b32 v242, v244, v158
	ds_bpermute_b32 v243, v244, v159
	s_waitcnt lgkmcnt(0)
	global_store_dwordx4 v[242:243], v[238:241], off offset:64
	s_waitcnt lgkmcnt(0)
	v_pk_mul_f32 v[168:169], v[30:31], v[134:135] op_sel_hi:[1,0]
	v_pk_mul_f32 v[166:167], v[28:29], v[134:135] op_sel_hi:[1,0]
	v_pk_mul_f32 v[138:139], v[32:33], v[134:135] op_sel_hi:[1,0]
	s_and_b64 vcc, exec, s[40:41]
	v_pk_mul_f32 v[170:171], v[26:27], v[134:135] op_sel_hi:[1,0]
	s_cbranch_vccnz .LBB0_376
	v_max_f32_e32 v114, v168, v168
	v_max_f32_e32 v136, 0xc2a00000, v114
	v_max_f32_e32 v114, v170, v170
	v_max_f32_e32 v158, 0xc2a00000, v114
	v_mul_f32_e32 v114, 0xbfb8aa3b, v136
	v_exp_f32_e32 v114, v114
	v_mul_f32_e32 v135, 0xbfb8aa3b, v158
	v_exp_f32_e32 v135, v135
	v_add_f32_e32 v114, 1.0, v114
	v_rcp_f32_e32 v160, v114
	v_add_f32_e32 v114, 1.0, v135
	v_max_f32_e32 v135, v169, v169
	v_max_f32_e32 v137, 0xc2a00000, v135
	v_max_f32_e32 v135, v171, v171
	v_max_f32_e32 v159, 0xc2a00000, v135
	v_mul_f32_e32 v135, 0xbfb8aa3b, v137
	v_exp_f32_e32 v135, v135
	v_mul_f32_e32 v155, 0xbfb8aa3b, v159
	v_rcp_f32_e32 v170, v114
	v_exp_f32_e32 v155, v155
	v_add_f32_e32 v114, 1.0, v135
	v_max_f32_e32 v135, v138, v138
	v_max_f32_e32 v138, 0xc2a00000, v135
	v_max_f32_e32 v135, v166, v166
	v_max_f32_e32 v166, 0xc2a00000, v135
	v_mul_f32_e32 v135, 0xbfb8aa3b, v138
	v_exp_f32_e32 v135, v135
	v_rcp_f32_e32 v161, v114
	v_add_f32_e32 v114, 1.0, v155
	v_mul_f32_e32 v155, 0xbfb8aa3b, v166
	v_exp_f32_e32 v155, v155
	v_rcp_f32_e32 v171, v114
	v_add_f32_e32 v114, 1.0, v135
	v_max_f32_e32 v135, v139, v139
	v_max_f32_e32 v139, 0xc2a00000, v135
	v_max_f32_e32 v135, v167, v167
	v_max_f32_e32 v167, 0xc2a00000, v135
	v_mul_f32_e32 v135, 0xbfb8aa3b, v139
	v_rcp_f32_e32 v178, v114
	v_add_f32_e32 v114, 1.0, v155
	v_exp_f32_e32 v135, v135
	v_mul_f32_e32 v155, 0xbfb8aa3b, v167
	v_exp_f32_e32 v155, v155
	v_rcp_f32_e32 v180, v114
	v_add_f32_e32 v114, 1.0, v135
	v_rcp_f32_e32 v179, v114
	v_add_f32_e32 v114, 1.0, v155
	v_rcp_f32_e32 v181, v114
	v_pk_mul_f32 v[168:169], v[136:137], v[160:161]
	v_pk_mul_f32 v[138:139], v[138:139], v[178:179]
	v_pk_mul_f32 v[170:171], v[158:159], v[170:171]
	v_pk_mul_f32 v[166:167], v[166:167], v[180:181]
.LBB0_376:
	v_lshlrev_b64 v[136:137], 12, v[152:153]
	v_lshl_add_u64 v[136:137], v[132:133], 0, v[136:137]
	s_mov_b32 s14, 0xa0000
	v_cvt_pk_bf16_f32 v168, v168, v169
	v_cvt_pk_bf16_f32 v169, v138, v139
	v_add_co_u32_e32 v138, vcc, s14, v136
	v_mov_b32_e32 v135, v134
	v_cvt_pk_bf16_f32 v170, v170, v171
	v_cvt_pk_bf16_f32 v171, v166, v167
	s_nop 0
	v_addc_co_u32_e32 v139, vcc, 0, v137, vcc
	v_mov_b32_e32 v158, v134
	v_mov_b32_e32 v159, v134
	ds_bpermute_b32 v232, v244, v168
	ds_bpermute_b32 v233, v244, v169
	ds_bpermute_b32 v234, v244, v170
	ds_bpermute_b32 v235, v244, v171
	ds_bpermute_b32 v236, v244, v138
	ds_bpermute_b32 v237, v244, v139
	s_waitcnt lgkmcnt(0)
	global_store_dwordx4 v[236:237], v[232:235], off
	v_pk_mul_f32 v[138:139], v[24:25], v[158:159]
	v_pk_mul_f32 v[166:167], v[20:21], v[158:159]
	v_pk_mul_f32 v[168:169], v[22:23], v[134:135]
	s_and_b64 vcc, exec, s[40:41]
	v_pk_mul_f32 v[170:171], v[18:19], v[134:135]
	s_cbranch_vccnz .LBB0_378
	v_max_f32_e32 v114, v168, v168
	v_max_f32_e32 v134, 0xc2a00000, v114
	v_max_f32_e32 v114, v170, v170
	v_max_f32_e32 v158, 0xc2a00000, v114
	v_mul_f32_e32 v114, 0xbfb8aa3b, v134
	v_exp_f32_e32 v114, v114
	v_mul_f32_e32 v135, 0xbfb8aa3b, v158
	v_exp_f32_e32 v135, v135
	v_max_f32_e32 v155, v171, v171
	v_add_f32_e32 v114, 1.0, v114
	v_rcp_f32_e32 v160, v114
	v_add_f32_e32 v114, 1.0, v135
	v_max_f32_e32 v135, v169, v169
	v_max_f32_e32 v135, 0xc2a00000, v135
	v_max_f32_e32 v159, 0xc2a00000, v155
	v_mul_f32_e32 v155, 0xbfb8aa3b, v135
	v_exp_f32_e32 v155, v155
	v_mul_f32_e32 v161, 0xbfb8aa3b, v159
	v_exp_f32_e32 v168, v161
	v_max_f32_e32 v138, v138, v138
	v_rcp_f32_e32 v170, v114
	v_add_f32_e32 v114, 1.0, v155
	v_max_f32_e32 v138, 0xc2a00000, v138
	v_max_f32_e32 v155, v166, v166
	v_max_f32_e32 v166, 0xc2a00000, v155
	v_mul_f32_e32 v155, 0xbfb8aa3b, v138
	v_exp_f32_e32 v155, v155
	v_rcp_f32_e32 v161, v114
	v_add_f32_e32 v114, 1.0, v168
	v_mul_f32_e32 v168, 0xbfb8aa3b, v166
	v_exp_f32_e32 v168, v168
	v_max_f32_e32 v139, v139, v139
	v_rcp_f32_e32 v171, v114
	v_add_f32_e32 v114, 1.0, v155
	v_max_f32_e32 v139, 0xc2a00000, v139
	v_max_f32_e32 v155, v167, v167
	v_max_f32_e32 v167, 0xc2a00000, v155
	v_mul_f32_e32 v155, 0xbfb8aa3b, v139
	v_rcp_f32_e32 v178, v114
	v_add_f32_e32 v114, 1.0, v168
	v_exp_f32_e32 v155, v155
	v_mul_f32_e32 v168, 0xbfb8aa3b, v167
	v_exp_f32_e32 v168, v168
	v_rcp_f32_e32 v180, v114
	v_add_f32_e32 v114, 1.0, v155
	v_rcp_f32_e32 v179, v114
	v_add_f32_e32 v114, 1.0, v168
	v_rcp_f32_e32 v181, v114
	v_pk_mul_f32 v[168:169], v[134:135], v[160:161]
	v_pk_mul_f32 v[138:139], v[138:139], v[178:179]
	v_pk_mul_f32 v[170:171], v[158:159], v[170:171]
	v_pk_mul_f32 v[166:167], v[166:167], v[180:181]
.LBB0_378:
	ds_read_b32 v134, v176 offset:704
	s_mov_b64 s[14:15], 0xa0000
	v_lshl_add_u64 v[158:159], v[136:137], 0, s[14:15]
	v_cvt_pk_bf16_f32 v136, v168, v169
	v_cvt_pk_bf16_f32 v137, v138, v139
	v_cvt_pk_bf16_f32 v138, v170, v171
	v_cvt_pk_bf16_f32 v139, v166, v167
	ds_bpermute_b32 v238, v244, v136
	ds_bpermute_b32 v239, v244, v137
	ds_bpermute_b32 v240, v244, v138
	ds_bpermute_b32 v241, v244, v139
	ds_bpermute_b32 v242, v244, v158
	ds_bpermute_b32 v243, v244, v159
	s_waitcnt lgkmcnt(0)
	global_store_dwordx4 v[242:243], v[238:241], off offset:64
	s_waitcnt lgkmcnt(0)
	v_pk_mul_f32 v[166:167], v[14:15], v[134:135] op_sel_hi:[1,0]
	s_and_b64 vcc, exec, s[40:41]
	v_pk_mul_f32 v[136:137], v[16:17], v[134:135] op_sel_hi:[1,0]
	v_pk_mul_f32 v[138:139], v[12:13], v[134:135] op_sel_hi:[1,0]
	v_pk_mul_f32 v[168:169], v[10:11], v[134:135] op_sel_hi:[1,0]
	s_cbranch_vccnz .LBB0_380
	v_max_f32_e32 v114, v166, v166
	v_max_f32_e32 v158, 0xc2a00000, v114
	v_max_f32_e32 v114, v168, v168
	v_max_f32_e32 v160, 0xc2a00000, v114
	v_mul_f32_e32 v114, 0xbfb8aa3b, v158
	v_exp_f32_e32 v114, v114
	v_mul_f32_e32 v135, 0xbfb8aa3b, v160
	v_exp_f32_e32 v135, v135
	v_add_f32_e32 v114, 1.0, v114
	v_rcp_f32_e32 v166, v114
	v_add_f32_e32 v114, 1.0, v135
	v_max_f32_e32 v135, v167, v167
	v_max_f32_e32 v159, 0xc2a00000, v135
	v_max_f32_e32 v135, v169, v169
	v_max_f32_e32 v161, 0xc2a00000, v135
	v_mul_f32_e32 v135, 0xbfb8aa3b, v159
	v_exp_f32_e32 v135, v135
	v_mul_f32_e32 v155, 0xbfb8aa3b, v161
	v_rcp_f32_e32 v168, v114
	v_exp_f32_e32 v155, v155
	v_add_f32_e32 v114, 1.0, v135
	v_max_f32_e32 v135, v136, v136
	v_max_f32_e32 v136, 0xc2a00000, v135
	v_max_f32_e32 v135, v138, v138
	v_max_f32_e32 v138, 0xc2a00000, v135
	v_mul_f32_e32 v135, 0xbfb8aa3b, v136
	v_exp_f32_e32 v135, v135
	v_rcp_f32_e32 v167, v114
	v_add_f32_e32 v114, 1.0, v155
	v_mul_f32_e32 v155, 0xbfb8aa3b, v138
	v_exp_f32_e32 v155, v155
	v_rcp_f32_e32 v169, v114
	v_add_f32_e32 v114, 1.0, v135
	v_max_f32_e32 v135, v137, v137
	v_max_f32_e32 v137, 0xc2a00000, v135
	v_max_f32_e32 v135, v139, v139
	v_max_f32_e32 v139, 0xc2a00000, v135
	v_mul_f32_e32 v135, 0xbfb8aa3b, v137
	v_rcp_f32_e32 v170, v114
	v_add_f32_e32 v114, 1.0, v155
	v_exp_f32_e32 v135, v135
	v_mul_f32_e32 v155, 0xbfb8aa3b, v139
	v_exp_f32_e32 v155, v155
	v_rcp_f32_e32 v178, v114
	v_add_f32_e32 v114, 1.0, v135
	v_rcp_f32_e32 v171, v114
	v_add_f32_e32 v114, 1.0, v155
	v_rcp_f32_e32 v179, v114
	v_pk_mul_f32 v[166:167], v[158:159], v[166:167]
	v_pk_mul_f32 v[136:137], v[136:137], v[170:171]
	v_pk_mul_f32 v[168:169], v[160:161], v[168:169]
	v_pk_mul_f32 v[138:139], v[138:139], v[178:179]
.LBB0_380:
	v_lshlrev_b64 v[158:159], 12, v[152:153]
	v_lshl_add_u64 v[132:133], v[132:133], 0, v[158:159]
	s_mov_b32 s14, 0xb0000
	v_cvt_pk_bf16_f32 v166, v166, v167
	v_cvt_pk_bf16_f32 v167, v136, v137
	v_add_co_u32_e32 v136, vcc, s14, v132
	v_mov_b32_e32 v135, v134
	s_nop 0
	v_addc_co_u32_e32 v137, vcc, 0, v133, vcc
	v_cvt_pk_bf16_f32 v168, v168, v169
	v_cvt_pk_bf16_f32 v169, v138, v139
	ds_bpermute_b32 v232, v244, v166
	ds_bpermute_b32 v233, v244, v167
	ds_bpermute_b32 v234, v244, v168
	ds_bpermute_b32 v235, v244, v169
	ds_bpermute_b32 v236, v244, v136
	ds_bpermute_b32 v237, v244, v137
	s_waitcnt lgkmcnt(0)
	global_store_dwordx4 v[236:237], v[232:235], off
	v_mov_b32_e32 v136, v134
	v_mov_b32_e32 v137, v134
	v_pk_mul_f32 v[138:139], v[8:9], v[136:137]
	v_pk_mul_f32 v[168:169], v[6:7], v[134:135]
	v_pk_mul_f32 v[166:167], v[4:5], v[136:137]
	s_and_b64 vcc, exec, s[40:41]
	v_pk_mul_f32 v[134:135], v[2:3], v[134:135]
	s_cbranch_vccnz .LBB0_382
	v_max_f32_e32 v114, v168, v168
	v_max_f32_e32 v136, 0xc2a00000, v114
	v_max_f32_e32 v114, v134, v134
	v_max_f32_e32 v134, 0xc2a00000, v114
	v_mul_f32_e32 v114, 0xbfb8aa3b, v136
	v_exp_f32_e32 v114, v114
	v_mul_f32_e32 v137, 0xbfb8aa3b, v134
	v_exp_f32_e32 v137, v137
	v_max_f32_e32 v135, v135, v135
	v_add_f32_e32 v114, 1.0, v114
	v_rcp_f32_e32 v158, v114
	v_add_f32_e32 v114, 1.0, v137
	v_max_f32_e32 v137, v169, v169
	v_max_f32_e32 v137, 0xc2a00000, v137
	v_mul_f32_e32 v153, 0xbfb8aa3b, v137
	v_exp_f32_e32 v153, v153
	v_max_f32_e32 v135, 0xc2a00000, v135
	v_mul_f32_e32 v155, 0xbfb8aa3b, v135
	v_exp_f32_e32 v155, v155
	v_max_f32_e32 v138, v138, v138
	v_rcp_f32_e32 v160, v114
	v_add_f32_e32 v114, 1.0, v153
	v_max_f32_e32 v138, 0xc2a00000, v138
	v_max_f32_e32 v153, v166, v166
	v_max_f32_e32 v166, 0xc2a00000, v153
	v_mul_f32_e32 v153, 0xbfb8aa3b, v138
	v_exp_f32_e32 v153, v153
	v_rcp_f32_e32 v159, v114
	v_add_f32_e32 v114, 1.0, v155
	v_mul_f32_e32 v155, 0xbfb8aa3b, v166
	v_exp_f32_e32 v155, v155
	v_max_f32_e32 v139, v139, v139
	v_rcp_f32_e32 v161, v114
	v_add_f32_e32 v114, 1.0, v153
	v_max_f32_e32 v139, 0xc2a00000, v139
	v_max_f32_e32 v153, v167, v167
	v_max_f32_e32 v167, 0xc2a00000, v153
	v_mul_f32_e32 v153, 0xbfb8aa3b, v139
	v_rcp_f32_e32 v170, v114
	v_add_f32_e32 v114, 1.0, v155
	v_exp_f32_e32 v153, v153
	v_mul_f32_e32 v155, 0xbfb8aa3b, v167
	v_exp_f32_e32 v155, v155
	v_rcp_f32_e32 v178, v114
	v_add_f32_e32 v114, 1.0, v153
	v_rcp_f32_e32 v171, v114
	v_add_f32_e32 v114, 1.0, v155
	v_rcp_f32_e32 v179, v114
	v_pk_mul_f32 v[168:169], v[136:137], v[158:159]
	v_pk_mul_f32 v[138:139], v[138:139], v[170:171]
	v_pk_mul_f32 v[134:135], v[134:135], v[160:161]
	v_pk_mul_f32 v[166:167], v[166:167], v[178:179]

.LBB0_383:
	s_andn2_b64 vcc, exec, s[38:39]
	s_mov_b64 s[28:29], -1
	ds_bpermute_b32 v238, v244, v132
	ds_bpermute_b32 v239, v244, v133
	ds_bpermute_b32 v240, v244, v134
	ds_bpermute_b32 v241, v244, v135
	ds_bpermute_b32 v242, v244, v136
	ds_bpermute_b32 v243, v244, v137
	s_waitcnt lgkmcnt(0)
	global_store_dwordx4 v[242:243], v[238:241], off offset:64
	s_cbranch_vccnz .LBB0_338
	s_branch .LBB0_386
.LBB0_384:
	s_and_b64 vcc, exec, s[40:41]
	s_cbranch_vccz .LBB0_383
	v_lshlrev_b32_e32 v155, 2, v177
	global_load_dwordx4 v[136:139], v155, s[44:45]
	global_load_dwordx4 v[132:135], v155, s[44:45] offset:16
	s_waitcnt lgkmcnt(0)
	v_mul_f32_e32 v160, v128, v154
	v_mul_f32_e32 v161, v129, v154
	v_mul_f32_e32 v166, v130, v154
	v_mul_f32_e32 v167, v131, v154
	v_mul_f32_e32 v168, v124, v154
	v_mul_f32_e32 v169, v125, v154
	v_mul_f32_e32 v170, v126, v154
	v_mul_f32_e32 v171, v127, v154
	global_load_dwordx4 v[124:127], v155, s[44:45] offset:144
	global_load_dwordx4 v[128:131], v155, s[44:45] offset:128
	v_ashrrev_i32_e32 v153, 31, v152
	v_lshlrev_b64 v[158:159], 12, v[152:153]
	v_max_f32_e32 v153, 0xc2a00000, v160
	v_max_f32_e32 v155, 0xc2a00000, v161
	v_max_f32_e32 v160, 0xc2a00000, v166
	v_max_f32_e32 v161, 0xc2a00000, v167
	v_max_f32_e32 v166, 0xc2a00000, v168
	v_max_f32_e32 v167, 0xc2a00000, v169
	v_max_f32_e32 v168, 0xc2a00000, v170
	v_max_f32_e32 v169, 0xc2a00000, v171
	v_mul_f32_e32 v153, 0xbfb8aa3b, v153
	v_mul_f32_e32 v155, 0xbfb8aa3b, v155
	v_mul_f32_e32 v168, 0xbfb8aa3b, v168
	v_mul_f32_e32 v169, 0xbfb8aa3b, v169
	v_exp_f32_e32 v153, v153
	v_exp_f32_e32 v155, v155
	v_mul_f32_e32 v160, 0xbfb8aa3b, v160
	v_mul_f32_e32 v161, 0xbfb8aa3b, v161
	v_exp_f32_e32 v168, v168
	v_exp_f32_e32 v169, v169
	v_exp_f32_e32 v160, v160
	v_exp_f32_e32 v161, v161
	v_mul_f32_e32 v120, v120, v154
	v_max_f32_e32 v120, 0xc2a00000, v120
	v_add_f32_e32 v153, 1.0, v153
	v_add_f32_e32 v155, 1.0, v155
	v_mul_f32_e32 v121, v121, v154
	v_lshlrev_b32_e32 v114, 1, v177
	v_mul_f32_e32 v166, 0xbfb8aa3b, v166
	v_mul_f32_e32 v167, 0xbfb8aa3b, v167
	v_lshl_add_u64 v[158:159], s[42:43], 0, v[158:159]
	v_add_f32_e32 v168, 1.0, v168
	v_add_f32_e32 v169, 1.0, v169
	v_rcp_f32_e32 v153, v153
	v_rcp_f32_e32 v181, v155
	v_mul_f32_e32 v120, 0xbfb8aa3b, v120
	v_max_f32_e32 v121, 0xc2a00000, v121
	v_exp_f32_e32 v170, v166
	v_exp_f32_e32 v171, v167
	v_lshl_add_u64 v[166:167], v[158:159], 0, v[114:115]
	v_add_f32_e32 v158, 1.0, v160
	v_add_f32_e32 v159, 1.0, v161
	v_rcp_f32_e32 v168, v168
	v_rcp_f32_e32 v182, v169
	v_exp_f32_e32 v120, v120
	v_mul_f32_e32 v121, 0xbfb8aa3b, v121
	v_rcp_f32_e32 v158, v158
	v_rcp_f32_e32 v159, v159
	v_exp_f32_e32 v121, v121
	v_add_f32_e32 v120, 1.0, v120
	v_rcp_f32_e32 v120, v120
	v_mul_f32_e32 v116, v116, v154
	v_add_f32_e32 v121, 1.0, v121
	v_rcp_f32_e32 v121, v121
	v_add_f32_e32 v160, 1.0, v170
	v_add_f32_e32 v161, 1.0, v171
	v_max_f32_e32 v116, 0xc2a00000, v116
	v_mul_f32_e32 v117, v117, v154
	v_rcp_f32_e32 v160, v160
	v_rcp_f32_e32 v161, v161
	v_mul_f32_e32 v116, 0xbfb8aa3b, v116
	v_max_f32_e32 v117, 0xc2a00000, v117
	v_exp_f32_e32 v116, v116
	v_mul_f32_e32 v117, 0xbfb8aa3b, v117
	v_exp_f32_e32 v117, v117
	s_mov_b64 s[14:15], 0x80000
	v_add_f32_e32 v116, 1.0, v116
	v_rcp_f32_e32 v116, v116
	v_add_f32_e32 v117, 1.0, v117
	s_waitcnt vmcnt(0)
	v_sub_f32_e32 v180, 1.0, v136
	v_sub_f32_e32 v179, 1.0, v137
	v_sub_f32_e32 v169, 1.0, v134
	v_sub_f32_e32 v155, 1.0, v135
	v_fma_f32 v153, v180, v153, v136
	v_fma_f32 v181, v179, v181, v137
	v_sub_f32_e32 v178, 1.0, v138
	v_sub_f32_e32 v177, 1.0, v139
	v_fma_f32 v168, v169, v168, v134
	v_fma_f32 v182, v155, v182, v135
	v_log_f32_e32 v153, v153
	v_log_f32_e32 v181, v181
	v_fma_f32 v158, v178, v158, v138
	v_fma_f32 v159, v177, v159, v139
	v_log_f32_e32 v168, v168
	v_log_f32_e32 v182, v182
	v_log_f32_e32 v158, v158
	v_log_f32_e32 v159, v159
	v_cvt_pk_f16_f32 v194, v153, v181
	v_sub_f32_e32 v153, 1.0, v128
	v_cvt_pk_f16_f32 v197, v168, v182
	v_fma_f32 v120, v153, v120, v128
	v_sub_f32_e32 v168, 1.0, v129
	v_cvt_pk_f16_f32 v195, v158, v159
	v_log_f32_e32 v158, v120
	v_fma_f32 v120, v168, v121, v129
	v_log_f32_e32 v159, v120
	v_mul_f32_e32 v120, v122, v154
	v_max_f32_e32 v120, 0xc2a00000, v120
	v_mul_f32_e32 v121, v123, v154
	v_mul_f32_e32 v120, 0xbfb8aa3b, v120
	v_max_f32_e32 v121, 0xc2a00000, v121
	v_exp_f32_e32 v120, v120
	v_mul_f32_e32 v121, 0xbfb8aa3b, v121
	v_exp_f32_e32 v122, v121
	v_sub_f32_e32 v171, 1.0, v132
	v_sub_f32_e32 v170, 1.0, v133
	v_add_f32_e32 v120, 1.0, v120
	v_fma_f32 v160, v171, v160, v132
	v_fma_f32 v161, v170, v161, v133
	v_rcp_f32_e32 v120, v120
	v_add_f32_e32 v122, 1.0, v122
	v_log_f32_e32 v160, v160
	v_log_f32_e32 v161, v161
	v_rcp_f32_e32 v123, v122
	v_sub_f32_e32 v121, 1.0, v130
	v_rcp_f32_e32 v117, v117
	v_fma_f32 v120, v121, v120, v130
	v_sub_f32_e32 v122, 1.0, v131
	v_cvt_pk_f16_f32 v196, v160, v161
	v_log_f32_e32 v160, v120
	v_fma_f32 v120, v122, v123, v131
	v_sub_f32_e32 v123, 1.0, v124
	v_log_f32_e32 v161, v120
	v_fma_f32 v116, v123, v116, v124
	v_sub_f32_e32 v120, 1.0, v125
	v_log_f32_e32 v181, v116
	v_fma_f32 v116, v120, v117, v125
	v_log_f32_e32 v182, v116
	v_mul_f32_e32 v116, v118, v154
	v_max_f32_e32 v116, 0xc2a00000, v116
	v_mul_f32_e32 v117, v119, v154
	v_mul_f32_e32 v116, 0xbfb8aa3b, v116
	v_max_f32_e32 v117, 0xc2a00000, v117
	v_exp_f32_e32 v116, v116
	v_mul_f32_e32 v117, 0xbfb8aa3b, v117
	v_exp_f32_e32 v117, v117
	v_sub_f32_e32 v118, 1.0, v126
	v_add_f32_e32 v116, 1.0, v116
	v_rcp_f32_e32 v116, v116
	v_add_f32_e32 v117, 1.0, v117
	v_rcp_f32_e32 v117, v117
	v_sub_f32_e32 v119, 1.0, v127
	v_fma_f32 v116, v118, v116, v126
	v_log_f32_e32 v154, v116
	v_fma_f32 v116, v119, v117, v127
	v_log_f32_e32 v183, v116
	ds_read2_b32 v[116:117], v176 offset0:16 offset1:32
	ds_bpermute_b32 v232, v244, v194
	ds_bpermute_b32 v233, v244, v195
	ds_bpermute_b32 v234, v244, v196
	ds_bpermute_b32 v235, v244, v197
	ds_bpermute_b32 v236, v244, v166
	ds_bpermute_b32 v237, v244, v167
	s_waitcnt lgkmcnt(0)
	global_store_dwordx4 v[236:237], v[232:235], off
	s_waitcnt lgkmcnt(0)
	v_mul_f32_e32 v106, v106, v116
	v_max_f32_e32 v106, 0xc2a00000, v106
	v_mul_f32_e32 v106, 0xbfb8aa3b, v106
	v_exp_f32_e32 v106, v106
	v_mul_f32_e32 v110, v110, v116
	v_max_f32_e32 v110, 0xc2a00000, v110
	v_mul_f32_e32 v111, v111, v116
	v_mul_f32_e32 v110, 0xbfb8aa3b, v110
	v_max_f32_e32 v111, 0xc2a00000, v111
	v_mul_f32_e32 v107, v107, v116
	v_exp_f32_e32 v110, v110
	v_mul_f32_e32 v111, 0xbfb8aa3b, v111
	v_add_f32_e32 v106, 1.0, v106
	v_max_f32_e32 v107, 0xc2a00000, v107
	v_exp_f32_e32 v111, v111
	v_rcp_f32_e32 v106, v106
	v_mul_f32_e32 v107, 0xbfb8aa3b, v107
	v_exp_f32_e32 v107, v107
	v_cvt_pk_f16_f32 v194, v158, v159
	v_or_b32_e32 v158, 16, v152
	v_add_f32_e32 v110, 1.0, v110
	v_mul_f32_e32 v112, v112, v116
	v_mul_f32_e32 v113, v113, v116
	v_cvt_pk_f16_f32 v197, v154, v183
	v_ashrrev_i32_e32 v159, 31, v158
	v_rcp_f32_e32 v154, v110
	v_add_f32_e32 v110, 1.0, v111
	v_max_f32_e32 v112, 0xc2a00000, v112
	v_max_f32_e32 v113, 0xc2a00000, v113
	v_fma_f32 v106, v171, v106, v132
	v_cvt_pk_f16_f32 v195, v160, v161
	v_rcp_f32_e32 v160, v110
	v_lshlrev_b64 v[110:111], 12, v[158:159]
	v_mul_f32_e32 v112, 0xbfb8aa3b, v112
	v_mul_f32_e32 v113, 0xbfb8aa3b, v113
	v_log_f32_e32 v159, v106
	v_add_f32_e32 v106, 1.0, v107
	v_mul_f32_e32 v107, v108, v116
	v_exp_f32_e32 v112, v112
	v_exp_f32_e32 v113, v113
	v_max_f32_e32 v107, 0xc2a00000, v107
	v_mul_f32_e32 v108, v109, v116
	v_mul_f32_e32 v107, 0xbfb8aa3b, v107
	v_max_f32_e32 v108, 0xc2a00000, v108
	v_exp_f32_e32 v107, v107
	v_mul_f32_e32 v108, 0xbfb8aa3b, v108
	v_exp_f32_e32 v108, v108
	v_add_f32_e32 v112, 1.0, v112
	v_add_f32_e32 v113, 1.0, v113
	v_rcp_f32_e32 v112, v112
	v_rcp_f32_e32 v113, v113
	v_mul_f32_e32 v98, v98, v116
	v_rcp_f32_e32 v106, v106
	v_add_f32_e32 v107, 1.0, v107
	v_max_f32_e32 v98, 0xc2a00000, v98
	v_rcp_f32_e32 v107, v107
	v_add_f32_e32 v108, 1.0, v108
	v_mul_f32_e32 v98, 0xbfb8aa3b, v98
	v_rcp_f32_e32 v108, v108
	v_exp_f32_e32 v98, v98
	v_fma_f32 v112, v178, v112, v138
	v_fma_f32 v113, v177, v113, v139
	v_log_f32_e32 v112, v112
	v_log_f32_e32 v113, v113
	v_fma_f32 v106, v170, v106, v133
	v_log_f32_e32 v109, v106
	v_fma_f32 v106, v169, v107, v134
	v_mul_f32_e32 v102, v102, v116
	v_mul_f32_e32 v99, v99, v116
	v_fma_f32 v154, v180, v154, v136
	v_fma_f32 v158, v179, v160, v137
	v_log_f32_e32 v160, v106
	v_fma_f32 v106, v155, v108, v135
	v_max_f32_e32 v102, 0xc2a00000, v102
	v_add_f32_e32 v98, 1.0, v98
	v_max_f32_e32 v99, 0xc2a00000, v99
	v_log_f32_e32 v154, v154
	v_log_f32_e32 v158, v158
	v_log_f32_e32 v161, v106
	v_mul_f32_e32 v102, 0xbfb8aa3b, v102
	v_rcp_f32_e32 v98, v98
	v_mul_f32_e32 v99, 0xbfb8aa3b, v99
	v_cvt_pk_f16_f32 v107, v112, v113
	v_exp_f32_e32 v112, v102
	v_mul_f32_e32 v102, v103, v116
	v_exp_f32_e32 v99, v99
	v_max_f32_e32 v102, 0xc2a00000, v102
	v_lshl_add_u64 v[110:111], s[42:43], 0, v[110:111]
	v_mul_f32_e32 v102, 0xbfb8aa3b, v102
	v_cvt_pk_f16_f32 v106, v154, v158
	v_cvt_pk_f16_f32 v108, v159, v109
	v_cvt_pk_f16_f32 v109, v160, v161
	v_exp_f32_e32 v113, v102
	v_lshl_add_u64 v[102:103], v[110:111], 0, v[114:115]
	v_fma_f32 v98, v123, v98, v124
	ds_bpermute_b32 v238, v244, v106
	ds_bpermute_b32 v239, v244, v107
	ds_bpermute_b32 v240, v244, v108
	ds_bpermute_b32 v241, v244, v109
	ds_bpermute_b32 v242, v244, v102
	ds_bpermute_b32 v243, v244, v103
	s_waitcnt lgkmcnt(0)
	global_store_dwordx4 v[242:243], v[238:241], off
	v_mul_f32_e32 v104, v104, v116
	v_mul_f32_e32 v105, v105, v116
	v_log_f32_e32 v108, v98
	v_add_f32_e32 v98, 1.0, v99
	v_mul_f32_e32 v99, v100, v116
	v_max_f32_e32 v99, 0xc2a00000, v99
	v_mul_f32_e32 v100, v101, v116
	v_max_f32_e32 v104, 0xc2a00000, v104
	v_max_f32_e32 v105, 0xc2a00000, v105
	v_mul_f32_e32 v99, 0xbfb8aa3b, v99
	v_max_f32_e32 v100, 0xc2a00000, v100
	v_mul_f32_e32 v104, 0xbfb8aa3b, v104
	v_mul_f32_e32 v105, 0xbfb8aa3b, v105
	v_exp_f32_e32 v99, v99
	v_mul_f32_e32 v100, 0xbfb8aa3b, v100
	v_exp_f32_e32 v104, v104
	v_exp_f32_e32 v105, v105
	v_exp_f32_e32 v100, v100
	v_rcp_f32_e32 v98, v98
	v_add_f32_e32 v99, 1.0, v99
	v_add_f32_e32 v110, 1.0, v112
	v_add_f32_e32 v111, 1.0, v113
	v_add_f32_e32 v104, 1.0, v104
	v_add_f32_e32 v105, 1.0, v105
	v_rcp_f32_e32 v99, v99
	v_add_f32_e32 v100, 1.0, v100
	v_rcp_f32_e32 v110, v110
	v_rcp_f32_e32 v111, v111
	v_rcp_f32_e32 v104, v104
	v_rcp_f32_e32 v105, v105
	v_rcp_f32_e32 v100, v100
	v_mul_f32_e32 v90, v90, v117
	v_fma_f32 v98, v120, v98, v125
	v_mul_f32_e32 v94, v94, v117
	v_max_f32_e32 v90, 0xc2a00000, v90
	v_log_f32_e32 v101, v98
	v_fma_f32 v98, v118, v99, v126
	v_max_f32_e32 v94, 0xc2a00000, v94
	v_mul_f32_e32 v90, 0xbfb8aa3b, v90
	v_fma_f32 v106, v153, v110, v128
	v_fma_f32 v107, v168, v111, v129
	v_fma_f32 v104, v121, v104, v130
	v_fma_f32 v105, v122, v105, v131
	v_log_f32_e32 v109, v98
	v_fma_f32 v98, v119, v100, v127
	v_mul_f32_e32 v94, 0xbfb8aa3b, v94
	v_exp_f32_e32 v90, v90
	v_log_f32_e32 v106, v106
	v_log_f32_e32 v107, v107
	v_log_f32_e32 v104, v104
	v_log_f32_e32 v105, v105
	v_log_f32_e32 v110, v98
	v_exp_f32_e32 v94, v94
	v_mul_f32_e32 v95, v95, v117
	v_max_f32_e32 v95, 0xc2a00000, v95
	v_mul_f32_e32 v91, v91, v117
	v_mul_f32_e32 v95, 0xbfb8aa3b, v95
	v_add_f32_e32 v90, 1.0, v90
	v_max_f32_e32 v91, 0xc2a00000, v91
	v_cvt_pk_f16_f32 v98, v106, v107
	v_cvt_pk_f16_f32 v99, v104, v105
	v_cvt_pk_f16_f32 v100, v108, v101
	v_cvt_pk_f16_f32 v101, v109, v110
	v_exp_f32_e32 v95, v95
	v_add_f32_e32 v94, 1.0, v94
	v_rcp_f32_e32 v90, v90
	v_mul_f32_e32 v91, 0xbfb8aa3b, v91
	ds_bpermute_b32 v232, v244, v98
	ds_bpermute_b32 v233, v244, v99
	ds_bpermute_b32 v234, v244, v100
	ds_bpermute_b32 v235, v244, v101
	ds_bpermute_b32 v236, v244, v102
	ds_bpermute_b32 v237, v244, v103
	s_waitcnt lgkmcnt(0)
	global_store_dwordx4 v[236:237], v[232:235], off offset:64
	v_exp_f32_e32 v91, v91
	v_fma_f32 v90, v171, v90, v132
	v_rcp_f32_e32 v100, v94
	v_or_b32_e32 v98, 32, v152
	v_ashrrev_i32_e32 v99, 31, v98
	v_add_f32_e32 v94, 1.0, v95
	v_rcp_f32_e32 v101, v94
	v_lshlrev_b64 v[94:95], 12, v[98:99]
	v_fma_f32 v98, v180, v100, v136
	v_log_f32_e32 v100, v90
	v_add_f32_e32 v90, 1.0, v91
	v_mul_f32_e32 v91, v92, v117
	v_mul_f32_e32 v96, v96, v117
	v_mul_f32_e32 v97, v97, v117
	v_max_f32_e32 v91, 0xc2a00000, v91
	v_mul_f32_e32 v92, v93, v117
	v_max_f32_e32 v96, 0xc2a00000, v96
	v_max_f32_e32 v97, 0xc2a00000, v97
	v_mul_f32_e32 v91, 0xbfb8aa3b, v91
	v_max_f32_e32 v92, 0xc2a00000, v92
	v_mul_f32_e32 v96, 0xbfb8aa3b, v96
	v_mul_f32_e32 v97, 0xbfb8aa3b, v97
	v_exp_f32_e32 v91, v91
	v_mul_f32_e32 v92, 0xbfb8aa3b, v92
	v_exp_f32_e32 v96, v96
	v_exp_f32_e32 v97, v97
	v_exp_f32_e32 v92, v92
	v_mul_f32_e32 v82, v82, v117
	v_rcp_f32_e32 v90, v90
	v_add_f32_e32 v91, 1.0, v91
	v_max_f32_e32 v82, 0xc2a00000, v82
	v_add_f32_e32 v96, 1.0, v96
	v_add_f32_e32 v97, 1.0, v97
	v_rcp_f32_e32 v91, v91
	v_add_f32_e32 v92, 1.0, v92
	v_mul_f32_e32 v82, 0xbfb8aa3b, v82
	v_rcp_f32_e32 v96, v96
	v_rcp_f32_e32 v97, v97
	v_rcp_f32_e32 v92, v92
	v_exp_f32_e32 v82, v82
	v_fma_f32 v90, v170, v90, v133
	v_log_f32_e32 v93, v90
	v_fma_f32 v90, v169, v91, v134
	v_mul_f32_e32 v83, v83, v117
	v_fma_f32 v99, v179, v101, v137
	v_fma_f32 v96, v178, v96, v138
	v_fma_f32 v97, v177, v97, v139
	v_log_f32_e32 v101, v90
	v_fma_f32 v90, v155, v92, v135
	v_add_f32_e32 v82, 1.0, v82
	v_max_f32_e32 v83, 0xc2a00000, v83
	v_log_f32_e32 v98, v98
	v_log_f32_e32 v99, v99
	v_log_f32_e32 v96, v96
	v_log_f32_e32 v97, v97
	v_log_f32_e32 v102, v90
	v_rcp_f32_e32 v82, v82
	v_mul_f32_e32 v83, 0xbfb8aa3b, v83
	v_exp_f32_e32 v83, v83
	v_lshl_add_u64 v[94:95], s[42:43], 0, v[94:95]
	v_cvt_pk_f16_f32 v90, v98, v99
	v_cvt_pk_f16_f32 v91, v96, v97
	v_cvt_pk_f16_f32 v92, v100, v93
	v_cvt_pk_f16_f32 v93, v101, v102
	v_lshl_add_u64 v[94:95], v[94:95], 0, v[114:115]
	v_fma_f32 v82, v123, v82, v124
	ds_bpermute_b32 v238, v244, v90
	ds_bpermute_b32 v239, v244, v91
	ds_bpermute_b32 v240, v244, v92
	ds_bpermute_b32 v241, v244, v93
	ds_bpermute_b32 v242, v244, v94
	ds_bpermute_b32 v243, v244, v95
	s_waitcnt lgkmcnt(0)
	global_store_dwordx4 v[242:243], v[238:241], off
	v_mul_f32_e32 v86, v86, v117
	v_mul_f32_e32 v87, v87, v117
	v_log_f32_e32 v90, v82
	v_add_f32_e32 v82, 1.0, v83
	v_mul_f32_e32 v83, v84, v117
	v_max_f32_e32 v83, 0xc2a00000, v83
	v_mul_f32_e32 v84, v85, v117
	v_mul_f32_e32 v83, 0xbfb8aa3b, v83
	v_max_f32_e32 v84, 0xc2a00000, v84
	v_exp_f32_e32 v83, v83
	v_mul_f32_e32 v84, 0xbfb8aa3b, v84
	v_exp_f32_e32 v84, v84
	v_rcp_f32_e32 v82, v82
	v_add_f32_e32 v83, 1.0, v83
	v_rcp_f32_e32 v83, v83
	v_add_f32_e32 v84, 1.0, v84
	v_rcp_f32_e32 v84, v84
	v_mul_f32_e32 v88, v88, v117
	v_mul_f32_e32 v89, v89, v117
	v_max_f32_e32 v86, 0xc2a00000, v86
	v_max_f32_e32 v87, 0xc2a00000, v87
	v_max_f32_e32 v88, 0xc2a00000, v88
	v_max_f32_e32 v89, 0xc2a00000, v89
	v_fma_f32 v82, v120, v82, v125
	v_mul_f32_e32 v86, 0xbfb8aa3b, v86
	v_mul_f32_e32 v87, 0xbfb8aa3b, v87
	v_mul_f32_e32 v88, 0xbfb8aa3b, v88
	v_mul_f32_e32 v89, 0xbfb8aa3b, v89
	v_log_f32_e32 v91, v82
	v_fma_f32 v82, v118, v83, v126
	v_exp_f32_e32 v86, v86
	v_exp_f32_e32 v87, v87
	v_exp_f32_e32 v88, v88
	v_exp_f32_e32 v89, v89
	v_log_f32_e32 v92, v82
	v_fma_f32 v82, v119, v84, v127
	v_log_f32_e32 v93, v82
	ds_read2_b32 v[82:83], v176 offset0:48 offset1:128
	v_add_f32_e32 v86, 1.0, v86
	v_add_f32_e32 v87, 1.0, v87
	v_add_f32_e32 v88, 1.0, v88
	v_add_f32_e32 v89, 1.0, v89
	v_rcp_f32_e32 v86, v86
	v_rcp_f32_e32 v87, v87
	v_rcp_f32_e32 v88, v88
	v_rcp_f32_e32 v89, v89
	s_waitcnt lgkmcnt(0)
	v_mul_f32_e32 v74, v74, v82
	v_mul_f32_e32 v78, v78, v82
	v_max_f32_e32 v74, 0xc2a00000, v74
	v_max_f32_e32 v78, 0xc2a00000, v78
	v_mul_f32_e32 v74, 0xbfb8aa3b, v74
	v_fma_f32 v86, v153, v86, v128
	v_fma_f32 v87, v168, v87, v129
	v_fma_f32 v88, v121, v88, v130
	v_fma_f32 v89, v122, v89, v131
	v_mul_f32_e32 v78, 0xbfb8aa3b, v78
	v_exp_f32_e32 v74, v74
	v_log_f32_e32 v86, v86
	v_log_f32_e32 v87, v87
	v_log_f32_e32 v88, v88
	v_log_f32_e32 v89, v89
	v_exp_f32_e32 v78, v78
	v_mul_f32_e32 v79, v79, v82
	v_max_f32_e32 v79, 0xc2a00000, v79
	v_mul_f32_e32 v75, v75, v82
	v_mul_f32_e32 v79, 0xbfb8aa3b, v79
	v_add_f32_e32 v74, 1.0, v74
	v_max_f32_e32 v75, 0xc2a00000, v75
	v_cvt_pk_f16_f32 v84, v86, v87
	v_cvt_pk_f16_f32 v85, v88, v89
	v_cvt_pk_f16_f32 v86, v90, v91
	v_cvt_pk_f16_f32 v87, v92, v93
	v_exp_f32_e32 v79, v79
	v_add_f32_e32 v78, 1.0, v78
	v_rcp_f32_e32 v74, v74
	v_mul_f32_e32 v75, 0xbfb8aa3b, v75
	ds_bpermute_b32 v232, v244, v84
	ds_bpermute_b32 v233, v244, v85
	ds_bpermute_b32 v234, v244, v86
	ds_bpermute_b32 v235, v244, v87
	ds_bpermute_b32 v236, v244, v94
	ds_bpermute_b32 v237, v244, v95
	s_waitcnt lgkmcnt(0)
	global_store_dwordx4 v[236:237], v[232:235], off offset:64
	v_exp_f32_e32 v75, v75
	v_mul_f32_e32 v80, v80, v82
	v_rcp_f32_e32 v86, v78
	v_or_b32_e32 v84, 48, v152
	v_mul_f32_e32 v81, v81, v82
	v_ashrrev_i32_e32 v85, 31, v84
	v_add_f32_e32 v78, 1.0, v79
	v_max_f32_e32 v80, 0xc2a00000, v80
	v_max_f32_e32 v81, 0xc2a00000, v81
	v_fma_f32 v74, v171, v74, v132
	v_rcp_f32_e32 v87, v78
	v_lshlrev_b64 v[78:79], 12, v[84:85]
	v_fma_f32 v84, v180, v86, v136
	v_mul_f32_e32 v80, 0xbfb8aa3b, v80
	v_mul_f32_e32 v81, 0xbfb8aa3b, v81
	v_log_f32_e32 v86, v74
	v_add_f32_e32 v74, 1.0, v75
	v_mul_f32_e32 v75, v76, v82
	v_exp_f32_e32 v80, v80
	v_exp_f32_e32 v81, v81
	v_max_f32_e32 v75, 0xc2a00000, v75
	v_mul_f32_e32 v76, v77, v82
	v_mul_f32_e32 v75, 0xbfb8aa3b, v75
	v_max_f32_e32 v76, 0xc2a00000, v76
	v_exp_f32_e32 v75, v75
	v_mul_f32_e32 v76, 0xbfb8aa3b, v76
	v_exp_f32_e32 v76, v76
	v_add_f32_e32 v80, 1.0, v80
	v_add_f32_e32 v81, 1.0, v81
	v_rcp_f32_e32 v80, v80
	v_rcp_f32_e32 v81, v81
	v_mul_f32_e32 v66, v66, v82
	v_rcp_f32_e32 v74, v74
	v_add_f32_e32 v75, 1.0, v75
	v_max_f32_e32 v66, 0xc2a00000, v66
	v_rcp_f32_e32 v75, v75
	v_add_f32_e32 v76, 1.0, v76
	v_mul_f32_e32 v66, 0xbfb8aa3b, v66
	v_rcp_f32_e32 v76, v76
	v_exp_f32_e32 v66, v66
	v_fma_f32 v80, v178, v80, v138
	v_fma_f32 v81, v177, v81, v139
	v_log_f32_e32 v80, v80
	v_log_f32_e32 v81, v81
	v_fma_f32 v74, v170, v74, v133
	v_log_f32_e32 v77, v74
	v_fma_f32 v74, v169, v75, v134
	v_mul_f32_e32 v70, v70, v82
	v_mul_f32_e32 v67, v67, v82
	v_fma_f32 v85, v179, v87, v137
	v_log_f32_e32 v87, v74
	v_fma_f32 v74, v155, v76, v135
	v_max_f32_e32 v70, 0xc2a00000, v70
	v_add_f32_e32 v66, 1.0, v66
	v_max_f32_e32 v67, 0xc2a00000, v67
	v_log_f32_e32 v84, v84
	v_log_f32_e32 v85, v85
	v_log_f32_e32 v88, v74
	v_mul_f32_e32 v70, 0xbfb8aa3b, v70
	v_rcp_f32_e32 v66, v66
	v_mul_f32_e32 v67, 0xbfb8aa3b, v67
	v_cvt_pk_f16_f32 v75, v80, v81
	v_exp_f32_e32 v80, v70
	v_mul_f32_e32 v70, v71, v82
	v_exp_f32_e32 v67, v67
	v_max_f32_e32 v70, 0xc2a00000, v70
	v_lshl_add_u64 v[78:79], s[42:43], 0, v[78:79]
	v_mul_f32_e32 v70, 0xbfb8aa3b, v70
	v_cvt_pk_f16_f32 v74, v84, v85
	v_cvt_pk_f16_f32 v76, v86, v77
	v_cvt_pk_f16_f32 v77, v87, v88
	v_exp_f32_e32 v81, v70
	v_lshl_add_u64 v[70:71], v[78:79], 0, v[114:115]
	v_fma_f32 v66, v123, v66, v124
	ds_bpermute_b32 v238, v244, v74
	ds_bpermute_b32 v239, v244, v75
	ds_bpermute_b32 v240, v244, v76
	ds_bpermute_b32 v241, v244, v77
	ds_bpermute_b32 v242, v244, v70
	ds_bpermute_b32 v243, v244, v71
	s_waitcnt lgkmcnt(0)
	global_store_dwordx4 v[242:243], v[238:241], off
	v_mul_f32_e32 v72, v72, v82
	v_mul_f32_e32 v73, v73, v82
	v_log_f32_e32 v76, v66
	v_add_f32_e32 v66, 1.0, v67
	v_mul_f32_e32 v67, v68, v82
	v_max_f32_e32 v67, 0xc2a00000, v67
	v_mul_f32_e32 v68, v69, v82
	v_max_f32_e32 v72, 0xc2a00000, v72
	v_max_f32_e32 v73, 0xc2a00000, v73
	v_mul_f32_e32 v67, 0xbfb8aa3b, v67
	v_max_f32_e32 v68, 0xc2a00000, v68
	v_mul_f32_e32 v72, 0xbfb8aa3b, v72
	v_mul_f32_e32 v73, 0xbfb8aa3b, v73
	v_exp_f32_e32 v67, v67
	v_mul_f32_e32 v68, 0xbfb8aa3b, v68
	v_exp_f32_e32 v72, v72
	v_exp_f32_e32 v73, v73
	v_exp_f32_e32 v68, v68
	v_mul_f32_e32 v58, v58, v83
	v_rcp_f32_e32 v66, v66
	v_add_f32_e32 v67, 1.0, v67
	v_max_f32_e32 v58, 0xc2a00000, v58
	v_add_f32_e32 v78, 1.0, v80
	v_add_f32_e32 v79, 1.0, v81
	v_add_f32_e32 v72, 1.0, v72
	v_add_f32_e32 v73, 1.0, v73
	v_rcp_f32_e32 v67, v67
	v_add_f32_e32 v68, 1.0, v68
	v_mul_f32_e32 v58, 0xbfb8aa3b, v58
	v_rcp_f32_e32 v78, v78
	v_rcp_f32_e32 v79, v79
	v_rcp_f32_e32 v72, v72
	v_rcp_f32_e32 v73, v73
	v_rcp_f32_e32 v68, v68
	v_exp_f32_e32 v58, v58
	v_fma_f32 v66, v120, v66, v125
	v_log_f32_e32 v69, v66
	v_fma_f32 v66, v118, v67, v126
	v_mul_f32_e32 v59, v59, v83
	v_fma_f32 v74, v153, v78, v128
	v_fma_f32 v75, v168, v79, v129
	v_fma_f32 v72, v121, v72, v130
	v_fma_f32 v73, v122, v73, v131
	v_log_f32_e32 v77, v66
	v_fma_f32 v66, v119, v68, v127
	v_add_f32_e32 v58, 1.0, v58
	v_max_f32_e32 v59, 0xc2a00000, v59
	v_log_f32_e32 v74, v74
	v_log_f32_e32 v75, v75
	v_log_f32_e32 v72, v72
	v_log_f32_e32 v73, v73
	v_log_f32_e32 v78, v66
	v_rcp_f32_e32 v58, v58
	v_mul_f32_e32 v59, 0xbfb8aa3b, v59
	v_exp_f32_e32 v59, v59
	v_mul_f32_e32 v64, v64, v83
	v_mul_f32_e32 v65, v65, v83
	v_max_f32_e32 v64, 0xc2a00000, v64
	v_max_f32_e32 v65, 0xc2a00000, v65
	v_cvt_pk_f16_f32 v66, v74, v75
	v_cvt_pk_f16_f32 v67, v72, v73
	v_cvt_pk_f16_f32 v68, v76, v69
	v_mul_f32_e32 v62, v62, v83
	v_mul_f32_e32 v63, v63, v83
	v_cvt_pk_f16_f32 v69, v77, v78
	v_mul_f32_e32 v64, 0xbfb8aa3b, v64
	v_mul_f32_e32 v65, 0xbfb8aa3b, v65
	v_fma_f32 v58, v171, v58, v132
	v_max_f32_e32 v62, 0xc2a00000, v62
	v_max_f32_e32 v63, 0xc2a00000, v63
	ds_bpermute_b32 v232, v244, v66
	ds_bpermute_b32 v233, v244, v67
	ds_bpermute_b32 v234, v244, v68
	ds_bpermute_b32 v235, v244, v69
	ds_bpermute_b32 v236, v244, v70
	ds_bpermute_b32 v237, v244, v71
	s_waitcnt lgkmcnt(0)
	global_store_dwordx4 v[236:237], v[232:235], off offset:64
	v_exp_f32_e32 v64, v64
	v_exp_f32_e32 v65, v65
	v_log_f32_e32 v66, v58
	v_add_f32_e32 v58, 1.0, v59
	v_mul_f32_e32 v59, v60, v83
	v_mul_f32_e32 v62, 0xbfb8aa3b, v62
	v_mul_f32_e32 v63, 0xbfb8aa3b, v63
	v_max_f32_e32 v59, 0xc2a00000, v59
	v_mul_f32_e32 v60, v61, v83
	v_exp_f32_e32 v62, v62
	v_exp_f32_e32 v63, v63
	v_mul_f32_e32 v59, 0xbfb8aa3b, v59
	v_max_f32_e32 v60, 0xc2a00000, v60
	v_exp_f32_e32 v59, v59
	v_mul_f32_e32 v60, 0xbfb8aa3b, v60
	v_add_f32_e32 v64, 1.0, v64
	v_add_f32_e32 v65, 1.0, v65
	v_exp_f32_e32 v60, v60
	v_rcp_f32_e32 v64, v64
	v_rcp_f32_e32 v65, v65
	v_add_f32_e32 v62, 1.0, v62
	v_add_f32_e32 v63, 1.0, v63
	v_mul_f32_e32 v50, v50, v83
	v_rcp_f32_e32 v62, v62
	v_rcp_f32_e32 v63, v63
	v_rcp_f32_e32 v58, v58
	v_add_f32_e32 v59, 1.0, v59
	v_max_f32_e32 v50, 0xc2a00000, v50
	v_rcp_f32_e32 v59, v59
	v_add_f32_e32 v60, 1.0, v60
	v_mul_f32_e32 v50, 0xbfb8aa3b, v50
	v_fma_f32 v64, v178, v64, v138
	v_fma_f32 v65, v177, v65, v139
	v_rcp_f32_e32 v60, v60
	v_exp_f32_e32 v50, v50
	v_log_f32_e32 v64, v64
	v_log_f32_e32 v65, v65
	v_fma_f32 v62, v180, v62, v136
	v_fma_f32 v63, v179, v63, v137
	v_fma_f32 v58, v170, v58, v133
	v_mul_f32_e32 v54, v54, v83
	v_log_f32_e32 v62, v62
	v_log_f32_e32 v63, v63
	v_log_f32_e32 v61, v58
	v_fma_f32 v58, v169, v59, v134
	v_max_f32_e32 v54, 0xc2a00000, v54
	v_mul_f32_e32 v51, v51, v83
	v_log_f32_e32 v67, v58
	v_fma_f32 v58, v155, v60, v135
	v_mul_f32_e32 v54, 0xbfb8aa3b, v54
	v_add_f32_e32 v50, 1.0, v50
	v_max_f32_e32 v51, 0xc2a00000, v51
	v_log_f32_e32 v68, v58
	v_cvt_pk_f16_f32 v59, v64, v65
	v_exp_f32_e32 v64, v54
	v_mul_f32_e32 v54, v55, v83
	v_rcp_f32_e32 v50, v50
	v_mul_f32_e32 v51, 0xbfb8aa3b, v51
	v_max_f32_e32 v54, 0xc2a00000, v54
	v_exp_f32_e32 v51, v51
	v_cvt_pk_f16_f32 v58, v62, v63
	v_lshl_add_u64 v[62:63], v[166:167], 0, s[14:15]
	v_mul_f32_e32 v54, 0xbfb8aa3b, v54
	s_mov_b32 s14, 0x80000
	v_exp_f32_e32 v65, v54
	v_add_co_u32_e32 v54, vcc, s14, v166
	v_cvt_pk_f16_f32 v60, v66, v61
	v_cvt_pk_f16_f32 v61, v67, v68
	v_addc_co_u32_e32 v55, vcc, 0, v167, vcc
	v_fma_f32 v50, v123, v50, v124
	ds_bpermute_b32 v238, v244, v58
	ds_bpermute_b32 v239, v244, v59
	ds_bpermute_b32 v240, v244, v60
	ds_bpermute_b32 v241, v244, v61
	ds_bpermute_b32 v242, v244, v54
	ds_bpermute_b32 v243, v244, v55
	s_waitcnt lgkmcnt(0)
	global_store_dwordx4 v[242:243], v[238:241], off
	v_mul_f32_e32 v56, v56, v83
	v_mul_f32_e32 v57, v57, v83
	v_log_f32_e32 v58, v50
	v_add_f32_e32 v50, 1.0, v51
	v_mul_f32_e32 v51, v52, v83
	v_max_f32_e32 v51, 0xc2a00000, v51
	v_mul_f32_e32 v51, 0xbfb8aa3b, v51
	v_exp_f32_e32 v51, v51
	v_rcp_f32_e32 v50, v50
	v_mul_f32_e32 v52, v53, v83
	v_max_f32_e32 v56, 0xc2a00000, v56
	v_add_f32_e32 v51, 1.0, v51
	v_rcp_f32_e32 v51, v51
	v_fma_f32 v50, v120, v50, v125
	v_log_f32_e32 v59, v50
	v_max_f32_e32 v57, 0xc2a00000, v57
	v_fma_f32 v50, v118, v51, v126
	v_log_f32_e32 v60, v50
	ds_read2_b32 v[50:51], v176 offset0:144 offset1:160
	v_max_f32_e32 v52, 0xc2a00000, v52
	v_mul_f32_e32 v56, 0xbfb8aa3b, v56
	v_mul_f32_e32 v57, 0xbfb8aa3b, v57
	v_mul_f32_e32 v52, 0xbfb8aa3b, v52
	v_exp_f32_e32 v56, v56
	v_exp_f32_e32 v57, v57
	v_exp_f32_e32 v52, v52
	s_waitcnt lgkmcnt(0)
	v_mul_f32_e32 v42, v42, v50
	v_max_f32_e32 v42, 0xc2a00000, v42
	v_add_f32_e32 v64, 1.0, v64
	v_add_f32_e32 v65, 1.0, v65
	v_add_f32_e32 v56, 1.0, v56
	v_add_f32_e32 v57, 1.0, v57
	v_add_f32_e32 v52, 1.0, v52
	v_mul_f32_e32 v42, 0xbfb8aa3b, v42
	v_rcp_f32_e32 v64, v64
	v_rcp_f32_e32 v65, v65
	v_rcp_f32_e32 v56, v56
	v_rcp_f32_e32 v57, v57
	v_rcp_f32_e32 v52, v52
	v_exp_f32_e32 v42, v42
	v_mul_f32_e32 v43, v43, v50
	v_fma_f32 v54, v153, v64, v128
	v_fma_f32 v55, v168, v65, v129
	v_fma_f32 v56, v121, v56, v130
	v_fma_f32 v57, v122, v57, v131
	v_fma_f32 v52, v119, v52, v127
	v_add_f32_e32 v42, 1.0, v42
	v_max_f32_e32 v43, 0xc2a00000, v43
	v_log_f32_e32 v54, v54
	v_log_f32_e32 v55, v55
	v_log_f32_e32 v56, v56
	v_log_f32_e32 v57, v57
	v_log_f32_e32 v61, v52
	v_rcp_f32_e32 v42, v42
	v_mul_f32_e32 v43, 0xbfb8aa3b, v43
	v_exp_f32_e32 v43, v43
	v_mul_f32_e32 v48, v48, v50
	v_mul_f32_e32 v49, v49, v50
	v_max_f32_e32 v48, 0xc2a00000, v48
	v_max_f32_e32 v49, 0xc2a00000, v49
	v_cvt_pk_f16_f32 v52, v54, v55
	v_cvt_pk_f16_f32 v53, v56, v57
	v_cvt_pk_f16_f32 v54, v58, v59
	v_mul_f32_e32 v46, v46, v50
	v_mul_f32_e32 v47, v47, v50
	v_cvt_pk_f16_f32 v55, v60, v61
	v_mul_f32_e32 v48, 0xbfb8aa3b, v48
	v_mul_f32_e32 v49, 0xbfb8aa3b, v49
	v_fma_f32 v42, v171, v42, v132
	v_max_f32_e32 v46, 0xc2a00000, v46
	v_max_f32_e32 v47, 0xc2a00000, v47
	ds_bpermute_b32 v232, v244, v52
	ds_bpermute_b32 v233, v244, v53
	ds_bpermute_b32 v234, v244, v54
	ds_bpermute_b32 v235, v244, v55
	ds_bpermute_b32 v236, v244, v62
	ds_bpermute_b32 v237, v244, v63
	s_waitcnt lgkmcnt(0)
	global_store_dwordx4 v[236:237], v[232:235], off offset:64
	v_exp_f32_e32 v48, v48
	v_exp_f32_e32 v49, v49
	v_log_f32_e32 v52, v42
	v_add_f32_e32 v42, 1.0, v43
	v_mul_f32_e32 v43, v44, v50
	v_mul_f32_e32 v46, 0xbfb8aa3b, v46
	v_mul_f32_e32 v47, 0xbfb8aa3b, v47
	v_max_f32_e32 v43, 0xc2a00000, v43
	v_mul_f32_e32 v44, v45, v50
	v_exp_f32_e32 v46, v46
	v_exp_f32_e32 v47, v47
	v_mul_f32_e32 v43, 0xbfb8aa3b, v43
	v_max_f32_e32 v44, 0xc2a00000, v44
	v_exp_f32_e32 v43, v43
	v_mul_f32_e32 v44, 0xbfb8aa3b, v44
	v_add_f32_e32 v48, 1.0, v48
	v_add_f32_e32 v49, 1.0, v49
	v_exp_f32_e32 v44, v44
	v_rcp_f32_e32 v48, v48
	v_rcp_f32_e32 v49, v49
	v_add_f32_e32 v46, 1.0, v46
	v_add_f32_e32 v47, 1.0, v47
	v_mul_f32_e32 v34, v34, v50
	v_rcp_f32_e32 v46, v46
	v_rcp_f32_e32 v47, v47
	v_rcp_f32_e32 v42, v42
	v_add_f32_e32 v43, 1.0, v43
	v_max_f32_e32 v34, 0xc2a00000, v34
	v_rcp_f32_e32 v43, v43
	v_add_f32_e32 v44, 1.0, v44
	v_mul_f32_e32 v34, 0xbfb8aa3b, v34
	v_fma_f32 v48, v178, v48, v138
	v_fma_f32 v49, v177, v49, v139
	v_rcp_f32_e32 v44, v44
	v_exp_f32_e32 v34, v34
	v_log_f32_e32 v48, v48
	v_log_f32_e32 v49, v49
	v_fma_f32 v46, v180, v46, v136
	v_fma_f32 v47, v179, v47, v137
	v_fma_f32 v42, v170, v42, v133
	v_mul_f32_e32 v38, v38, v50
	v_log_f32_e32 v46, v46
	v_log_f32_e32 v47, v47
	v_log_f32_e32 v45, v42
	v_fma_f32 v42, v169, v43, v134
	v_max_f32_e32 v38, 0xc2a00000, v38
	v_mul_f32_e32 v35, v35, v50
	v_log_f32_e32 v53, v42
	v_fma_f32 v42, v155, v44, v135
	v_mul_f32_e32 v38, 0xbfb8aa3b, v38
	v_add_f32_e32 v34, 1.0, v34
	v_max_f32_e32 v35, 0xc2a00000, v35
	v_log_f32_e32 v54, v42
	v_cvt_pk_f16_f32 v43, v48, v49
	v_exp_f32_e32 v48, v38
	v_mul_f32_e32 v38, v39, v50
	v_rcp_f32_e32 v34, v34
	v_mul_f32_e32 v35, 0xbfb8aa3b, v35
	s_mov_b64 s[14:15], 0x90000
	v_max_f32_e32 v38, 0xc2a00000, v38
	v_exp_f32_e32 v35, v35
	v_cvt_pk_f16_f32 v42, v46, v47
	v_lshl_add_u64 v[46:47], v[166:167], 0, s[14:15]
	v_mul_f32_e32 v38, 0xbfb8aa3b, v38
	s_mov_b32 s14, 0x90000
	v_exp_f32_e32 v49, v38
	v_add_co_u32_e32 v38, vcc, s14, v166
	v_cvt_pk_f16_f32 v44, v52, v45
	v_cvt_pk_f16_f32 v45, v53, v54
	v_addc_co_u32_e32 v39, vcc, 0, v167, vcc
	v_fma_f32 v34, v123, v34, v124
	ds_bpermute_b32 v238, v244, v42
	ds_bpermute_b32 v239, v244, v43
	ds_bpermute_b32 v240, v244, v44
	ds_bpermute_b32 v241, v244, v45
	ds_bpermute_b32 v242, v244, v38
	ds_bpermute_b32 v243, v244, v39
	s_waitcnt lgkmcnt(0)
	global_store_dwordx4 v[242:243], v[238:241], off
	v_mul_f32_e32 v40, v40, v50
	v_mul_f32_e32 v41, v41, v50
	v_log_f32_e32 v42, v34
	v_add_f32_e32 v34, 1.0, v35
	v_mul_f32_e32 v35, v36, v50
	v_max_f32_e32 v35, 0xc2a00000, v35
	v_mul_f32_e32 v36, v37, v50
	v_max_f32_e32 v40, 0xc2a00000, v40
	v_max_f32_e32 v41, 0xc2a00000, v41
	v_mul_f32_e32 v35, 0xbfb8aa3b, v35
	v_max_f32_e32 v36, 0xc2a00000, v36
	v_mul_f32_e32 v40, 0xbfb8aa3b, v40
	v_mul_f32_e32 v41, 0xbfb8aa3b, v41
	v_exp_f32_e32 v35, v35
	v_mul_f32_e32 v36, 0xbfb8aa3b, v36
	v_exp_f32_e32 v40, v40
	v_exp_f32_e32 v41, v41
	v_exp_f32_e32 v36, v36
	v_mul_f32_e32 v26, v26, v51
	v_rcp_f32_e32 v34, v34
	v_add_f32_e32 v35, 1.0, v35
	v_max_f32_e32 v26, 0xc2a00000, v26
	v_add_f32_e32 v48, 1.0, v48
	v_add_f32_e32 v49, 1.0, v49
	v_add_f32_e32 v40, 1.0, v40
	v_add_f32_e32 v41, 1.0, v41
	v_rcp_f32_e32 v35, v35
	v_add_f32_e32 v36, 1.0, v36
	v_mul_f32_e32 v26, 0xbfb8aa3b, v26
	v_rcp_f32_e32 v48, v48
	v_rcp_f32_e32 v49, v49
	v_rcp_f32_e32 v40, v40
	v_rcp_f32_e32 v41, v41
	v_rcp_f32_e32 v36, v36
	v_exp_f32_e32 v26, v26
	v_fma_f32 v34, v120, v34, v125
	v_log_f32_e32 v37, v34
	v_fma_f32 v34, v118, v35, v126
	v_mul_f32_e32 v27, v27, v51
	v_fma_f32 v38, v153, v48, v128
	v_fma_f32 v39, v168, v49, v129
	v_fma_f32 v40, v121, v40, v130
	v_fma_f32 v41, v122, v41, v131
	v_log_f32_e32 v43, v34
	v_fma_f32 v34, v119, v36, v127
	v_add_f32_e32 v26, 1.0, v26
	v_max_f32_e32 v27, 0xc2a00000, v27
	v_log_f32_e32 v38, v38
	v_log_f32_e32 v39, v39
	v_log_f32_e32 v40, v40
	v_log_f32_e32 v41, v41
	v_log_f32_e32 v44, v34
	v_rcp_f32_e32 v26, v26
	v_mul_f32_e32 v27, 0xbfb8aa3b, v27
	v_exp_f32_e32 v27, v27
	v_mul_f32_e32 v32, v32, v51
	v_mul_f32_e32 v33, v33, v51
	v_max_f32_e32 v32, 0xc2a00000, v32
	v_max_f32_e32 v33, 0xc2a00000, v33
	v_cvt_pk_f16_f32 v34, v38, v39
	v_cvt_pk_f16_f32 v35, v40, v41
	v_cvt_pk_f16_f32 v36, v42, v37
	v_mul_f32_e32 v30, v30, v51
	v_mul_f32_e32 v31, v31, v51
	v_cvt_pk_f16_f32 v37, v43, v44
	v_mul_f32_e32 v32, 0xbfb8aa3b, v32
	v_mul_f32_e32 v33, 0xbfb8aa3b, v33
	v_fma_f32 v26, v171, v26, v132
	v_max_f32_e32 v30, 0xc2a00000, v30
	v_max_f32_e32 v31, 0xc2a00000, v31
	ds_bpermute_b32 v232, v244, v34
	ds_bpermute_b32 v233, v244, v35
	ds_bpermute_b32 v234, v244, v36
	ds_bpermute_b32 v235, v244, v37
	ds_bpermute_b32 v236, v244, v46
	ds_bpermute_b32 v237, v244, v47
	s_waitcnt lgkmcnt(0)
	global_store_dwordx4 v[236:237], v[232:235], off offset:64
	v_exp_f32_e32 v32, v32
	v_exp_f32_e32 v33, v33
	v_log_f32_e32 v34, v26
	v_add_f32_e32 v26, 1.0, v27
	v_mul_f32_e32 v27, v28, v51
	v_mul_f32_e32 v30, 0xbfb8aa3b, v30
	v_mul_f32_e32 v31, 0xbfb8aa3b, v31
	v_max_f32_e32 v27, 0xc2a00000, v27
	v_mul_f32_e32 v28, v29, v51
	v_exp_f32_e32 v30, v30
	v_exp_f32_e32 v31, v31
	v_mul_f32_e32 v27, 0xbfb8aa3b, v27
	v_max_f32_e32 v28, 0xc2a00000, v28
	v_exp_f32_e32 v27, v27
	v_mul_f32_e32 v28, 0xbfb8aa3b, v28
	v_add_f32_e32 v32, 1.0, v32
	v_add_f32_e32 v33, 1.0, v33
	v_exp_f32_e32 v28, v28
	v_rcp_f32_e32 v32, v32
	v_rcp_f32_e32 v33, v33
	v_add_f32_e32 v30, 1.0, v30
	v_add_f32_e32 v31, 1.0, v31
	v_mul_f32_e32 v18, v18, v51
	v_rcp_f32_e32 v30, v30
	v_rcp_f32_e32 v31, v31
	v_rcp_f32_e32 v26, v26
	v_add_f32_e32 v27, 1.0, v27
	v_max_f32_e32 v18, 0xc2a00000, v18
	v_rcp_f32_e32 v27, v27
	v_add_f32_e32 v28, 1.0, v28
	v_mul_f32_e32 v18, 0xbfb8aa3b, v18
	v_fma_f32 v32, v178, v32, v138
	v_fma_f32 v33, v177, v33, v139
	v_rcp_f32_e32 v28, v28
	v_exp_f32_e32 v18, v18
	v_log_f32_e32 v32, v32
	v_log_f32_e32 v33, v33
	v_fma_f32 v30, v180, v30, v136
	v_fma_f32 v31, v179, v31, v137
	v_fma_f32 v26, v170, v26, v133
	v_mul_f32_e32 v22, v22, v51
	v_log_f32_e32 v30, v30
	v_log_f32_e32 v31, v31
	v_log_f32_e32 v29, v26
	v_fma_f32 v26, v169, v27, v134
	v_max_f32_e32 v22, 0xc2a00000, v22
	v_mul_f32_e32 v19, v19, v51
	v_log_f32_e32 v35, v26
	v_fma_f32 v26, v155, v28, v135
	v_mul_f32_e32 v22, 0xbfb8aa3b, v22
	v_add_f32_e32 v18, 1.0, v18
	v_max_f32_e32 v19, 0xc2a00000, v19
	v_log_f32_e32 v36, v26
	v_cvt_pk_f16_f32 v27, v32, v33
	v_exp_f32_e32 v32, v22
	v_mul_f32_e32 v22, v23, v51
	v_rcp_f32_e32 v18, v18
	v_mul_f32_e32 v19, 0xbfb8aa3b, v19
	s_mov_b64 s[14:15], 0xa0000
	v_max_f32_e32 v22, 0xc2a00000, v22
	v_exp_f32_e32 v19, v19
	v_cvt_pk_f16_f32 v26, v30, v31
	v_lshl_add_u64 v[30:31], v[166:167], 0, s[14:15]
	v_mul_f32_e32 v22, 0xbfb8aa3b, v22
	s_mov_b32 s14, 0xa0000
	v_exp_f32_e32 v33, v22
	v_add_co_u32_e32 v22, vcc, s14, v166
	v_cvt_pk_f16_f32 v28, v34, v29
	v_cvt_pk_f16_f32 v29, v35, v36
	v_addc_co_u32_e32 v23, vcc, 0, v167, vcc
	v_fma_f32 v18, v123, v18, v124
	ds_bpermute_b32 v238, v244, v26
	ds_bpermute_b32 v239, v244, v27
	ds_bpermute_b32 v240, v244, v28
	ds_bpermute_b32 v241, v244, v29
	ds_bpermute_b32 v242, v244, v22
	ds_bpermute_b32 v243, v244, v23
	s_waitcnt lgkmcnt(0)
	global_store_dwordx4 v[242:243], v[238:241], off
	v_mul_f32_e32 v24, v24, v51
	v_mul_f32_e32 v25, v25, v51
	v_log_f32_e32 v26, v18
	v_add_f32_e32 v18, 1.0, v19
	v_mul_f32_e32 v19, v20, v51
	v_max_f32_e32 v19, 0xc2a00000, v19
	v_mul_f32_e32 v20, v21, v51
	ds_read_b32 v28, v176 offset:704
	v_max_f32_e32 v24, 0xc2a00000, v24
	v_max_f32_e32 v25, 0xc2a00000, v25
	v_mul_f32_e32 v19, 0xbfb8aa3b, v19
	v_max_f32_e32 v20, 0xc2a00000, v20
	v_mul_f32_e32 v24, 0xbfb8aa3b, v24
	v_mul_f32_e32 v25, 0xbfb8aa3b, v25
	v_exp_f32_e32 v19, v19
	v_mul_f32_e32 v20, 0xbfb8aa3b, v20
	v_exp_f32_e32 v24, v24
	v_exp_f32_e32 v25, v25
	v_exp_f32_e32 v20, v20
	s_waitcnt lgkmcnt(0)
	v_mul_f32_e32 v10, v10, v28
	v_rcp_f32_e32 v18, v18
	v_add_f32_e32 v19, 1.0, v19
	v_max_f32_e32 v10, 0xc2a00000, v10
	v_add_f32_e32 v32, 1.0, v32
	v_add_f32_e32 v33, 1.0, v33
	v_add_f32_e32 v24, 1.0, v24
	v_add_f32_e32 v25, 1.0, v25
	v_rcp_f32_e32 v19, v19
	v_add_f32_e32 v20, 1.0, v20
	v_mul_f32_e32 v10, 0xbfb8aa3b, v10
	v_rcp_f32_e32 v32, v32
	v_rcp_f32_e32 v33, v33
	v_rcp_f32_e32 v24, v24
	v_rcp_f32_e32 v25, v25
	v_rcp_f32_e32 v20, v20
	v_exp_f32_e32 v10, v10
	v_fma_f32 v18, v120, v18, v125
	v_log_f32_e32 v21, v18
	v_fma_f32 v18, v118, v19, v126
	v_mul_f32_e32 v11, v11, v28
	v_fma_f32 v22, v153, v32, v128
	v_fma_f32 v23, v168, v33, v129
	v_fma_f32 v24, v121, v24, v130
	v_fma_f32 v25, v122, v25, v131
	v_log_f32_e32 v27, v18
	v_fma_f32 v18, v119, v20, v127
	v_add_f32_e32 v10, 1.0, v10
	v_max_f32_e32 v11, 0xc2a00000, v11
	v_log_f32_e32 v22, v22
	v_log_f32_e32 v23, v23
	v_log_f32_e32 v24, v24
	v_log_f32_e32 v25, v25
	v_log_f32_e32 v29, v18
	v_rcp_f32_e32 v10, v10
	v_mul_f32_e32 v11, 0xbfb8aa3b, v11
	v_mul_f32_e32 v14, v14, v28
	v_mul_f32_e32 v15, v15, v28
	v_exp_f32_e32 v11, v11
	v_max_f32_e32 v14, 0xc2a00000, v14
	v_max_f32_e32 v15, 0xc2a00000, v15
	v_mul_f32_e32 v14, 0xbfb8aa3b, v14
	v_mul_f32_e32 v15, 0xbfb8aa3b, v15
	v_cvt_pk_f16_f32 v18, v22, v23
	v_cvt_pk_f16_f32 v19, v24, v25
	v_cvt_pk_f16_f32 v20, v26, v21
	v_exp_f32_e32 v14, v14
	v_exp_f32_e32 v15, v15
	v_cvt_pk_f16_f32 v21, v27, v29
	v_fma_f32 v10, v171, v10, v132
	ds_bpermute_b32 v232, v244, v18
	ds_bpermute_b32 v233, v244, v19
	ds_bpermute_b32 v234, v244, v20
	ds_bpermute_b32 v235, v244, v21
	ds_bpermute_b32 v236, v244, v30
	ds_bpermute_b32 v237, v244, v31
	s_waitcnt lgkmcnt(0)
	global_store_dwordx4 v[236:237], v[232:235], off offset:64
	v_add_f32_e32 v14, 1.0, v14
	v_add_f32_e32 v15, 1.0, v15
	v_log_f32_e32 v18, v10
	v_add_f32_e32 v10, 1.0, v11
	v_mul_f32_e32 v11, v12, v28
	v_max_f32_e32 v11, 0xc2a00000, v11
	v_mul_f32_e32 v11, 0xbfb8aa3b, v11
	v_exp_f32_e32 v11, v11
	v_rcp_f32_e32 v14, v14
	v_rcp_f32_e32 v15, v15
	v_mul_f32_e32 v16, v16, v28
	v_mul_f32_e32 v17, v17, v28
	v_rcp_f32_e32 v10, v10
	v_mul_f32_e32 v12, v13, v28
	v_add_f32_e32 v11, 1.0, v11
	v_fma_f32 v14, v180, v14, v136
	v_fma_f32 v15, v179, v15, v137
	v_max_f32_e32 v16, 0xc2a00000, v16
	v_max_f32_e32 v17, 0xc2a00000, v17
	v_max_f32_e32 v12, 0xc2a00000, v12
	v_rcp_f32_e32 v11, v11
	v_log_f32_e32 v14, v14
	v_mul_f32_e32 v16, 0xbfb8aa3b, v16
	v_mul_f32_e32 v17, 0xbfb8aa3b, v17
	v_log_f32_e32 v15, v15
	v_mul_f32_e32 v12, 0xbfb8aa3b, v12
	v_exp_f32_e32 v16, v16
	v_exp_f32_e32 v17, v17
	v_exp_f32_e32 v12, v12
	v_mul_f32_e32 v6, v6, v28
	v_fma_f32 v10, v170, v10, v133
	v_max_f32_e32 v6, 0xc2a00000, v6
	v_log_f32_e32 v13, v10
	v_fma_f32 v10, v169, v11, v134
	v_mul_f32_e32 v6, 0xbfb8aa3b, v6
	v_log_f32_e32 v19, v10
	v_cvt_pk_f16_f32 v10, v14, v15
	v_exp_f32_e32 v14, v6
	v_mul_f32_e32 v6, v7, v28
	v_mul_f32_e32 v8, v8, v28
	v_mul_f32_e32 v9, v9, v28
	v_mul_f32_e32 v2, v2, v28
	v_mul_f32_e32 v3, v3, v28
	v_mul_f32_e32 v4, v4, v28
	v_mul_f32_e32 v5, v5, v28
	v_add_f32_e32 v16, 1.0, v16
	v_add_f32_e32 v17, 1.0, v17
	v_add_f32_e32 v12, 1.0, v12
	v_max_f32_e32 v6, 0xc2a00000, v6
	v_max_f32_e32 v8, 0xc2a00000, v8
	v_max_f32_e32 v9, 0xc2a00000, v9
	v_max_f32_e32 v2, 0xc2a00000, v2
	v_max_f32_e32 v3, 0xc2a00000, v3
	v_max_f32_e32 v4, 0xc2a00000, v4
	v_max_f32_e32 v5, 0xc2a00000, v5
	v_rcp_f32_e32 v16, v16
	v_rcp_f32_e32 v17, v17
	v_rcp_f32_e32 v12, v12
	v_mul_f32_e32 v6, 0xbfb8aa3b, v6
	v_mul_f32_e32 v8, 0xbfb8aa3b, v8
	v_mul_f32_e32 v9, 0xbfb8aa3b, v9
	v_mul_f32_e32 v2, 0xbfb8aa3b, v2
	v_mul_f32_e32 v3, 0xbfb8aa3b, v3
	v_mul_f32_e32 v4, 0xbfb8aa3b, v4
	v_mul_f32_e32 v5, 0xbfb8aa3b, v5
	v_exp_f32_e32 v15, v6
	v_exp_f32_e32 v8, v8
	v_exp_f32_e32 v9, v9
	v_exp_f32_e32 v2, v2
	v_exp_f32_e32 v3, v3
	v_exp_f32_e32 v4, v4
	v_exp_f32_e32 v5, v5
	v_fma_f32 v16, v178, v16, v138
	v_fmac_f32_e32 v139, v177, v17
	v_fmac_f32_e32 v135, v155, v12
	v_log_f32_e32 v16, v16
	v_log_f32_e32 v17, v139
	v_log_f32_e32 v20, v135
	v_add_f32_e32 v14, 1.0, v14
	v_add_f32_e32 v15, 1.0, v15
	v_add_f32_e32 v8, 1.0, v8
	v_add_f32_e32 v9, 1.0, v9
	v_add_f32_e32 v2, 1.0, v2
	v_add_f32_e32 v3, 1.0, v3
	v_add_f32_e32 v4, 1.0, v4
	v_add_f32_e32 v5, 1.0, v5
	s_mov_b64 s[14:15], 0xb0000
	v_rcp_f32_e32 v14, v14
	v_rcp_f32_e32 v15, v15
	v_rcp_f32_e32 v8, v8
	v_rcp_f32_e32 v9, v9
	v_rcp_f32_e32 v2, v2
	v_rcp_f32_e32 v3, v3
	v_rcp_f32_e32 v4, v4
	v_rcp_f32_e32 v5, v5
	v_lshl_add_u64 v[136:137], v[166:167], 0, s[14:15]
	s_mov_b32 s14, 0xb0000
	v_add_co_u32_e32 v6, vcc, s14, v166
	v_cvt_pk_f16_f32 v11, v16, v17
	v_cvt_pk_f16_f32 v12, v18, v13
	v_cvt_pk_f16_f32 v13, v19, v20
	v_addc_co_u32_e32 v7, vcc, 0, v167, vcc
	ds_bpermute_b32 v238, v244, v10
	ds_bpermute_b32 v239, v244, v11
	ds_bpermute_b32 v240, v244, v12
	ds_bpermute_b32 v241, v244, v13
	ds_bpermute_b32 v242, v244, v6
	ds_bpermute_b32 v243, v244, v7
	s_waitcnt lgkmcnt(0)
	global_store_dwordx4 v[242:243], v[238:241], off
	v_fma_f32 v6, v153, v14, v128
	v_fma_f32 v7, v168, v15, v129
	v_fma_f32 v8, v121, v8, v130
	v_fmac_f32_e32 v131, v122, v9
	v_fma_f32 v2, v123, v2, v124
	v_fma_f32 v3, v120, v3, v125
	v_fma_f32 v4, v118, v4, v126
	v_fmac_f32_e32 v127, v119, v5
	v_log_f32_e32 v6, v6
	v_log_f32_e32 v7, v7
	v_log_f32_e32 v8, v8
	v_log_f32_e32 v9, v131
	v_log_f32_e32 v2, v2
	v_log_f32_e32 v3, v3
	v_log_f32_e32 v4, v4
	v_log_f32_e32 v5, v127
	v_cvt_pk_f16_f32 v196, v181, v182
	v_cvt_pk_f16_f32 v132, v6, v7
	v_cvt_pk_f16_f32 v133, v8, v9
	v_cvt_pk_f16_f32 v134, v2, v3
	v_cvt_pk_f16_f32 v135, v4, v5
	ds_bpermute_b32 v232, v244, v194
	ds_bpermute_b32 v233, v244, v195
	ds_bpermute_b32 v234, v244, v196
	ds_bpermute_b32 v235, v244, v197
	ds_bpermute_b32 v236, v244, v166
	ds_bpermute_b32 v237, v244, v167
	s_waitcnt lgkmcnt(0)
	global_store_dwordx4 v[236:237], v[232:235], off offset:64
	s_andn2_b64 vcc, exec, s[38:39]
	s_mov_b64 s[28:29], -1
	ds_bpermute_b32 v238, v244, v132
	ds_bpermute_b32 v239, v244, v133
	ds_bpermute_b32 v240, v244, v134
	ds_bpermute_b32 v241, v244, v135
	ds_bpermute_b32 v242, v244, v136
	ds_bpermute_b32 v243, v244, v137
	s_waitcnt lgkmcnt(0)
	global_store_dwordx4 v[242:243], v[238:241], off offset:64
	s_cbranch_vccnz .LBB0_338

.LBB0_506:
	v_mbcnt_lo_u32_b32 v244, -1, 0
	v_mbcnt_hi_u32_b32 v244, -1, v244
	v_lshrrev_b32_e32 v245, 2, v244
	v_and_b32_e32 v244, 3, v244
	v_lshl_add_u32 v244, v244, 4, v245
	v_lshlrev_b32_e32 v244, 2, v244
	s_lshl_b32 s14, s14, 10
	v_add_u32_e32 v176, s14, v174
	ds_read_b32 v154, v176
	s_lshl_b32 s15, s28, 8
	s_ashr_i32 s56, s28, 3
	s_and_b32 s14, s15, 0x700
	v_lshl_add_u32 v152, s40, 8, v1
	v_or_b32_e32 v177, s14, v173
	s_cmp_lg_u32 s56, 1
	s_mov_b64 s[40:41], -1
	s_cbranch_scc0 .LBB0_541
	s_cmp_lt_u32 s28, 8
	s_cselect_b64 s[54:55], -1, 0
	s_cmp_gt_u32 s28, 7
	s_waitcnt lgkmcnt(0)
	v_pk_mul_f32 v[134:135], v[130:131], v[154:155] op_sel_hi:[1,0]
	v_pk_mul_f32 v[166:167], v[128:129], v[154:155] op_sel_hi:[1,0]
	v_pk_mul_f32 v[138:139], v[126:127], v[154:155] op_sel_hi:[1,0]
	v_pk_mul_f32 v[168:169], v[124:125], v[154:155] op_sel_hi:[1,0]
	s_cbranch_scc1 .LBB0_509
	v_max_f32_e32 v114, v166, v166
	v_max_f32_e32 v132, 0xc2a00000, v114
	v_max_f32_e32 v114, v168, v168
	v_max_f32_e32 v136, 0xc2a00000, v114
	v_mul_f32_e32 v114, 0xbfb8aa3b, v132
	v_exp_f32_e32 v114, v114
	v_mul_f32_e32 v133, 0xbfb8aa3b, v136
	v_exp_f32_e32 v133, v133
	v_max_f32_e32 v137, v169, v169
	v_add_f32_e32 v114, 1.0, v114
	v_rcp_f32_e32 v158, v114
	v_add_f32_e32 v114, 1.0, v133
	v_max_f32_e32 v133, v167, v167
	v_max_f32_e32 v133, 0xc2a00000, v133
	v_max_f32_e32 v137, 0xc2a00000, v137
	v_mul_f32_e32 v153, 0xbfb8aa3b, v133
	v_exp_f32_e32 v153, v153
	v_mul_f32_e32 v155, 0xbfb8aa3b, v137
	v_exp_f32_e32 v155, v155
	v_max_f32_e32 v134, v134, v134
	v_max_f32_e32 v134, 0xc2a00000, v134
	v_max_f32_e32 v138, v138, v138
	v_rcp_f32_e32 v160, v114
	v_add_f32_e32 v114, 1.0, v153
	v_max_f32_e32 v138, 0xc2a00000, v138
	v_mul_f32_e32 v153, 0xbfb8aa3b, v134
	v_rcp_f32_e32 v159, v114
	v_add_f32_e32 v114, 1.0, v155
	v_exp_f32_e32 v153, v153
	v_mul_f32_e32 v155, 0xbfb8aa3b, v138
	v_exp_f32_e32 v155, v155
	v_max_f32_e32 v135, v135, v135
	v_max_f32_e32 v135, 0xc2a00000, v135
	v_max_f32_e32 v139, v139, v139
	v_rcp_f32_e32 v161, v114
	v_add_f32_e32 v114, 1.0, v153
	v_max_f32_e32 v139, 0xc2a00000, v139
	v_mul_f32_e32 v153, 0xbfb8aa3b, v135
	v_rcp_f32_e32 v168, v114
	v_add_f32_e32 v114, 1.0, v155
	v_exp_f32_e32 v153, v153
	v_mul_f32_e32 v155, 0xbfb8aa3b, v139
	v_exp_f32_e32 v155, v155
	v_rcp_f32_e32 v170, v114
	v_add_f32_e32 v114, 1.0, v153
	v_rcp_f32_e32 v169, v114
	v_add_f32_e32 v114, 1.0, v155
	v_rcp_f32_e32 v171, v114
	v_pk_mul_f32 v[166:167], v[132:133], v[158:159]
	v_pk_mul_f32 v[134:135], v[134:135], v[168:169]
	v_pk_mul_f32 v[168:169], v[136:137], v[160:161]
	v_pk_mul_f32 v[138:139], v[138:139], v[170:171]
.LBB0_509:
	s_ashr_i32 s57, s56, 31
	s_lshl_b64 s[14:15], s[56:57], 25
	s_add_u32 s14, s24, s14
	s_addc_u32 s15, s37, s15
	v_lshlrev_b32_e32 v114, 1, v177
	v_ashrrev_i32_e32 v153, 31, v152
	v_lshl_add_u64 v[132:133], s[14:15], 0, v[114:115]
	v_lshlrev_b64 v[136:137], 12, v[152:153]
	v_mov_b32_e32 v155, v154
	v_lshl_add_u64 v[136:137], v[132:133], 0, v[136:137]
	v_cvt_pk_bf16_f32 v166, v166, v167
	v_cvt_pk_bf16_f32 v167, v134, v135
	v_cvt_pk_bf16_f32 v168, v168, v169
	v_cvt_pk_bf16_f32 v169, v138, v139
	v_mov_b32_e32 v158, v154
	v_mov_b32_e32 v159, v154
	v_cndmask_b32_e64 v114, 0, 1, s[54:55]
	ds_bpermute_b32 v232, v244, v166
	ds_bpermute_b32 v233, v244, v167
	ds_bpermute_b32 v234, v244, v168
	ds_bpermute_b32 v235, v244, v169
	ds_bpermute_b32 v236, v244, v136
	ds_bpermute_b32 v237, v244, v137
	s_waitcnt lgkmcnt(0)
	global_store_dwordx4 v[236:237], v[232:235], off
	v_pk_mul_f32 v[138:139], v[122:123], v[158:159]
	v_pk_mul_f32 v[134:135], v[120:121], v[154:155]
	v_pk_mul_f32 v[166:167], v[118:119], v[158:159]
	v_cmp_ne_u32_e64 s[40:41], 1, v114
	s_andn2_b64 vcc, exec, s[54:55]
	v_pk_mul_f32 v[168:169], v[116:117], v[154:155]
	s_cbranch_vccnz .LBB0_511
	v_max_f32_e32 v114, v134, v134
	v_max_f32_e32 v134, 0xc2a00000, v114
	v_max_f32_e32 v114, v168, v168
	v_max_f32_e32 v158, 0xc2a00000, v114
	v_mul_f32_e32 v114, 0xbfb8aa3b, v134
	v_exp_f32_e32 v114, v114
	v_mul_f32_e32 v155, 0xbfb8aa3b, v158
	v_exp_f32_e32 v155, v155
	v_max_f32_e32 v135, v135, v135
	v_add_f32_e32 v114, 1.0, v114
	v_rcp_f32_e32 v160, v114
	v_add_f32_e32 v114, 1.0, v155
	v_max_f32_e32 v135, 0xc2a00000, v135
	v_max_f32_e32 v155, v169, v169
	v_max_f32_e32 v159, 0xc2a00000, v155
	v_mul_f32_e32 v155, 0xbfb8aa3b, v135
	v_exp_f32_e32 v155, v155
	v_mul_f32_e32 v161, 0xbfb8aa3b, v159
	v_exp_f32_e32 v169, v161
	v_max_f32_e32 v138, v138, v138
	v_rcp_f32_e32 v168, v114
	v_add_f32_e32 v114, 1.0, v155
	v_max_f32_e32 v138, 0xc2a00000, v138
	v_max_f32_e32 v155, v166, v166
	v_max_f32_e32 v166, 0xc2a00000, v155
	v_mul_f32_e32 v155, 0xbfb8aa3b, v138
	v_exp_f32_e32 v155, v155
	v_rcp_f32_e32 v161, v114
	v_add_f32_e32 v114, 1.0, v169
	v_mul_f32_e32 v169, 0xbfb8aa3b, v166
	v_exp_f32_e32 v171, v169
	v_max_f32_e32 v139, v139, v139
	v_rcp_f32_e32 v169, v114
	v_add_f32_e32 v114, 1.0, v155
	v_max_f32_e32 v139, 0xc2a00000, v139
	v_max_f32_e32 v155, v167, v167
	v_max_f32_e32 v167, 0xc2a00000, v155
	v_mul_f32_e32 v155, 0xbfb8aa3b, v139
	v_rcp_f32_e32 v170, v114
	v_add_f32_e32 v114, 1.0, v171
	v_exp_f32_e32 v155, v155
	v_mul_f32_e32 v171, 0xbfb8aa3b, v167
	v_exp_f32_e32 v179, v171
	v_rcp_f32_e32 v178, v114
	v_add_f32_e32 v114, 1.0, v155
	v_rcp_f32_e32 v171, v114
	v_add_f32_e32 v114, 1.0, v179
	v_rcp_f32_e32 v179, v114
	v_pk_mul_f32 v[134:135], v[134:135], v[160:161]
	v_pk_mul_f32 v[138:139], v[138:139], v[170:171]
	v_pk_mul_f32 v[168:169], v[158:159], v[168:169]
	v_pk_mul_f32 v[166:167], v[166:167], v[178:179]

.LBB0_541:
	s_and_b64 vcc, exec, s[40:41]
	s_cbranch_vccz .LBB0_540
	v_lshlrev_b32_e32 v155, 2, v177
	global_load_dwordx4 v[136:139], v155, s[42:43]
	global_load_dwordx4 v[132:135], v155, s[42:43] offset:16
	s_waitcnt lgkmcnt(0)
	v_mul_f32_e32 v160, v128, v154
	v_mul_f32_e32 v161, v129, v154
	v_mul_f32_e32 v166, v130, v154
	v_mul_f32_e32 v167, v131, v154
	v_mul_f32_e32 v168, v124, v154
	v_mul_f32_e32 v169, v125, v154
	v_mul_f32_e32 v170, v126, v154
	v_mul_f32_e32 v171, v127, v154
	global_load_dwordx4 v[124:127], v155, s[42:43] offset:144
	global_load_dwordx4 v[128:131], v155, s[42:43] offset:128
	v_ashrrev_i32_e32 v153, 31, v152
	v_lshlrev_b64 v[158:159], 12, v[152:153]
	v_max_f32_e32 v153, 0xc2a00000, v160
	v_max_f32_e32 v155, 0xc2a00000, v161
	v_max_f32_e32 v160, 0xc2a00000, v166
	v_max_f32_e32 v161, 0xc2a00000, v167
	v_max_f32_e32 v166, 0xc2a00000, v168
	v_max_f32_e32 v167, 0xc2a00000, v169
	v_max_f32_e32 v168, 0xc2a00000, v170
	v_max_f32_e32 v169, 0xc2a00000, v171
	v_mul_f32_e32 v153, 0xbfb8aa3b, v153
	v_mul_f32_e32 v155, 0xbfb8aa3b, v155
	v_mul_f32_e32 v168, 0xbfb8aa3b, v168
	v_mul_f32_e32 v169, 0xbfb8aa3b, v169
	v_exp_f32_e32 v153, v153
	v_exp_f32_e32 v155, v155
	v_mul_f32_e32 v160, 0xbfb8aa3b, v160
	v_mul_f32_e32 v161, 0xbfb8aa3b, v161
	v_exp_f32_e32 v168, v168
	v_exp_f32_e32 v169, v169
	v_exp_f32_e32 v160, v160
	v_exp_f32_e32 v161, v161
	v_mul_f32_e32 v120, v120, v154
	v_max_f32_e32 v120, 0xc2a00000, v120
	v_add_f32_e32 v153, 1.0, v153
	v_add_f32_e32 v155, 1.0, v155
	v_mul_f32_e32 v121, v121, v154
	v_lshlrev_b32_e32 v114, 1, v177
	v_mul_f32_e32 v166, 0xbfb8aa3b, v166
	v_mul_f32_e32 v167, 0xbfb8aa3b, v167
	v_lshl_add_u64 v[158:159], s[26:27], 0, v[158:159]
	v_add_f32_e32 v168, 1.0, v168
	v_add_f32_e32 v169, 1.0, v169
	v_rcp_f32_e32 v153, v153
	v_rcp_f32_e32 v181, v155
	v_mul_f32_e32 v120, 0xbfb8aa3b, v120
	v_max_f32_e32 v121, 0xc2a00000, v121
	v_exp_f32_e32 v170, v166
	v_exp_f32_e32 v171, v167
	v_lshl_add_u64 v[166:167], v[158:159], 0, v[114:115]
	v_add_f32_e32 v158, 1.0, v160
	v_add_f32_e32 v159, 1.0, v161
	v_rcp_f32_e32 v168, v168
	v_rcp_f32_e32 v182, v169
	v_exp_f32_e32 v120, v120
	v_mul_f32_e32 v121, 0xbfb8aa3b, v121
	v_rcp_f32_e32 v158, v158
	v_rcp_f32_e32 v159, v159
	v_exp_f32_e32 v121, v121
	v_add_f32_e32 v120, 1.0, v120
	v_rcp_f32_e32 v120, v120
	v_mul_f32_e32 v116, v116, v154
	v_add_f32_e32 v121, 1.0, v121
	v_rcp_f32_e32 v121, v121
	v_add_f32_e32 v160, 1.0, v170
	v_add_f32_e32 v161, 1.0, v171
	v_max_f32_e32 v116, 0xc2a00000, v116
	v_mul_f32_e32 v117, v117, v154
	v_rcp_f32_e32 v160, v160
	v_rcp_f32_e32 v161, v161
	v_mul_f32_e32 v116, 0xbfb8aa3b, v116
	v_max_f32_e32 v117, 0xc2a00000, v117
	v_exp_f32_e32 v116, v116
	v_mul_f32_e32 v117, 0xbfb8aa3b, v117
	v_exp_f32_e32 v117, v117
	s_mov_b64 s[14:15], 0x80000
	v_add_f32_e32 v116, 1.0, v116
	v_rcp_f32_e32 v116, v116
	v_add_f32_e32 v117, 1.0, v117
	s_waitcnt vmcnt(0)
	v_sub_f32_e32 v180, 1.0, v136
	v_sub_f32_e32 v179, 1.0, v137
	v_sub_f32_e32 v169, 1.0, v134
	v_sub_f32_e32 v155, 1.0, v135
	v_fma_f32 v153, v180, v153, v136
	v_fma_f32 v181, v179, v181, v137
	v_sub_f32_e32 v178, 1.0, v138
	v_sub_f32_e32 v177, 1.0, v139
	v_fma_f32 v168, v169, v168, v134
	v_fma_f32 v182, v155, v182, v135
	v_log_f32_e32 v153, v153
	v_log_f32_e32 v181, v181
	v_fma_f32 v158, v178, v158, v138
	v_fma_f32 v159, v177, v159, v139
	v_log_f32_e32 v168, v168
	v_log_f32_e32 v182, v182
	v_log_f32_e32 v158, v158
	v_log_f32_e32 v159, v159
	v_cvt_pk_f16_f32 v194, v153, v181
	v_sub_f32_e32 v153, 1.0, v128
	v_cvt_pk_f16_f32 v197, v168, v182
	v_fma_f32 v120, v153, v120, v128
	v_sub_f32_e32 v168, 1.0, v129
	v_cvt_pk_f16_f32 v195, v158, v159
	v_log_f32_e32 v158, v120
	v_fma_f32 v120, v168, v121, v129
	v_log_f32_e32 v159, v120
	v_mul_f32_e32 v120, v122, v154
	v_max_f32_e32 v120, 0xc2a00000, v120
	v_mul_f32_e32 v121, v123, v154
	v_mul_f32_e32 v120, 0xbfb8aa3b, v120
	v_max_f32_e32 v121, 0xc2a00000, v121
	v_exp_f32_e32 v120, v120
	v_mul_f32_e32 v121, 0xbfb8aa3b, v121
	v_exp_f32_e32 v122, v121
	v_sub_f32_e32 v171, 1.0, v132
	v_sub_f32_e32 v170, 1.0, v133
	v_add_f32_e32 v120, 1.0, v120
	v_fma_f32 v160, v171, v160, v132
	v_fma_f32 v161, v170, v161, v133
	v_rcp_f32_e32 v120, v120
	v_add_f32_e32 v122, 1.0, v122
	v_log_f32_e32 v160, v160
	v_log_f32_e32 v161, v161
	v_rcp_f32_e32 v123, v122
	v_sub_f32_e32 v121, 1.0, v130
	v_rcp_f32_e32 v117, v117
	v_fma_f32 v120, v121, v120, v130
	v_sub_f32_e32 v122, 1.0, v131
	v_cvt_pk_f16_f32 v196, v160, v161
	v_log_f32_e32 v160, v120
	v_fma_f32 v120, v122, v123, v131
	v_sub_f32_e32 v123, 1.0, v124
	v_log_f32_e32 v161, v120
	v_fma_f32 v116, v123, v116, v124
	v_sub_f32_e32 v120, 1.0, v125
	v_log_f32_e32 v181, v116
	v_fma_f32 v116, v120, v117, v125
	v_log_f32_e32 v182, v116
	v_mul_f32_e32 v116, v118, v154
	v_max_f32_e32 v116, 0xc2a00000, v116
	v_mul_f32_e32 v117, v119, v154
	v_mul_f32_e32 v116, 0xbfb8aa3b, v116
	v_max_f32_e32 v117, 0xc2a00000, v117
	v_exp_f32_e32 v116, v116
	v_mul_f32_e32 v117, 0xbfb8aa3b, v117
	v_exp_f32_e32 v117, v117
	v_sub_f32_e32 v118, 1.0, v126
	v_add_f32_e32 v116, 1.0, v116
	v_rcp_f32_e32 v116, v116
	v_add_f32_e32 v117, 1.0, v117
	v_rcp_f32_e32 v117, v117
	v_sub_f32_e32 v119, 1.0, v127
	v_fma_f32 v116, v118, v116, v126
	v_log_f32_e32 v154, v116
	v_fma_f32 v116, v119, v117, v127
	v_log_f32_e32 v183, v116
	ds_read2_b32 v[116:117], v176 offset0:16 offset1:32
	ds_bpermute_b32 v232, v244, v194
	ds_bpermute_b32 v233, v244, v195
	ds_bpermute_b32 v234, v244, v196
	ds_bpermute_b32 v235, v244, v197
	ds_bpermute_b32 v236, v244, v166
	ds_bpermute_b32 v237, v244, v167
	s_waitcnt lgkmcnt(0)
	global_store_dwordx4 v[236:237], v[232:235], off
	s_waitcnt lgkmcnt(0)
	v_mul_f32_e32 v106, v106, v116
	v_max_f32_e32 v106, 0xc2a00000, v106
	v_mul_f32_e32 v106, 0xbfb8aa3b, v106
	v_exp_f32_e32 v106, v106
	v_mul_f32_e32 v110, v110, v116
	v_max_f32_e32 v110, 0xc2a00000, v110
	v_mul_f32_e32 v111, v111, v116
	v_mul_f32_e32 v110, 0xbfb8aa3b, v110
	v_max_f32_e32 v111, 0xc2a00000, v111
	v_mul_f32_e32 v107, v107, v116
	v_exp_f32_e32 v110, v110
	v_mul_f32_e32 v111, 0xbfb8aa3b, v111
	v_add_f32_e32 v106, 1.0, v106
	v_max_f32_e32 v107, 0xc2a00000, v107
	v_exp_f32_e32 v111, v111
	v_rcp_f32_e32 v106, v106
	v_mul_f32_e32 v107, 0xbfb8aa3b, v107
	v_exp_f32_e32 v107, v107
	v_cvt_pk_f16_f32 v194, v158, v159
	v_or_b32_e32 v158, 16, v152
	v_add_f32_e32 v110, 1.0, v110
	v_mul_f32_e32 v112, v112, v116
	v_mul_f32_e32 v113, v113, v116
	v_cvt_pk_f16_f32 v197, v154, v183
	v_ashrrev_i32_e32 v159, 31, v158
	v_rcp_f32_e32 v154, v110
	v_add_f32_e32 v110, 1.0, v111
	v_max_f32_e32 v112, 0xc2a00000, v112
	v_max_f32_e32 v113, 0xc2a00000, v113
	v_fma_f32 v106, v171, v106, v132
	v_cvt_pk_f16_f32 v195, v160, v161
	v_rcp_f32_e32 v160, v110
	v_lshlrev_b64 v[110:111], 12, v[158:159]
	v_mul_f32_e32 v112, 0xbfb8aa3b, v112
	v_mul_f32_e32 v113, 0xbfb8aa3b, v113
	v_log_f32_e32 v159, v106
	v_add_f32_e32 v106, 1.0, v107
	v_mul_f32_e32 v107, v108, v116
	v_exp_f32_e32 v112, v112
	v_exp_f32_e32 v113, v113
	v_max_f32_e32 v107, 0xc2a00000, v107
	v_mul_f32_e32 v108, v109, v116
	v_mul_f32_e32 v107, 0xbfb8aa3b, v107
	v_max_f32_e32 v108, 0xc2a00000, v108
	v_exp_f32_e32 v107, v107
	v_mul_f32_e32 v108, 0xbfb8aa3b, v108
	v_exp_f32_e32 v108, v108
	v_add_f32_e32 v112, 1.0, v112
	v_add_f32_e32 v113, 1.0, v113
	v_rcp_f32_e32 v112, v112
	v_rcp_f32_e32 v113, v113
	v_mul_f32_e32 v98, v98, v116
	v_rcp_f32_e32 v106, v106
	v_add_f32_e32 v107, 1.0, v107
	v_max_f32_e32 v98, 0xc2a00000, v98
	v_rcp_f32_e32 v107, v107
	v_add_f32_e32 v108, 1.0, v108
	v_mul_f32_e32 v98, 0xbfb8aa3b, v98
	v_rcp_f32_e32 v108, v108
	v_exp_f32_e32 v98, v98
	v_fma_f32 v112, v178, v112, v138
	v_fma_f32 v113, v177, v113, v139
	v_log_f32_e32 v112, v112
	v_log_f32_e32 v113, v113
	v_fma_f32 v106, v170, v106, v133
	v_log_f32_e32 v109, v106
	v_fma_f32 v106, v169, v107, v134
	v_mul_f32_e32 v102, v102, v116
	v_mul_f32_e32 v99, v99, v116
	v_fma_f32 v154, v180, v154, v136
	v_fma_f32 v158, v179, v160, v137
	v_log_f32_e32 v160, v106
	v_fma_f32 v106, v155, v108, v135
	v_max_f32_e32 v102, 0xc2a00000, v102
	v_add_f32_e32 v98, 1.0, v98
	v_max_f32_e32 v99, 0xc2a00000, v99
	v_log_f32_e32 v154, v154
	v_log_f32_e32 v158, v158
	v_log_f32_e32 v161, v106
	v_mul_f32_e32 v102, 0xbfb8aa3b, v102
	v_rcp_f32_e32 v98, v98
	v_mul_f32_e32 v99, 0xbfb8aa3b, v99
	v_cvt_pk_f16_f32 v107, v112, v113
	v_exp_f32_e32 v112, v102
	v_mul_f32_e32 v102, v103, v116
	v_exp_f32_e32 v99, v99
	v_max_f32_e32 v102, 0xc2a00000, v102
	v_lshl_add_u64 v[110:111], s[26:27], 0, v[110:111]
	v_mul_f32_e32 v102, 0xbfb8aa3b, v102
	v_cvt_pk_f16_f32 v106, v154, v158
	v_cvt_pk_f16_f32 v108, v159, v109
	v_cvt_pk_f16_f32 v109, v160, v161
	v_exp_f32_e32 v113, v102
	v_lshl_add_u64 v[102:103], v[110:111], 0, v[114:115]
	v_fma_f32 v98, v123, v98, v124
	ds_bpermute_b32 v238, v244, v106
	ds_bpermute_b32 v239, v244, v107
	ds_bpermute_b32 v240, v244, v108
	ds_bpermute_b32 v241, v244, v109
	ds_bpermute_b32 v242, v244, v102
	ds_bpermute_b32 v243, v244, v103
	s_waitcnt lgkmcnt(0)
	global_store_dwordx4 v[242:243], v[238:241], off
	v_mul_f32_e32 v104, v104, v116
	v_mul_f32_e32 v105, v105, v116
	v_log_f32_e32 v108, v98
	v_add_f32_e32 v98, 1.0, v99
	v_mul_f32_e32 v99, v100, v116
	v_max_f32_e32 v99, 0xc2a00000, v99
	v_mul_f32_e32 v100, v101, v116
	v_max_f32_e32 v104, 0xc2a00000, v104
	v_max_f32_e32 v105, 0xc2a00000, v105
	v_mul_f32_e32 v99, 0xbfb8aa3b, v99
	v_max_f32_e32 v100, 0xc2a00000, v100
	v_mul_f32_e32 v104, 0xbfb8aa3b, v104
	v_mul_f32_e32 v105, 0xbfb8aa3b, v105
	v_exp_f32_e32 v99, v99
	v_mul_f32_e32 v100, 0xbfb8aa3b, v100
	v_exp_f32_e32 v104, v104
	v_exp_f32_e32 v105, v105
	v_exp_f32_e32 v100, v100
	v_rcp_f32_e32 v98, v98
	v_add_f32_e32 v99, 1.0, v99
	v_add_f32_e32 v110, 1.0, v112
	v_add_f32_e32 v111, 1.0, v113
	v_add_f32_e32 v104, 1.0, v104
	v_add_f32_e32 v105, 1.0, v105
	v_rcp_f32_e32 v99, v99
	v_add_f32_e32 v100, 1.0, v100
	v_rcp_f32_e32 v110, v110
	v_rcp_f32_e32 v111, v111
	v_rcp_f32_e32 v104, v104
	v_rcp_f32_e32 v105, v105
	v_rcp_f32_e32 v100, v100
	v_mul_f32_e32 v90, v90, v117
	v_fma_f32 v98, v120, v98, v125
	v_mul_f32_e32 v94, v94, v117
	v_max_f32_e32 v90, 0xc2a00000, v90
	v_log_f32_e32 v101, v98
	v_fma_f32 v98, v118, v99, v126
	v_max_f32_e32 v94, 0xc2a00000, v94
	v_mul_f32_e32 v90, 0xbfb8aa3b, v90
	v_fma_f32 v106, v153, v110, v128
	v_fma_f32 v107, v168, v111, v129
	v_fma_f32 v104, v121, v104, v130
	v_fma_f32 v105, v122, v105, v131
	v_log_f32_e32 v109, v98
	v_fma_f32 v98, v119, v100, v127
	v_mul_f32_e32 v94, 0xbfb8aa3b, v94
	v_exp_f32_e32 v90, v90
	v_log_f32_e32 v106, v106
	v_log_f32_e32 v107, v107
	v_log_f32_e32 v104, v104
	v_log_f32_e32 v105, v105
	v_log_f32_e32 v110, v98
	v_exp_f32_e32 v94, v94
	v_mul_f32_e32 v95, v95, v117
	v_max_f32_e32 v95, 0xc2a00000, v95
	v_mul_f32_e32 v91, v91, v117
	v_mul_f32_e32 v95, 0xbfb8aa3b, v95
	v_add_f32_e32 v90, 1.0, v90
	v_max_f32_e32 v91, 0xc2a00000, v91
	v_cvt_pk_f16_f32 v98, v106, v107
	v_cvt_pk_f16_f32 v99, v104, v105
	v_cvt_pk_f16_f32 v100, v108, v101
	v_cvt_pk_f16_f32 v101, v109, v110
	v_exp_f32_e32 v95, v95
	v_add_f32_e32 v94, 1.0, v94
	v_rcp_f32_e32 v90, v90
	v_mul_f32_e32 v91, 0xbfb8aa3b, v91
	ds_bpermute_b32 v232, v244, v98
	ds_bpermute_b32 v233, v244, v99
	ds_bpermute_b32 v234, v244, v100
	ds_bpermute_b32 v235, v244, v101
	ds_bpermute_b32 v236, v244, v102
	ds_bpermute_b32 v237, v244, v103
	s_waitcnt lgkmcnt(0)
	global_store_dwordx4 v[236:237], v[232:235], off offset:64
	v_exp_f32_e32 v91, v91
	v_fma_f32 v90, v171, v90, v132
	v_rcp_f32_e32 v100, v94
	v_or_b32_e32 v98, 32, v152
	v_ashrrev_i32_e32 v99, 31, v98
	v_add_f32_e32 v94, 1.0, v95
	v_rcp_f32_e32 v101, v94
	v_lshlrev_b64 v[94:95], 12, v[98:99]
	v_fma_f32 v98, v180, v100, v136
	v_log_f32_e32 v100, v90
	v_add_f32_e32 v90, 1.0, v91
	v_mul_f32_e32 v91, v92, v117
	v_mul_f32_e32 v96, v96, v117
	v_mul_f32_e32 v97, v97, v117
	v_max_f32_e32 v91, 0xc2a00000, v91
	v_mul_f32_e32 v92, v93, v117
	v_max_f32_e32 v96, 0xc2a00000, v96
	v_max_f32_e32 v97, 0xc2a00000, v97
	v_mul_f32_e32 v91, 0xbfb8aa3b, v91
	v_max_f32_e32 v92, 0xc2a00000, v92
	v_mul_f32_e32 v96, 0xbfb8aa3b, v96
	v_mul_f32_e32 v97, 0xbfb8aa3b, v97
	v_exp_f32_e32 v91, v91
	v_mul_f32_e32 v92, 0xbfb8aa3b, v92
	v_exp_f32_e32 v96, v96
	v_exp_f32_e32 v97, v97
	v_exp_f32_e32 v92, v92
	v_mul_f32_e32 v82, v82, v117
	v_rcp_f32_e32 v90, v90
	v_add_f32_e32 v91, 1.0, v91
	v_max_f32_e32 v82, 0xc2a00000, v82
	v_add_f32_e32 v96, 1.0, v96
	v_add_f32_e32 v97, 1.0, v97
	v_rcp_f32_e32 v91, v91
	v_add_f32_e32 v92, 1.0, v92
	v_mul_f32_e32 v82, 0xbfb8aa3b, v82
	v_rcp_f32_e32 v96, v96
	v_rcp_f32_e32 v97, v97
	v_rcp_f32_e32 v92, v92
	v_exp_f32_e32 v82, v82
	v_fma_f32 v90, v170, v90, v133
	v_log_f32_e32 v93, v90
	v_fma_f32 v90, v169, v91, v134
	v_mul_f32_e32 v83, v83, v117
	v_fma_f32 v99, v179, v101, v137
	v_fma_f32 v96, v178, v96, v138
	v_fma_f32 v97, v177, v97, v139
	v_log_f32_e32 v101, v90
	v_fma_f32 v90, v155, v92, v135
	v_add_f32_e32 v82, 1.0, v82
	v_max_f32_e32 v83, 0xc2a00000, v83
	v_log_f32_e32 v98, v98
	v_log_f32_e32 v99, v99
	v_log_f32_e32 v96, v96
	v_log_f32_e32 v97, v97
	v_log_f32_e32 v102, v90
	v_rcp_f32_e32 v82, v82
	v_mul_f32_e32 v83, 0xbfb8aa3b, v83
	v_exp_f32_e32 v83, v83
	v_lshl_add_u64 v[94:95], s[26:27], 0, v[94:95]
	v_cvt_pk_f16_f32 v90, v98, v99
	v_cvt_pk_f16_f32 v91, v96, v97
	v_cvt_pk_f16_f32 v92, v100, v93
	v_cvt_pk_f16_f32 v93, v101, v102
	v_lshl_add_u64 v[94:95], v[94:95], 0, v[114:115]
	v_fma_f32 v82, v123, v82, v124
	ds_bpermute_b32 v238, v244, v90
	ds_bpermute_b32 v239, v244, v91
	ds_bpermute_b32 v240, v244, v92
	ds_bpermute_b32 v241, v244, v93
	ds_bpermute_b32 v242, v244, v94
	ds_bpermute_b32 v243, v244, v95
	s_waitcnt lgkmcnt(0)
	global_store_dwordx4 v[242:243], v[238:241], off
	v_mul_f32_e32 v86, v86, v117
	v_mul_f32_e32 v87, v87, v117
	v_log_f32_e32 v90, v82
	v_add_f32_e32 v82, 1.0, v83
	v_mul_f32_e32 v83, v84, v117
	v_max_f32_e32 v83, 0xc2a00000, v83
	v_mul_f32_e32 v84, v85, v117
	v_mul_f32_e32 v83, 0xbfb8aa3b, v83
	v_max_f32_e32 v84, 0xc2a00000, v84
	v_exp_f32_e32 v83, v83
	v_mul_f32_e32 v84, 0xbfb8aa3b, v84
	v_exp_f32_e32 v84, v84
	v_rcp_f32_e32 v82, v82
	v_add_f32_e32 v83, 1.0, v83
	v_rcp_f32_e32 v83, v83
	v_add_f32_e32 v84, 1.0, v84
	v_rcp_f32_e32 v84, v84
	v_mul_f32_e32 v88, v88, v117
	v_mul_f32_e32 v89, v89, v117
	v_max_f32_e32 v86, 0xc2a00000, v86
	v_max_f32_e32 v87, 0xc2a00000, v87
	v_max_f32_e32 v88, 0xc2a00000, v88
	v_max_f32_e32 v89, 0xc2a00000, v89
	v_fma_f32 v82, v120, v82, v125
	v_mul_f32_e32 v86, 0xbfb8aa3b, v86
	v_mul_f32_e32 v87, 0xbfb8aa3b, v87
	v_mul_f32_e32 v88, 0xbfb8aa3b, v88
	v_mul_f32_e32 v89, 0xbfb8aa3b, v89
	v_log_f32_e32 v91, v82
	v_fma_f32 v82, v118, v83, v126
	v_exp_f32_e32 v86, v86
	v_exp_f32_e32 v87, v87
	v_exp_f32_e32 v88, v88
	v_exp_f32_e32 v89, v89
	v_log_f32_e32 v92, v82
	v_fma_f32 v82, v119, v84, v127
	v_log_f32_e32 v93, v82
	ds_read2_b32 v[82:83], v176 offset0:48 offset1:128
	v_add_f32_e32 v86, 1.0, v86
	v_add_f32_e32 v87, 1.0, v87
	v_add_f32_e32 v88, 1.0, v88
	v_add_f32_e32 v89, 1.0, v89
	v_rcp_f32_e32 v86, v86
	v_rcp_f32_e32 v87, v87
	v_rcp_f32_e32 v88, v88
	v_rcp_f32_e32 v89, v89
	s_waitcnt lgkmcnt(0)
	v_mul_f32_e32 v74, v74, v82
	v_mul_f32_e32 v78, v78, v82
	v_max_f32_e32 v74, 0xc2a00000, v74
	v_max_f32_e32 v78, 0xc2a00000, v78
	v_mul_f32_e32 v74, 0xbfb8aa3b, v74
	v_fma_f32 v86, v153, v86, v128
	v_fma_f32 v87, v168, v87, v129
	v_fma_f32 v88, v121, v88, v130
	v_fma_f32 v89, v122, v89, v131
	v_mul_f32_e32 v78, 0xbfb8aa3b, v78
	v_exp_f32_e32 v74, v74
	v_log_f32_e32 v86, v86
	v_log_f32_e32 v87, v87
	v_log_f32_e32 v88, v88
	v_log_f32_e32 v89, v89
	v_exp_f32_e32 v78, v78
	v_mul_f32_e32 v79, v79, v82
	v_max_f32_e32 v79, 0xc2a00000, v79
	v_mul_f32_e32 v75, v75, v82
	v_mul_f32_e32 v79, 0xbfb8aa3b, v79
	v_add_f32_e32 v74, 1.0, v74
	v_max_f32_e32 v75, 0xc2a00000, v75
	v_cvt_pk_f16_f32 v84, v86, v87
	v_cvt_pk_f16_f32 v85, v88, v89
	v_cvt_pk_f16_f32 v86, v90, v91
	v_cvt_pk_f16_f32 v87, v92, v93
	v_exp_f32_e32 v79, v79
	v_add_f32_e32 v78, 1.0, v78
	v_rcp_f32_e32 v74, v74
	v_mul_f32_e32 v75, 0xbfb8aa3b, v75
	ds_bpermute_b32 v232, v244, v84
	ds_bpermute_b32 v233, v244, v85
	ds_bpermute_b32 v234, v244, v86
	ds_bpermute_b32 v235, v244, v87
	ds_bpermute_b32 v236, v244, v94
	ds_bpermute_b32 v237, v244, v95
	s_waitcnt lgkmcnt(0)
	global_store_dwordx4 v[236:237], v[232:235], off offset:64
	v_exp_f32_e32 v75, v75
	v_mul_f32_e32 v80, v80, v82
	v_rcp_f32_e32 v86, v78
	v_or_b32_e32 v84, 48, v152
	v_mul_f32_e32 v81, v81, v82
	v_ashrrev_i32_e32 v85, 31, v84
	v_add_f32_e32 v78, 1.0, v79
	v_max_f32_e32 v80, 0xc2a00000, v80
	v_max_f32_e32 v81, 0xc2a00000, v81
	v_fma_f32 v74, v171, v74, v132
	v_rcp_f32_e32 v87, v78
	v_lshlrev_b64 v[78:79], 12, v[84:85]
	v_fma_f32 v84, v180, v86, v136
	v_mul_f32_e32 v80, 0xbfb8aa3b, v80
	v_mul_f32_e32 v81, 0xbfb8aa3b, v81
	v_log_f32_e32 v86, v74
	v_add_f32_e32 v74, 1.0, v75
	v_mul_f32_e32 v75, v76, v82
	v_exp_f32_e32 v80, v80
	v_exp_f32_e32 v81, v81
	v_max_f32_e32 v75, 0xc2a00000, v75
	v_mul_f32_e32 v76, v77, v82
	v_mul_f32_e32 v75, 0xbfb8aa3b, v75
	v_max_f32_e32 v76, 0xc2a00000, v76
	v_exp_f32_e32 v75, v75
	v_mul_f32_e32 v76, 0xbfb8aa3b, v76
	v_exp_f32_e32 v76, v76
	v_add_f32_e32 v80, 1.0, v80
	v_add_f32_e32 v81, 1.0, v81
	v_rcp_f32_e32 v80, v80
	v_rcp_f32_e32 v81, v81
	v_mul_f32_e32 v66, v66, v82
	v_rcp_f32_e32 v74, v74
	v_add_f32_e32 v75, 1.0, v75
	v_max_f32_e32 v66, 0xc2a00000, v66
	v_rcp_f32_e32 v75, v75
	v_add_f32_e32 v76, 1.0, v76
	v_mul_f32_e32 v66, 0xbfb8aa3b, v66
	v_rcp_f32_e32 v76, v76
	v_exp_f32_e32 v66, v66
	v_fma_f32 v80, v178, v80, v138
	v_fma_f32 v81, v177, v81, v139
	v_log_f32_e32 v80, v80
	v_log_f32_e32 v81, v81
	v_fma_f32 v74, v170, v74, v133
	v_log_f32_e32 v77, v74
	v_fma_f32 v74, v169, v75, v134
	v_mul_f32_e32 v70, v70, v82
	v_mul_f32_e32 v67, v67, v82
	v_fma_f32 v85, v179, v87, v137
	v_log_f32_e32 v87, v74
	v_fma_f32 v74, v155, v76, v135
	v_max_f32_e32 v70, 0xc2a00000, v70
	v_add_f32_e32 v66, 1.0, v66
	v_max_f32_e32 v67, 0xc2a00000, v67
	v_log_f32_e32 v84, v84
	v_log_f32_e32 v85, v85
	v_log_f32_e32 v88, v74
	v_mul_f32_e32 v70, 0xbfb8aa3b, v70
	v_rcp_f32_e32 v66, v66
	v_mul_f32_e32 v67, 0xbfb8aa3b, v67
	v_cvt_pk_f16_f32 v75, v80, v81
	v_exp_f32_e32 v80, v70
	v_mul_f32_e32 v70, v71, v82
	v_exp_f32_e32 v67, v67
	v_max_f32_e32 v70, 0xc2a00000, v70
	v_lshl_add_u64 v[78:79], s[26:27], 0, v[78:79]
	v_mul_f32_e32 v70, 0xbfb8aa3b, v70
	v_cvt_pk_f16_f32 v74, v84, v85
	v_cvt_pk_f16_f32 v76, v86, v77
	v_cvt_pk_f16_f32 v77, v87, v88
	v_exp_f32_e32 v81, v70
	v_lshl_add_u64 v[70:71], v[78:79], 0, v[114:115]
	v_fma_f32 v66, v123, v66, v124
	ds_bpermute_b32 v238, v244, v74
	ds_bpermute_b32 v239, v244, v75
	ds_bpermute_b32 v240, v244, v76
	ds_bpermute_b32 v241, v244, v77
	ds_bpermute_b32 v242, v244, v70
	ds_bpermute_b32 v243, v244, v71
	s_waitcnt lgkmcnt(0)
	global_store_dwordx4 v[242:243], v[238:241], off
	v_mul_f32_e32 v72, v72, v82
	v_mul_f32_e32 v73, v73, v82
	v_log_f32_e32 v76, v66
	v_add_f32_e32 v66, 1.0, v67
	v_mul_f32_e32 v67, v68, v82
	v_max_f32_e32 v67, 0xc2a00000, v67
	v_mul_f32_e32 v68, v69, v82
	v_max_f32_e32 v72, 0xc2a00000, v72
	v_max_f32_e32 v73, 0xc2a00000, v73
	v_mul_f32_e32 v67, 0xbfb8aa3b, v67
	v_max_f32_e32 v68, 0xc2a00000, v68
	v_mul_f32_e32 v72, 0xbfb8aa3b, v72
	v_mul_f32_e32 v73, 0xbfb8aa3b, v73
	v_exp_f32_e32 v67, v67
	v_mul_f32_e32 v68, 0xbfb8aa3b, v68
	v_exp_f32_e32 v72, v72
	v_exp_f32_e32 v73, v73
	v_exp_f32_e32 v68, v68
	v_mul_f32_e32 v58, v58, v83
	v_rcp_f32_e32 v66, v66
	v_add_f32_e32 v67, 1.0, v67
	v_max_f32_e32 v58, 0xc2a00000, v58
	v_add_f32_e32 v78, 1.0, v80
	v_add_f32_e32 v79, 1.0, v81
	v_add_f32_e32 v72, 1.0, v72
	v_add_f32_e32 v73, 1.0, v73
	v_rcp_f32_e32 v67, v67
	v_add_f32_e32 v68, 1.0, v68
	v_mul_f32_e32 v58, 0xbfb8aa3b, v58
	v_rcp_f32_e32 v78, v78
	v_rcp_f32_e32 v79, v79
	v_rcp_f32_e32 v72, v72
	v_rcp_f32_e32 v73, v73
	v_rcp_f32_e32 v68, v68
	v_exp_f32_e32 v58, v58
	v_fma_f32 v66, v120, v66, v125
	v_log_f32_e32 v69, v66
	v_fma_f32 v66, v118, v67, v126
	v_mul_f32_e32 v59, v59, v83
	v_fma_f32 v74, v153, v78, v128
	v_fma_f32 v75, v168, v79, v129
	v_fma_f32 v72, v121, v72, v130
	v_fma_f32 v73, v122, v73, v131
	v_log_f32_e32 v77, v66
	v_fma_f32 v66, v119, v68, v127
	v_add_f32_e32 v58, 1.0, v58
	v_max_f32_e32 v59, 0xc2a00000, v59
	v_log_f32_e32 v74, v74
	v_log_f32_e32 v75, v75
	v_log_f32_e32 v72, v72
	v_log_f32_e32 v73, v73
	v_log_f32_e32 v78, v66
	v_rcp_f32_e32 v58, v58
	v_mul_f32_e32 v59, 0xbfb8aa3b, v59
	v_exp_f32_e32 v59, v59
	v_mul_f32_e32 v64, v64, v83
	v_mul_f32_e32 v65, v65, v83
	v_max_f32_e32 v64, 0xc2a00000, v64
	v_max_f32_e32 v65, 0xc2a00000, v65
	v_cvt_pk_f16_f32 v66, v74, v75
	v_cvt_pk_f16_f32 v67, v72, v73
	v_cvt_pk_f16_f32 v68, v76, v69
	v_mul_f32_e32 v62, v62, v83
	v_mul_f32_e32 v63, v63, v83
	v_cvt_pk_f16_f32 v69, v77, v78
	v_mul_f32_e32 v64, 0xbfb8aa3b, v64
	v_mul_f32_e32 v65, 0xbfb8aa3b, v65
	v_fma_f32 v58, v171, v58, v132
	v_max_f32_e32 v62, 0xc2a00000, v62
	v_max_f32_e32 v63, 0xc2a00000, v63
	ds_bpermute_b32 v232, v244, v66
	ds_bpermute_b32 v233, v244, v67
	ds_bpermute_b32 v234, v244, v68
	ds_bpermute_b32 v235, v244, v69
	ds_bpermute_b32 v236, v244, v70
	ds_bpermute_b32 v237, v244, v71
	s_waitcnt lgkmcnt(0)
	global_store_dwordx4 v[236:237], v[232:235], off offset:64
	v_exp_f32_e32 v64, v64
	v_exp_f32_e32 v65, v65
	v_log_f32_e32 v66, v58
	v_add_f32_e32 v58, 1.0, v59
	v_mul_f32_e32 v59, v60, v83
	v_mul_f32_e32 v62, 0xbfb8aa3b, v62
	v_mul_f32_e32 v63, 0xbfb8aa3b, v63
	v_max_f32_e32 v59, 0xc2a00000, v59
	v_mul_f32_e32 v60, v61, v83
	v_exp_f32_e32 v62, v62
	v_exp_f32_e32 v63, v63
	v_mul_f32_e32 v59, 0xbfb8aa3b, v59
	v_max_f32_e32 v60, 0xc2a00000, v60
	v_exp_f32_e32 v59, v59
	v_mul_f32_e32 v60, 0xbfb8aa3b, v60
	v_add_f32_e32 v64, 1.0, v64
	v_add_f32_e32 v65, 1.0, v65
	v_exp_f32_e32 v60, v60
	v_rcp_f32_e32 v64, v64
	v_rcp_f32_e32 v65, v65
	v_add_f32_e32 v62, 1.0, v62
	v_add_f32_e32 v63, 1.0, v63
	v_mul_f32_e32 v50, v50, v83
	v_rcp_f32_e32 v62, v62
	v_rcp_f32_e32 v63, v63
	v_rcp_f32_e32 v58, v58
	v_add_f32_e32 v59, 1.0, v59
	v_max_f32_e32 v50, 0xc2a00000, v50
	v_rcp_f32_e32 v59, v59
	v_add_f32_e32 v60, 1.0, v60
	v_mul_f32_e32 v50, 0xbfb8aa3b, v50
	v_fma_f32 v64, v178, v64, v138
	v_fma_f32 v65, v177, v65, v139
	v_rcp_f32_e32 v60, v60
	v_exp_f32_e32 v50, v50
	v_log_f32_e32 v64, v64
	v_log_f32_e32 v65, v65
	v_fma_f32 v62, v180, v62, v136
	v_fma_f32 v63, v179, v63, v137
	v_fma_f32 v58, v170, v58, v133
	v_mul_f32_e32 v54, v54, v83
	v_log_f32_e32 v62, v62
	v_log_f32_e32 v63, v63
	v_log_f32_e32 v61, v58
	v_fma_f32 v58, v169, v59, v134
	v_max_f32_e32 v54, 0xc2a00000, v54
	v_mul_f32_e32 v51, v51, v83
	v_log_f32_e32 v67, v58
	v_fma_f32 v58, v155, v60, v135
	v_mul_f32_e32 v54, 0xbfb8aa3b, v54
	v_add_f32_e32 v50, 1.0, v50
	v_max_f32_e32 v51, 0xc2a00000, v51
	v_log_f32_e32 v68, v58
	v_cvt_pk_f16_f32 v59, v64, v65
	v_exp_f32_e32 v64, v54
	v_mul_f32_e32 v54, v55, v83
	v_rcp_f32_e32 v50, v50
	v_mul_f32_e32 v51, 0xbfb8aa3b, v51
	v_max_f32_e32 v54, 0xc2a00000, v54
	v_exp_f32_e32 v51, v51
	v_cvt_pk_f16_f32 v58, v62, v63
	v_lshl_add_u64 v[62:63], v[166:167], 0, s[14:15]
	v_mul_f32_e32 v54, 0xbfb8aa3b, v54
	s_mov_b32 s14, 0x80000
	v_exp_f32_e32 v65, v54
	v_add_co_u32_e32 v54, vcc, s14, v166
	v_cvt_pk_f16_f32 v60, v66, v61
	v_cvt_pk_f16_f32 v61, v67, v68
	v_addc_co_u32_e32 v55, vcc, 0, v167, vcc
	v_fma_f32 v50, v123, v50, v124
	ds_bpermute_b32 v238, v244, v58
	ds_bpermute_b32 v239, v244, v59
	ds_bpermute_b32 v240, v244, v60
	ds_bpermute_b32 v241, v244, v61
	ds_bpermute_b32 v242, v244, v54
	ds_bpermute_b32 v243, v244, v55
	s_waitcnt lgkmcnt(0)
	global_store_dwordx4 v[242:243], v[238:241], off
	v_mul_f32_e32 v56, v56, v83
	v_mul_f32_e32 v57, v57, v83
	v_log_f32_e32 v58, v50
	v_add_f32_e32 v50, 1.0, v51
	v_mul_f32_e32 v51, v52, v83
	v_max_f32_e32 v51, 0xc2a00000, v51
	v_mul_f32_e32 v51, 0xbfb8aa3b, v51
	v_exp_f32_e32 v51, v51
	v_rcp_f32_e32 v50, v50
	v_mul_f32_e32 v52, v53, v83
	v_max_f32_e32 v56, 0xc2a00000, v56
	v_add_f32_e32 v51, 1.0, v51
	v_rcp_f32_e32 v51, v51
	v_fma_f32 v50, v120, v50, v125
	v_log_f32_e32 v59, v50
	v_max_f32_e32 v57, 0xc2a00000, v57
	v_fma_f32 v50, v118, v51, v126
	v_log_f32_e32 v60, v50
	ds_read2_b32 v[50:51], v176 offset0:144 offset1:160
	v_max_f32_e32 v52, 0xc2a00000, v52
	v_mul_f32_e32 v56, 0xbfb8aa3b, v56
	v_mul_f32_e32 v57, 0xbfb8aa3b, v57
	v_mul_f32_e32 v52, 0xbfb8aa3b, v52
	v_exp_f32_e32 v56, v56
	v_exp_f32_e32 v57, v57
	v_exp_f32_e32 v52, v52
	s_waitcnt lgkmcnt(0)
	v_mul_f32_e32 v42, v42, v50
	v_max_f32_e32 v42, 0xc2a00000, v42
	v_add_f32_e32 v64, 1.0, v64
	v_add_f32_e32 v65, 1.0, v65
	v_add_f32_e32 v56, 1.0, v56
	v_add_f32_e32 v57, 1.0, v57
	v_add_f32_e32 v52, 1.0, v52
	v_mul_f32_e32 v42, 0xbfb8aa3b, v42
	v_rcp_f32_e32 v64, v64
	v_rcp_f32_e32 v65, v65
	v_rcp_f32_e32 v56, v56
	v_rcp_f32_e32 v57, v57
	v_rcp_f32_e32 v52, v52
	v_exp_f32_e32 v42, v42
	v_mul_f32_e32 v43, v43, v50
	v_fma_f32 v54, v153, v64, v128
	v_fma_f32 v55, v168, v65, v129
	v_fma_f32 v56, v121, v56, v130
	v_fma_f32 v57, v122, v57, v131
	v_fma_f32 v52, v119, v52, v127
	v_add_f32_e32 v42, 1.0, v42
	v_max_f32_e32 v43, 0xc2a00000, v43
	v_log_f32_e32 v54, v54
	v_log_f32_e32 v55, v55
	v_log_f32_e32 v56, v56
	v_log_f32_e32 v57, v57
	v_log_f32_e32 v61, v52
	v_rcp_f32_e32 v42, v42
	v_mul_f32_e32 v43, 0xbfb8aa3b, v43
	v_exp_f32_e32 v43, v43
	v_mul_f32_e32 v48, v48, v50
	v_mul_f32_e32 v49, v49, v50
	v_max_f32_e32 v48, 0xc2a00000, v48
	v_max_f32_e32 v49, 0xc2a00000, v49
	v_cvt_pk_f16_f32 v52, v54, v55
	v_cvt_pk_f16_f32 v53, v56, v57
	v_cvt_pk_f16_f32 v54, v58, v59
	v_mul_f32_e32 v46, v46, v50
	v_mul_f32_e32 v47, v47, v50
	v_cvt_pk_f16_f32 v55, v60, v61
	v_mul_f32_e32 v48, 0xbfb8aa3b, v48
	v_mul_f32_e32 v49, 0xbfb8aa3b, v49
	v_fma_f32 v42, v171, v42, v132
	v_max_f32_e32 v46, 0xc2a00000, v46
	v_max_f32_e32 v47, 0xc2a00000, v47
	ds_bpermute_b32 v232, v244, v52
	ds_bpermute_b32 v233, v244, v53
	ds_bpermute_b32 v234, v244, v54
	ds_bpermute_b32 v235, v244, v55
	ds_bpermute_b32 v236, v244, v62
	ds_bpermute_b32 v237, v244, v63
	s_waitcnt lgkmcnt(0)
	global_store_dwordx4 v[236:237], v[232:235], off offset:64
	v_exp_f32_e32 v48, v48
	v_exp_f32_e32 v49, v49
	v_log_f32_e32 v52, v42
	v_add_f32_e32 v42, 1.0, v43
	v_mul_f32_e32 v43, v44, v50
	v_mul_f32_e32 v46, 0xbfb8aa3b, v46
	v_mul_f32_e32 v47, 0xbfb8aa3b, v47
	v_max_f32_e32 v43, 0xc2a00000, v43
	v_mul_f32_e32 v44, v45, v50
	v_exp_f32_e32 v46, v46
	v_exp_f32_e32 v47, v47
	v_mul_f32_e32 v43, 0xbfb8aa3b, v43
	v_max_f32_e32 v44, 0xc2a00000, v44
	v_exp_f32_e32 v43, v43
	v_mul_f32_e32 v44, 0xbfb8aa3b, v44
	v_add_f32_e32 v48, 1.0, v48
	v_add_f32_e32 v49, 1.0, v49
	v_exp_f32_e32 v44, v44
	v_rcp_f32_e32 v48, v48
	v_rcp_f32_e32 v49, v49
	v_add_f32_e32 v46, 1.0, v46
	v_add_f32_e32 v47, 1.0, v47
	v_mul_f32_e32 v34, v34, v50
	v_rcp_f32_e32 v46, v46
	v_rcp_f32_e32 v47, v47
	v_rcp_f32_e32 v42, v42
	v_add_f32_e32 v43, 1.0, v43
	v_max_f32_e32 v34, 0xc2a00000, v34
	v_rcp_f32_e32 v43, v43
	v_add_f32_e32 v44, 1.0, v44
	v_mul_f32_e32 v34, 0xbfb8aa3b, v34
	v_fma_f32 v48, v178, v48, v138
	v_fma_f32 v49, v177, v49, v139
	v_rcp_f32_e32 v44, v44
	v_exp_f32_e32 v34, v34
	v_log_f32_e32 v48, v48
	v_log_f32_e32 v49, v49
	v_fma_f32 v46, v180, v46, v136
	v_fma_f32 v47, v179, v47, v137
	v_fma_f32 v42, v170, v42, v133
	v_mul_f32_e32 v38, v38, v50
	v_log_f32_e32 v46, v46
	v_log_f32_e32 v47, v47
	v_log_f32_e32 v45, v42
	v_fma_f32 v42, v169, v43, v134
	v_max_f32_e32 v38, 0xc2a00000, v38
	v_mul_f32_e32 v35, v35, v50
	v_log_f32_e32 v53, v42
	v_fma_f32 v42, v155, v44, v135
	v_mul_f32_e32 v38, 0xbfb8aa3b, v38
	v_add_f32_e32 v34, 1.0, v34
	v_max_f32_e32 v35, 0xc2a00000, v35
	v_log_f32_e32 v54, v42
	v_cvt_pk_f16_f32 v43, v48, v49
	v_exp_f32_e32 v48, v38
	v_mul_f32_e32 v38, v39, v50
	v_rcp_f32_e32 v34, v34
	v_mul_f32_e32 v35, 0xbfb8aa3b, v35
	s_mov_b64 s[14:15], 0x90000
	v_max_f32_e32 v38, 0xc2a00000, v38
	v_exp_f32_e32 v35, v35
	v_cvt_pk_f16_f32 v42, v46, v47
	v_lshl_add_u64 v[46:47], v[166:167], 0, s[14:15]
	v_mul_f32_e32 v38, 0xbfb8aa3b, v38
	s_mov_b32 s14, 0x90000
	v_exp_f32_e32 v49, v38
	v_add_co_u32_e32 v38, vcc, s14, v166
	v_cvt_pk_f16_f32 v44, v52, v45
	v_cvt_pk_f16_f32 v45, v53, v54
	v_addc_co_u32_e32 v39, vcc, 0, v167, vcc
	v_fma_f32 v34, v123, v34, v124
	ds_bpermute_b32 v238, v244, v42
	ds_bpermute_b32 v239, v244, v43
	ds_bpermute_b32 v240, v244, v44
	ds_bpermute_b32 v241, v244, v45
	ds_bpermute_b32 v242, v244, v38
	ds_bpermute_b32 v243, v244, v39
	s_waitcnt lgkmcnt(0)
	global_store_dwordx4 v[242:243], v[238:241], off
	v_mul_f32_e32 v40, v40, v50
	v_mul_f32_e32 v41, v41, v50
	v_log_f32_e32 v42, v34
	v_add_f32_e32 v34, 1.0, v35
	v_mul_f32_e32 v35, v36, v50
	v_max_f32_e32 v35, 0xc2a00000, v35
	v_mul_f32_e32 v36, v37, v50
	v_max_f32_e32 v40, 0xc2a00000, v40
	v_max_f32_e32 v41, 0xc2a00000, v41
	v_mul_f32_e32 v35, 0xbfb8aa3b, v35
	v_max_f32_e32 v36, 0xc2a00000, v36
	v_mul_f32_e32 v40, 0xbfb8aa3b, v40
	v_mul_f32_e32 v41, 0xbfb8aa3b, v41
	v_exp_f32_e32 v35, v35
	v_mul_f32_e32 v36, 0xbfb8aa3b, v36
	v_exp_f32_e32 v40, v40
	v_exp_f32_e32 v41, v41
	v_exp_f32_e32 v36, v36
	v_mul_f32_e32 v26, v26, v51
	v_rcp_f32_e32 v34, v34
	v_add_f32_e32 v35, 1.0, v35
	v_max_f32_e32 v26, 0xc2a00000, v26
	v_add_f32_e32 v48, 1.0, v48
	v_add_f32_e32 v49, 1.0, v49
	v_add_f32_e32 v40, 1.0, v40
	v_add_f32_e32 v41, 1.0, v41
	v_rcp_f32_e32 v35, v35
	v_add_f32_e32 v36, 1.0, v36
	v_mul_f32_e32 v26, 0xbfb8aa3b, v26
	v_rcp_f32_e32 v48, v48
	v_rcp_f32_e32 v49, v49
	v_rcp_f32_e32 v40, v40
	v_rcp_f32_e32 v41, v41
	v_rcp_f32_e32 v36, v36
	v_exp_f32_e32 v26, v26
	v_fma_f32 v34, v120, v34, v125
	v_log_f32_e32 v37, v34
	v_fma_f32 v34, v118, v35, v126
	v_mul_f32_e32 v27, v27, v51
	v_fma_f32 v38, v153, v48, v128
	v_fma_f32 v39, v168, v49, v129
	v_fma_f32 v40, v121, v40, v130
	v_fma_f32 v41, v122, v41, v131
	v_log_f32_e32 v43, v34
	v_fma_f32 v34, v119, v36, v127
	v_add_f32_e32 v26, 1.0, v26
	v_max_f32_e32 v27, 0xc2a00000, v27
	v_log_f32_e32 v38, v38
	v_log_f32_e32 v39, v39
	v_log_f32_e32 v40, v40
	v_log_f32_e32 v41, v41
	v_log_f32_e32 v44, v34
	v_rcp_f32_e32 v26, v26
	v_mul_f32_e32 v27, 0xbfb8aa3b, v27
	v_exp_f32_e32 v27, v27
	v_mul_f32_e32 v32, v32, v51
	v_mul_f32_e32 v33, v33, v51
	v_max_f32_e32 v32, 0xc2a00000, v32
	v_max_f32_e32 v33, 0xc2a00000, v33
	v_cvt_pk_f16_f32 v34, v38, v39
	v_cvt_pk_f16_f32 v35, v40, v41
	v_cvt_pk_f16_f32 v36, v42, v37
	v_mul_f32_e32 v30, v30, v51
	v_mul_f32_e32 v31, v31, v51
	v_cvt_pk_f16_f32 v37, v43, v44
	v_mul_f32_e32 v32, 0xbfb8aa3b, v32
	v_mul_f32_e32 v33, 0xbfb8aa3b, v33
	v_fma_f32 v26, v171, v26, v132
	v_max_f32_e32 v30, 0xc2a00000, v30
	v_max_f32_e32 v31, 0xc2a00000, v31
	ds_bpermute_b32 v232, v244, v34
	ds_bpermute_b32 v233, v244, v35
	ds_bpermute_b32 v234, v244, v36
	ds_bpermute_b32 v235, v244, v37
	ds_bpermute_b32 v236, v244, v46
	ds_bpermute_b32 v237, v244, v47
	s_waitcnt lgkmcnt(0)
	global_store_dwordx4 v[236:237], v[232:235], off offset:64
	v_exp_f32_e32 v32, v32
	v_exp_f32_e32 v33, v33
	v_log_f32_e32 v34, v26
	v_add_f32_e32 v26, 1.0, v27
	v_mul_f32_e32 v27, v28, v51
	v_mul_f32_e32 v30, 0xbfb8aa3b, v30
	v_mul_f32_e32 v31, 0xbfb8aa3b, v31
	v_max_f32_e32 v27, 0xc2a00000, v27
	v_mul_f32_e32 v28, v29, v51
	v_exp_f32_e32 v30, v30
	v_exp_f32_e32 v31, v31
	v_mul_f32_e32 v27, 0xbfb8aa3b, v27
	v_max_f32_e32 v28, 0xc2a00000, v28
	v_exp_f32_e32 v27, v27
	v_mul_f32_e32 v28, 0xbfb8aa3b, v28
	v_add_f32_e32 v32, 1.0, v32
	v_add_f32_e32 v33, 1.0, v33
	v_exp_f32_e32 v28, v28
	v_rcp_f32_e32 v32, v32
	v_rcp_f32_e32 v33, v33
	v_add_f32_e32 v30, 1.0, v30
	v_add_f32_e32 v31, 1.0, v31
	v_mul_f32_e32 v18, v18, v51
	v_rcp_f32_e32 v30, v30
	v_rcp_f32_e32 v31, v31
	v_rcp_f32_e32 v26, v26
	v_add_f32_e32 v27, 1.0, v27
	v_max_f32_e32 v18, 0xc2a00000, v18
	v_rcp_f32_e32 v27, v27
	v_add_f32_e32 v28, 1.0, v28
	v_mul_f32_e32 v18, 0xbfb8aa3b, v18
	v_fma_f32 v32, v178, v32, v138
	v_fma_f32 v33, v177, v33, v139
	v_rcp_f32_e32 v28, v28
	v_exp_f32_e32 v18, v18
	v_log_f32_e32 v32, v32
	v_log_f32_e32 v33, v33
	v_fma_f32 v30, v180, v30, v136
	v_fma_f32 v31, v179, v31, v137
	v_fma_f32 v26, v170, v26, v133
	v_mul_f32_e32 v22, v22, v51
	v_log_f32_e32 v30, v30
	v_log_f32_e32 v31, v31
	v_log_f32_e32 v29, v26
	v_fma_f32 v26, v169, v27, v134
	v_max_f32_e32 v22, 0xc2a00000, v22
	v_mul_f32_e32 v19, v19, v51
	v_log_f32_e32 v35, v26
	v_fma_f32 v26, v155, v28, v135
	v_mul_f32_e32 v22, 0xbfb8aa3b, v22
	v_add_f32_e32 v18, 1.0, v18
	v_max_f32_e32 v19, 0xc2a00000, v19
	v_log_f32_e32 v36, v26
	v_cvt_pk_f16_f32 v27, v32, v33
	v_exp_f32_e32 v32, v22
	v_mul_f32_e32 v22, v23, v51
	v_rcp_f32_e32 v18, v18
	v_mul_f32_e32 v19, 0xbfb8aa3b, v19
	s_mov_b64 s[14:15], 0xa0000
	v_max_f32_e32 v22, 0xc2a00000, v22
	v_exp_f32_e32 v19, v19
	v_cvt_pk_f16_f32 v26, v30, v31
	v_lshl_add_u64 v[30:31], v[166:167], 0, s[14:15]
	v_mul_f32_e32 v22, 0xbfb8aa3b, v22
	s_mov_b32 s14, 0xa0000
	v_exp_f32_e32 v33, v22
	v_add_co_u32_e32 v22, vcc, s14, v166
	v_cvt_pk_f16_f32 v28, v34, v29
	v_cvt_pk_f16_f32 v29, v35, v36
	v_addc_co_u32_e32 v23, vcc, 0, v167, vcc
	v_fma_f32 v18, v123, v18, v124
	ds_bpermute_b32 v238, v244, v26
	ds_bpermute_b32 v239, v244, v27
	ds_bpermute_b32 v240, v244, v28
	ds_bpermute_b32 v241, v244, v29
	ds_bpermute_b32 v242, v244, v22
	ds_bpermute_b32 v243, v244, v23
	s_waitcnt lgkmcnt(0)
	global_store_dwordx4 v[242:243], v[238:241], off
	v_mul_f32_e32 v24, v24, v51
	v_mul_f32_e32 v25, v25, v51
	v_log_f32_e32 v26, v18
	v_add_f32_e32 v18, 1.0, v19
	v_mul_f32_e32 v19, v20, v51
	v_max_f32_e32 v19, 0xc2a00000, v19
	v_mul_f32_e32 v20, v21, v51
	ds_read_b32 v28, v176 offset:704
	v_max_f32_e32 v24, 0xc2a00000, v24
	v_max_f32_e32 v25, 0xc2a00000, v25
	v_mul_f32_e32 v19, 0xbfb8aa3b, v19
	v_max_f32_e32 v20, 0xc2a00000, v20
	v_mul_f32_e32 v24, 0xbfb8aa3b, v24
	v_mul_f32_e32 v25, 0xbfb8aa3b, v25
	v_exp_f32_e32 v19, v19
	v_mul_f32_e32 v20, 0xbfb8aa3b, v20
	v_exp_f32_e32 v24, v24
	v_exp_f32_e32 v25, v25
	v_exp_f32_e32 v20, v20
	s_waitcnt lgkmcnt(0)
	v_mul_f32_e32 v10, v10, v28
	v_rcp_f32_e32 v18, v18
	v_add_f32_e32 v19, 1.0, v19
	v_max_f32_e32 v10, 0xc2a00000, v10
	v_add_f32_e32 v32, 1.0, v32
	v_add_f32_e32 v33, 1.0, v33
	v_add_f32_e32 v24, 1.0, v24
	v_add_f32_e32 v25, 1.0, v25
	v_rcp_f32_e32 v19, v19
	v_add_f32_e32 v20, 1.0, v20
	v_mul_f32_e32 v10, 0xbfb8aa3b, v10
	v_rcp_f32_e32 v32, v32
	v_rcp_f32_e32 v33, v33
	v_rcp_f32_e32 v24, v24
	v_rcp_f32_e32 v25, v25
	v_rcp_f32_e32 v20, v20
	v_exp_f32_e32 v10, v10
	v_fma_f32 v18, v120, v18, v125
	v_log_f32_e32 v21, v18
	v_fma_f32 v18, v118, v19, v126
	v_mul_f32_e32 v11, v11, v28
	v_fma_f32 v22, v153, v32, v128
	v_fma_f32 v23, v168, v33, v129
	v_fma_f32 v24, v121, v24, v130
	v_fma_f32 v25, v122, v25, v131
	v_log_f32_e32 v27, v18
	v_fma_f32 v18, v119, v20, v127
	v_add_f32_e32 v10, 1.0, v10
	v_max_f32_e32 v11, 0xc2a00000, v11
	v_log_f32_e32 v22, v22
	v_log_f32_e32 v23, v23
	v_log_f32_e32 v24, v24
	v_log_f32_e32 v25, v25
	v_log_f32_e32 v29, v18
	v_rcp_f32_e32 v10, v10
	v_mul_f32_e32 v11, 0xbfb8aa3b, v11
	v_mul_f32_e32 v14, v14, v28
	v_mul_f32_e32 v15, v15, v28
	v_exp_f32_e32 v11, v11
	v_max_f32_e32 v14, 0xc2a00000, v14
	v_max_f32_e32 v15, 0xc2a00000, v15
	v_mul_f32_e32 v14, 0xbfb8aa3b, v14
	v_mul_f32_e32 v15, 0xbfb8aa3b, v15
	v_cvt_pk_f16_f32 v18, v22, v23
	v_cvt_pk_f16_f32 v19, v24, v25
	v_cvt_pk_f16_f32 v20, v26, v21
	v_exp_f32_e32 v14, v14
	v_exp_f32_e32 v15, v15
	v_cvt_pk_f16_f32 v21, v27, v29
	v_fma_f32 v10, v171, v10, v132
	ds_bpermute_b32 v232, v244, v18
	ds_bpermute_b32 v233, v244, v19
	ds_bpermute_b32 v234, v244, v20
	ds_bpermute_b32 v235, v244, v21
	ds_bpermute_b32 v236, v244, v30
	ds_bpermute_b32 v237, v244, v31
	s_waitcnt lgkmcnt(0)
	global_store_dwordx4 v[236:237], v[232:235], off offset:64
	v_add_f32_e32 v14, 1.0, v14
	v_add_f32_e32 v15, 1.0, v15
	v_log_f32_e32 v18, v10
	v_add_f32_e32 v10, 1.0, v11
	v_mul_f32_e32 v11, v12, v28
	v_max_f32_e32 v11, 0xc2a00000, v11
	v_mul_f32_e32 v11, 0xbfb8aa3b, v11
	v_exp_f32_e32 v11, v11
	v_rcp_f32_e32 v14, v14
	v_rcp_f32_e32 v15, v15
	v_mul_f32_e32 v16, v16, v28
	v_mul_f32_e32 v17, v17, v28
	v_rcp_f32_e32 v10, v10
	v_mul_f32_e32 v12, v13, v28
	v_add_f32_e32 v11, 1.0, v11
	v_fma_f32 v14, v180, v14, v136
	v_fma_f32 v15, v179, v15, v137
	v_max_f32_e32 v16, 0xc2a00000, v16
	v_max_f32_e32 v17, 0xc2a00000, v17
	v_max_f32_e32 v12, 0xc2a00000, v12
	v_rcp_f32_e32 v11, v11
	v_log_f32_e32 v14, v14
	v_mul_f32_e32 v16, 0xbfb8aa3b, v16
	v_mul_f32_e32 v17, 0xbfb8aa3b, v17
	v_log_f32_e32 v15, v15
	v_mul_f32_e32 v12, 0xbfb8aa3b, v12
	v_exp_f32_e32 v16, v16
	v_exp_f32_e32 v17, v17
	v_exp_f32_e32 v12, v12
	v_mul_f32_e32 v6, v6, v28
	v_fma_f32 v10, v170, v10, v133
	v_max_f32_e32 v6, 0xc2a00000, v6
	v_log_f32_e32 v13, v10
	v_fma_f32 v10, v169, v11, v134
	v_mul_f32_e32 v6, 0xbfb8aa3b, v6
	v_log_f32_e32 v19, v10
	v_cvt_pk_f16_f32 v10, v14, v15
	v_exp_f32_e32 v14, v6
	v_mul_f32_e32 v6, v7, v28
	v_mul_f32_e32 v8, v8, v28
	v_mul_f32_e32 v9, v9, v28
	v_mul_f32_e32 v2, v2, v28
	v_mul_f32_e32 v3, v3, v28
	v_mul_f32_e32 v4, v4, v28
	v_mul_f32_e32 v5, v5, v28
	v_add_f32_e32 v16, 1.0, v16
	v_add_f32_e32 v17, 1.0, v17
	v_add_f32_e32 v12, 1.0, v12
	v_max_f32_e32 v6, 0xc2a00000, v6
	v_max_f32_e32 v8, 0xc2a00000, v8
	v_max_f32_e32 v9, 0xc2a00000, v9
	v_max_f32_e32 v2, 0xc2a00000, v2
	v_max_f32_e32 v3, 0xc2a00000, v3
	v_max_f32_e32 v4, 0xc2a00000, v4
	v_max_f32_e32 v5, 0xc2a00000, v5
	v_rcp_f32_e32 v16, v16
	v_rcp_f32_e32 v17, v17
	v_rcp_f32_e32 v12, v12
	v_mul_f32_e32 v6, 0xbfb8aa3b, v6
	v_mul_f32_e32 v8, 0xbfb8aa3b, v8
	v_mul_f32_e32 v9, 0xbfb8aa3b, v9
	v_mul_f32_e32 v2, 0xbfb8aa3b, v2
	v_mul_f32_e32 v3, 0xbfb8aa3b, v3
	v_mul_f32_e32 v4, 0xbfb8aa3b, v4
	v_mul_f32_e32 v5, 0xbfb8aa3b, v5
	v_exp_f32_e32 v15, v6
	v_exp_f32_e32 v8, v8
	v_exp_f32_e32 v9, v9
	v_exp_f32_e32 v2, v2
	v_exp_f32_e32 v3, v3
	v_exp_f32_e32 v4, v4
	v_exp_f32_e32 v5, v5
	v_fma_f32 v16, v178, v16, v138
	v_fmac_f32_e32 v139, v177, v17
	v_fmac_f32_e32 v135, v155, v12
	v_log_f32_e32 v16, v16
	v_log_f32_e32 v17, v139
	v_log_f32_e32 v20, v135
	v_add_f32_e32 v14, 1.0, v14
	v_add_f32_e32 v15, 1.0, v15
	v_add_f32_e32 v8, 1.0, v8
	v_add_f32_e32 v9, 1.0, v9
	v_add_f32_e32 v2, 1.0, v2
	v_add_f32_e32 v3, 1.0, v3
	v_add_f32_e32 v4, 1.0, v4
	v_add_f32_e32 v5, 1.0, v5
	s_mov_b64 s[14:15], 0xb0000
	v_rcp_f32_e32 v14, v14
	v_rcp_f32_e32 v15, v15
	v_rcp_f32_e32 v8, v8
	v_rcp_f32_e32 v9, v9
	v_rcp_f32_e32 v2, v2
	v_rcp_f32_e32 v3, v3
	v_rcp_f32_e32 v4, v4
	v_rcp_f32_e32 v5, v5
	v_lshl_add_u64 v[136:137], v[166:167], 0, s[14:15]
	s_mov_b32 s14, 0xb0000
	v_add_co_u32_e32 v6, vcc, s14, v166
	v_cvt_pk_f16_f32 v11, v16, v17
	v_cvt_pk_f16_f32 v12, v18, v13
	v_cvt_pk_f16_f32 v13, v19, v20
	v_addc_co_u32_e32 v7, vcc, 0, v167, vcc
	ds_bpermute_b32 v238, v244, v10
	ds_bpermute_b32 v239, v244, v11
	ds_bpermute_b32 v240, v244, v12
	ds_bpermute_b32 v241, v244, v13
	ds_bpermute_b32 v242, v244, v6
	ds_bpermute_b32 v243, v244, v7
	s_waitcnt lgkmcnt(0)
	global_store_dwordx4 v[242:243], v[238:241], off
	v_fma_f32 v6, v153, v14, v128
	v_fma_f32 v7, v168, v15, v129
	v_fma_f32 v8, v121, v8, v130
	v_fmac_f32_e32 v131, v122, v9
	v_fma_f32 v2, v123, v2, v124
	v_fma_f32 v3, v120, v3, v125
	v_fma_f32 v4, v118, v4, v126
	v_fmac_f32_e32 v127, v119, v5
	v_log_f32_e32 v6, v6
	v_log_f32_e32 v7, v7
	v_log_f32_e32 v8, v8
	v_log_f32_e32 v9, v131
	v_log_f32_e32 v2, v2
	v_log_f32_e32 v3, v3
	v_log_f32_e32 v4, v4
	v_log_f32_e32 v5, v127
	v_cvt_pk_f16_f32 v196, v181, v182
	v_cvt_pk_f16_f32 v132, v6, v7
	v_cvt_pk_f16_f32 v133, v8, v9
	v_cvt_pk_f16_f32 v134, v2, v3
	v_cvt_pk_f16_f32 v135, v4, v5
	ds_bpermute_b32 v232, v244, v194
	ds_bpermute_b32 v233, v244, v195
	ds_bpermute_b32 v234, v244, v196
	ds_bpermute_b32 v235, v244, v197
	ds_bpermute_b32 v236, v244, v166
	ds_bpermute_b32 v237, v244, v167
	s_waitcnt lgkmcnt(0)
	global_store_dwordx4 v[236:237], v[232:235], off offset:64
	s_andn2_b64 vcc, exec, s[38:39]
	s_mov_b64 s[28:29], -1
	ds_bpermute_b32 v238, v244, v132
	ds_bpermute_b32 v239, v244, v133
	ds_bpermute_b32 v240, v244, v134
	ds_bpermute_b32 v241, v244, v135
	ds_bpermute_b32 v242, v244, v136
	ds_bpermute_b32 v243, v244, v137
	s_waitcnt lgkmcnt(0)
	global_store_dwordx4 v[242:243], v[238:241], off offset:64
	s_cbranch_vccnz .LBB0_495

.LBB0_1082:
	v_mbcnt_lo_u32_b32 v244, -1, 0
	v_mbcnt_hi_u32_b32 v244, -1, v244
	v_lshrrev_b32_e32 v245, 2, v244
	v_and_b32_e32 v244, 3, v244
	v_lshl_add_u32 v244, v244, 4, v245
	v_lshlrev_b32_e32 v244, 2, v244
	v_pk_mul_f32 v[148:149], v[118:119], v[118:119]
	v_pk_mul_f32 v[150:151], v[126:127], v[126:127]
	v_pk_fma_f32 v[148:149], v[116:117], v[116:117], v[148:149]
	v_pk_fma_f32 v[150:151], v[124:125], v[124:125], v[150:151]
	v_lshl_add_u32 v144, s46, 8, v1
	v_pk_add_f32 v[152:153], v[148:149], v[150:151]
	v_cvt_pk_bf16_f32 v149, v118, v119
	v_cvt_pk_bf16_f32 v150, v124, v125
	v_pk_mul_f32 v[118:119], v[122:123], v[122:123]
	v_pk_mul_f32 v[124:125], v[130:131], v[130:131]
	v_pk_fma_f32 v[118:119], v[120:121], v[120:121], v[118:119]
	v_pk_fma_f32 v[124:125], v[128:129], v[128:129], v[124:125]
	s_lshl_b32 s16, s46, 5
	v_pk_add_f32 v[118:119], v[118:119], v[124:125]
	s_lshl_b32 s46, s48, 2
	v_pk_add_f32 v[124:125], v[152:153], v[118:119]
	s_or_b32 s17, s46, s12
	v_add_f32_e32 v124, v124, v125
	ds_swizzle_b32 v125, v124 offset:swizzle(SWAP,16)
	s_add_i32 s16, s17, s16
	s_ashr_i32 s17, s16, 31
	s_lshl_b64 s[16:17], s[16:17], 15
	v_cvt_pk_bf16_f32 v148, v116, v117
	v_lshl_add_u64 v[116:117], v[138:139], 0, s[16:17]
	v_cvt_pk_bf16_f32 v118, v120, v121
	v_cvt_pk_bf16_f32 v119, v122, v123
	v_cvt_pk_bf16_f32 v120, v128, v129
	v_cvt_pk_bf16_f32 v121, v130, v131
	ds_bpermute_b32 v232, v244, v118
	ds_bpermute_b32 v233, v244, v119
	ds_bpermute_b32 v234, v244, v120
	ds_bpermute_b32 v235, v244, v121
	ds_bpermute_b32 v236, v244, v116
	ds_bpermute_b32 v237, v244, v117
	s_waitcnt lgkmcnt(0)
	global_store_dwordx4 v[236:237], v[232:235], off offset:64
	s_ashr_i32 s47, s46, 31
	v_cvt_pk_bf16_f32 v151, v126, v127
	ds_bpermute_b32 v238, v244, v148
	ds_bpermute_b32 v239, v244, v149
	ds_bpermute_b32 v240, v244, v150
	ds_bpermute_b32 v241, v244, v151
	ds_bpermute_b32 v242, v244, v116
	ds_bpermute_b32 v243, v244, v117
	s_waitcnt lgkmcnt(0)
	global_store_dwordx4 v[242:243], v[238:241], off
	s_waitcnt lgkmcnt(0)
	v_add_f32_e32 v118, v124, v125
	v_mov_b32_e32 v119, v118
	s_nop 1
	v_permlane32_swap_b32_e32 v118, v119
	s_and_saveexec_b64 s[48:49], s[38:39]
	s_cbranch_execz .LBB0_1084
	v_ashrrev_i32_e32 v145, 31, v144
	v_add_f32_e32 v120, v118, v119
	v_lshlrev_b64 v[118:119], 7, v[144:145]
	v_lshl_add_u64 v[118:119], s[8:9], 0, v[118:119]
	v_lshl_add_u64 v[118:119], s[46:47], 2, v[118:119]
	s_lshl_b32 s24, s12, 2
	v_lshl_add_u64 v[118:119], v[118:119], 0, s[24:25]
	global_store_dword v[118:119], v120, off
.LBB0_1084:
	s_or_b64 exec, exec, s[48:49]
	v_pk_mul_f32 v[118:119], v[100:101], v[100:101]
	v_pk_mul_f32 v[120:121], v[104:105], v[104:105]
	v_pk_fma_f32 v[118:119], v[98:99], v[98:99], v[118:119]
	v_cvt_pk_bf16_f32 v98, v98, v99
	v_cvt_pk_bf16_f32 v99, v100, v101
	v_cvt_pk_bf16_f32 v100, v102, v103
	v_cvt_pk_bf16_f32 v101, v104, v105
	ds_bpermute_b32 v232, v244, v98
	ds_bpermute_b32 v233, v244, v99
	ds_bpermute_b32 v234, v244, v100
	ds_bpermute_b32 v235, v244, v101
	ds_bpermute_b32 v236, v244, v116
	ds_bpermute_b32 v237, v244, v117
	s_waitcnt lgkmcnt(0)
	global_store_dwordx4 v[236:237], v[232:235], off offset:2048
	v_pk_fma_f32 v[120:121], v[102:103], v[102:103], v[120:121]
	s_nop 0
	v_pk_mul_f32 v[98:99], v[108:109], v[108:109]
	v_pk_mul_f32 v[100:101], v[112:113], v[112:113]
	v_pk_fma_f32 v[98:99], v[106:107], v[106:107], v[98:99]
	v_pk_fma_f32 v[100:101], v[110:111], v[110:111], v[100:101]
	v_pk_add_f32 v[118:119], v[118:119], v[120:121]
	v_pk_add_f32 v[98:99], v[98:99], v[100:101]
	s_nop 0
	v_pk_add_f32 v[100:101], v[118:119], v[98:99]
	v_cvt_pk_bf16_f32 v98, v106, v107
	v_cvt_pk_bf16_f32 v99, v108, v109
	s_nop 0
	v_add_f32_e32 v102, v100, v101
	ds_swizzle_b32 v103, v102 offset:swizzle(SWAP,16)
	v_cvt_pk_bf16_f32 v100, v110, v111
	v_cvt_pk_bf16_f32 v101, v112, v113
	ds_bpermute_b32 v238, v244, v98
	ds_bpermute_b32 v239, v244, v99
	ds_bpermute_b32 v240, v244, v100
	ds_bpermute_b32 v241, v244, v101
	ds_bpermute_b32 v242, v244, v116
	ds_bpermute_b32 v243, v244, v117
	s_waitcnt lgkmcnt(0)
	global_store_dwordx4 v[242:243], v[238:241], off offset:2112
	s_waitcnt lgkmcnt(0)
	s_nop 0
	v_add_f32_e32 v98, v102, v103
	v_mov_b32_e32 v99, v98
	s_nop 1
	v_permlane32_swap_b32_e32 v98, v99
	s_and_saveexec_b64 s[48:49], s[38:39]
	s_cbranch_execz .LBB0_1086
	v_or_b32_e32 v100, 16, v144
	v_ashrrev_i32_e32 v101, 31, v100
	v_add_f32_e32 v102, v98, v99
	v_lshlrev_b64 v[98:99], 7, v[100:101]
	v_lshl_add_u64 v[98:99], s[8:9], 0, v[98:99]
	v_lshl_add_u64 v[98:99], s[46:47], 2, v[98:99]
	s_lshl_b32 s24, s12, 2
	v_lshl_add_u64 v[98:99], v[98:99], 0, s[24:25]
	global_store_dword v[98:99], v102, off
.LBB0_1086:
	s_or_b64 exec, exec, s[48:49]
	v_pk_mul_f32 v[98:99], v[84:85], v[84:85]
	v_pk_mul_f32 v[100:101], v[92:93], v[92:93]
	v_pk_fma_f32 v[98:99], v[82:83], v[82:83], v[98:99]
	v_pk_fma_f32 v[100:101], v[90:91], v[90:91], v[100:101]
	s_nop 0
	v_pk_add_f32 v[102:103], v[98:99], v[100:101]
	v_cvt_pk_bf16_f32 v99, v84, v85
	v_cvt_pk_bf16_f32 v100, v90, v91
	v_pk_mul_f32 v[84:85], v[88:89], v[88:89]
	v_pk_mul_f32 v[90:91], v[96:97], v[96:97]
	v_pk_fma_f32 v[84:85], v[86:87], v[86:87], v[84:85]
	v_pk_fma_f32 v[90:91], v[94:95], v[94:95], v[90:91]
	v_cvt_pk_bf16_f32 v98, v82, v83
	v_add_co_u32_e32 v82, vcc, s73, v116
	v_pk_add_f32 v[84:85], v[84:85], v[90:91]
	s_nop 0
	v_addc_co_u32_e32 v83, vcc, 0, v117, vcc
	v_pk_add_f32 v[90:91], v[102:103], v[84:85]
	v_cvt_pk_bf16_f32 v84, v86, v87
	v_cvt_pk_bf16_f32 v85, v88, v89
	v_cvt_pk_bf16_f32 v86, v94, v95
	v_cvt_pk_bf16_f32 v87, v96, v97
	ds_bpermute_b32 v232, v244, v84
	ds_bpermute_b32 v233, v244, v85
	ds_bpermute_b32 v234, v244, v86
	ds_bpermute_b32 v235, v244, v87
	ds_bpermute_b32 v236, v244, v82
	ds_bpermute_b32 v237, v244, v83
	s_waitcnt lgkmcnt(0)
	global_store_dwordx4 v[236:237], v[232:235], off offset:64
	v_add_f32_e32 v90, v90, v91
	ds_swizzle_b32 v91, v90 offset:swizzle(SWAP,16)
	v_cvt_pk_bf16_f32 v101, v92, v93
	ds_bpermute_b32 v238, v244, v98
	ds_bpermute_b32 v239, v244, v99
	ds_bpermute_b32 v240, v244, v100
	ds_bpermute_b32 v241, v244, v101
	ds_bpermute_b32 v242, v244, v82
	ds_bpermute_b32 v243, v244, v83
	s_waitcnt lgkmcnt(0)
	global_store_dwordx4 v[242:243], v[238:241], off
	s_waitcnt lgkmcnt(0)
	v_add_f32_e32 v84, v90, v91
	v_mov_b32_e32 v85, v84
	s_nop 1
	v_permlane32_swap_b32_e32 v84, v85
	s_and_saveexec_b64 s[48:49], s[38:39]
	s_cbranch_execz .LBB0_1088
	v_or_b32_e32 v86, 32, v144
	v_ashrrev_i32_e32 v87, 31, v86
	v_add_f32_e32 v88, v84, v85
	v_lshlrev_b64 v[84:85], 7, v[86:87]
	v_lshl_add_u64 v[84:85], s[8:9], 0, v[84:85]
	v_lshl_add_u64 v[84:85], s[46:47], 2, v[84:85]
	s_lshl_b32 s24, s12, 2
	v_lshl_add_u64 v[84:85], v[84:85], 0, s[24:25]
	global_store_dword v[84:85], v88, off
.LBB0_1088:
	s_or_b64 exec, exec, s[48:49]
	v_pk_mul_f32 v[84:85], v[60:61], v[60:61]
	v_pk_mul_f32 v[86:87], v[72:73], v[72:73]
	v_pk_fma_f32 v[84:85], v[58:59], v[58:59], v[84:85]
	v_cvt_pk_bf16_f32 v58, v58, v59
	v_cvt_pk_bf16_f32 v59, v60, v61
	v_cvt_pk_bf16_f32 v60, v70, v71
	v_cvt_pk_bf16_f32 v61, v72, v73
	ds_bpermute_b32 v232, v244, v58
	ds_bpermute_b32 v233, v244, v59
	ds_bpermute_b32 v234, v244, v60
	ds_bpermute_b32 v235, v244, v61
	ds_bpermute_b32 v236, v244, v82
	ds_bpermute_b32 v237, v244, v83
	s_waitcnt lgkmcnt(0)
	global_store_dwordx4 v[236:237], v[232:235], off offset:2048
	v_pk_fma_f32 v[86:87], v[70:71], v[70:71], v[86:87]
	s_nop 0
	v_pk_mul_f32 v[58:59], v[76:77], v[76:77]
	v_pk_mul_f32 v[60:61], v[80:81], v[80:81]
	v_pk_fma_f32 v[58:59], v[74:75], v[74:75], v[58:59]
	v_pk_fma_f32 v[60:61], v[78:79], v[78:79], v[60:61]
	v_pk_add_f32 v[84:85], v[84:85], v[86:87]
	v_pk_add_f32 v[58:59], v[58:59], v[60:61]
	s_nop 0
	v_pk_add_f32 v[60:61], v[84:85], v[58:59]
	v_cvt_pk_bf16_f32 v58, v74, v75
	v_cvt_pk_bf16_f32 v59, v76, v77
	s_nop 0
	v_add_f32_e32 v70, v60, v61
	ds_swizzle_b32 v71, v70 offset:swizzle(SWAP,16)
	v_cvt_pk_bf16_f32 v60, v78, v79
	v_cvt_pk_bf16_f32 v61, v80, v81
	ds_bpermute_b32 v238, v244, v58
	ds_bpermute_b32 v239, v244, v59
	ds_bpermute_b32 v240, v244, v60
	ds_bpermute_b32 v241, v244, v61
	ds_bpermute_b32 v242, v244, v82
	ds_bpermute_b32 v243, v244, v83
	s_waitcnt lgkmcnt(0)
	global_store_dwordx4 v[242:243], v[238:241], off offset:2112
	s_waitcnt lgkmcnt(0)
	s_nop 0
	v_add_f32_e32 v58, v70, v71
	v_mov_b32_e32 v59, v58
	s_nop 1
	v_permlane32_swap_b32_e32 v58, v59
	s_and_saveexec_b64 s[48:49], s[38:39]
	s_cbranch_execz .LBB0_1090
	v_or_b32_e32 v60, 48, v144
	v_ashrrev_i32_e32 v61, 31, v60
	v_add_f32_e32 v70, v58, v59
	v_lshlrev_b64 v[58:59], 7, v[60:61]
	v_lshl_add_u64 v[58:59], s[8:9], 0, v[58:59]
	v_lshl_add_u64 v[58:59], s[46:47], 2, v[58:59]
	s_lshl_b32 s24, s12, 2
	v_lshl_add_u64 v[58:59], v[58:59], 0, s[24:25]
	global_store_dword v[58:59], v70, off
.LBB0_1090:
	s_or_b64 exec, exec, s[48:49]
	v_pk_mul_f32 v[58:59], v[52:53], v[52:53]
	v_pk_mul_f32 v[60:61], v[64:65], v[64:65]
	v_pk_fma_f32 v[58:59], v[50:51], v[50:51], v[58:59]
	v_pk_fma_f32 v[60:61], v[62:63], v[62:63], v[60:61]
	s_nop 0
	v_pk_add_f32 v[70:71], v[58:59], v[60:61]
	v_cvt_pk_bf16_f32 v58, v50, v51
	v_add_co_u32_e32 v50, vcc, s72, v116
	v_cvt_pk_bf16_f32 v59, v52, v53
	v_cvt_pk_bf16_f32 v60, v62, v63
	v_cvt_pk_bf16_f32 v61, v64, v65
	v_pk_mul_f32 v[52:53], v[56:57], v[56:57]
	s_nop 0
	v_addc_co_u32_e32 v51, vcc, 0, v117, vcc
	ds_bpermute_b32 v232, v244, v58
	ds_bpermute_b32 v233, v244, v59
	ds_bpermute_b32 v234, v244, v60
	ds_bpermute_b32 v235, v244, v61
	ds_bpermute_b32 v236, v244, v50
	ds_bpermute_b32 v237, v244, v51
	s_waitcnt lgkmcnt(0)
	global_store_dwordx4 v[236:237], v[232:235], off
	v_pk_fma_f32 v[52:53], v[54:55], v[54:55], v[52:53]
	s_nop 0
	v_pk_mul_f32 v[58:59], v[68:69], v[68:69]
	s_nop 0
	v_pk_fma_f32 v[58:59], v[66:67], v[66:67], v[58:59]
	s_nop 0
	v_pk_add_f32 v[52:53], v[52:53], v[58:59]
	s_nop 0
	v_pk_add_f32 v[58:59], v[70:71], v[52:53]
	v_cvt_pk_bf16_f32 v52, v54, v55
	v_cvt_pk_bf16_f32 v53, v56, v57
	v_cvt_pk_bf16_f32 v54, v66, v67
	v_cvt_pk_bf16_f32 v55, v68, v69
	ds_bpermute_b32 v238, v244, v52
	ds_bpermute_b32 v239, v244, v53
	ds_bpermute_b32 v240, v244, v54
	ds_bpermute_b32 v241, v244, v55
	ds_bpermute_b32 v242, v244, v50
	ds_bpermute_b32 v243, v244, v51
	s_waitcnt lgkmcnt(0)
	global_store_dwordx4 v[242:243], v[238:241], off offset:64
	v_add_f32_e32 v58, v58, v59
	ds_swizzle_b32 v59, v58 offset:swizzle(SWAP,16)
	s_waitcnt lgkmcnt(0)
	v_add_f32_e32 v52, v58, v59
	v_mov_b32_e32 v53, v52
	s_nop 1
	v_permlane32_swap_b32_e32 v52, v53
	s_and_saveexec_b64 s[48:49], s[38:39]
	s_cbranch_execz .LBB0_1092
	v_ashrrev_i32_e32 v145, 31, v144
	v_add_f32_e32 v54, v52, v53
	v_lshlrev_b64 v[52:53], 7, v[144:145]
	v_lshl_add_u64 v[52:53], s[8:9], 0, v[52:53]
	v_lshl_add_u64 v[52:53], s[46:47], 2, v[52:53]
	s_lshl_b32 s24, s12, 2
	v_lshl_add_u64 v[52:53], v[52:53], 0, s[24:25]
	v_add_co_u32_e32 v52, vcc, 0x4000, v52
	s_nop 1
	v_addc_co_u32_e32 v53, vcc, 0, v53, vcc
	global_store_dword v[52:53], v54, off
.LBB0_1092:
	s_or_b64 exec, exec, s[48:49]
	v_pk_mul_f32 v[52:53], v[36:37], v[36:37]
	v_pk_mul_f32 v[54:55], v[40:41], v[40:41]
	v_pk_fma_f32 v[52:53], v[34:35], v[34:35], v[52:53]
	v_cvt_pk_bf16_f32 v34, v34, v35
	v_cvt_pk_bf16_f32 v35, v36, v37
	v_cvt_pk_bf16_f32 v36, v38, v39
	v_cvt_pk_bf16_f32 v37, v40, v41
	ds_bpermute_b32 v232, v244, v34
	ds_bpermute_b32 v233, v244, v35
	ds_bpermute_b32 v234, v244, v36
	ds_bpermute_b32 v235, v244, v37
	ds_bpermute_b32 v236, v244, v50
	ds_bpermute_b32 v237, v244, v51
	s_waitcnt lgkmcnt(0)
	global_store_dwordx4 v[236:237], v[232:235], off offset:2048
	v_pk_fma_f32 v[54:55], v[38:39], v[38:39], v[54:55]
	s_nop 0
	v_pk_mul_f32 v[34:35], v[44:45], v[44:45]
	v_pk_mul_f32 v[36:37], v[48:49], v[48:49]
	v_pk_fma_f32 v[34:35], v[42:43], v[42:43], v[34:35]
	v_pk_fma_f32 v[36:37], v[46:47], v[46:47], v[36:37]
	v_pk_add_f32 v[52:53], v[52:53], v[54:55]
	v_pk_add_f32 v[34:35], v[34:35], v[36:37]
	s_nop 0
	v_pk_add_f32 v[36:37], v[52:53], v[34:35]
	v_cvt_pk_bf16_f32 v34, v42, v43
	v_cvt_pk_bf16_f32 v35, v44, v45
	s_nop 0
	v_add_f32_e32 v38, v36, v37
	ds_swizzle_b32 v39, v38 offset:swizzle(SWAP,16)
	v_cvt_pk_bf16_f32 v36, v46, v47
	v_cvt_pk_bf16_f32 v37, v48, v49
	ds_bpermute_b32 v238, v244, v34
	ds_bpermute_b32 v239, v244, v35
	ds_bpermute_b32 v240, v244, v36
	ds_bpermute_b32 v241, v244, v37
	ds_bpermute_b32 v242, v244, v50
	ds_bpermute_b32 v243, v244, v51
	s_waitcnt lgkmcnt(0)
	global_store_dwordx4 v[242:243], v[238:241], off offset:2112
	s_waitcnt lgkmcnt(0)
	s_nop 0
	v_add_f32_e32 v34, v38, v39
	v_mov_b32_e32 v35, v34
	s_nop 1
	v_permlane32_swap_b32_e32 v34, v35
	s_and_saveexec_b64 s[48:49], s[38:39]
	s_cbranch_execz .LBB0_1094
	v_ashrrev_i32_e32 v145, 31, v144
	v_add_f32_e32 v36, v34, v35
	v_lshlrev_b64 v[34:35], 7, v[144:145]
	v_lshl_add_u64 v[34:35], s[8:9], 0, v[34:35]
	v_lshl_add_u64 v[34:35], s[46:47], 2, v[34:35]
	s_lshl_b32 s24, s12, 2
	v_lshl_add_u64 v[34:35], v[34:35], 0, s[24:25]
	v_add_co_u32_e32 v34, vcc, 0x4000, v34
	s_nop 1
	v_addc_co_u32_e32 v35, vcc, 0, v35, vcc
	global_store_dword v[34:35], v36, off offset:2048
.LBB0_1094:
	s_or_b64 exec, exec, s[48:49]
	v_pk_mul_f32 v[34:35], v[20:21], v[20:21]
	v_pk_mul_f32 v[36:37], v[28:29], v[28:29]
	v_pk_fma_f32 v[34:35], v[18:19], v[18:19], v[34:35]
	v_pk_fma_f32 v[36:37], v[26:27], v[26:27], v[36:37]
	s_nop 0
	v_pk_add_f32 v[38:39], v[34:35], v[36:37]
	v_cvt_pk_bf16_f32 v35, v20, v21
	v_cvt_pk_bf16_f32 v36, v26, v27
	v_pk_mul_f32 v[20:21], v[24:25], v[24:25]
	v_pk_mul_f32 v[26:27], v[32:33], v[32:33]
	v_pk_fma_f32 v[20:21], v[22:23], v[22:23], v[20:21]
	v_pk_fma_f32 v[26:27], v[30:31], v[30:31], v[26:27]
	v_cvt_pk_bf16_f32 v34, v18, v19
	v_add_co_u32_e32 v18, vcc, s31, v116
	v_pk_add_f32 v[20:21], v[20:21], v[26:27]
	s_nop 0
	v_addc_co_u32_e32 v19, vcc, 0, v117, vcc
	v_pk_add_f32 v[26:27], v[38:39], v[20:21]
	v_cvt_pk_bf16_f32 v20, v22, v23
	v_cvt_pk_bf16_f32 v21, v24, v25
	v_cvt_pk_bf16_f32 v22, v30, v31
	v_cvt_pk_bf16_f32 v23, v32, v33
	ds_bpermute_b32 v232, v244, v20
	ds_bpermute_b32 v233, v244, v21
	ds_bpermute_b32 v234, v244, v22
	ds_bpermute_b32 v235, v244, v23
	ds_bpermute_b32 v236, v244, v18
	ds_bpermute_b32 v237, v244, v19
	s_waitcnt lgkmcnt(0)
	global_store_dwordx4 v[236:237], v[232:235], off offset:64
	v_add_f32_e32 v26, v26, v27
	ds_swizzle_b32 v27, v26 offset:swizzle(SWAP,16)
	v_cvt_pk_bf16_f32 v37, v28, v29
	ds_bpermute_b32 v238, v244, v34
	ds_bpermute_b32 v239, v244, v35
	ds_bpermute_b32 v240, v244, v36
	ds_bpermute_b32 v241, v244, v37
	ds_bpermute_b32 v242, v244, v18
	ds_bpermute_b32 v243, v244, v19
	s_waitcnt lgkmcnt(0)
	global_store_dwordx4 v[242:243], v[238:241], off
	s_waitcnt lgkmcnt(0)
	v_add_f32_e32 v20, v26, v27
	v_mov_b32_e32 v21, v20
	s_nop 1
	v_permlane32_swap_b32_e32 v20, v21
	s_and_saveexec_b64 s[48:49], s[38:39]
	s_cbranch_execz .LBB0_1096
	v_ashrrev_i32_e32 v145, 31, v144
	v_add_f32_e32 v22, v20, v21
	v_lshlrev_b64 v[20:21], 7, v[144:145]
	v_lshl_add_u64 v[20:21], s[8:9], 0, v[20:21]
	v_lshl_add_u64 v[20:21], s[46:47], 2, v[20:21]
	s_lshl_b32 s24, s12, 2
	v_lshl_add_u64 v[20:21], v[20:21], 0, s[24:25]
	v_add_co_u32_e32 v20, vcc, 0x5000, v20
	s_nop 1
	v_addc_co_u32_e32 v21, vcc, 0, v21, vcc
	global_store_dword v[20:21], v22, off
.LBB0_1096:
	s_or_b64 exec, exec, s[48:49]
	v_pk_mul_f32 v[20:21], v[4:5], v[4:5]
	v_pk_mul_f32 v[22:23], v[8:9], v[8:9]
	v_pk_fma_f32 v[20:21], v[2:3], v[2:3], v[20:21]
	v_cvt_pk_bf16_f32 v2, v2, v3
	v_cvt_pk_bf16_f32 v3, v4, v5
	v_cvt_pk_bf16_f32 v4, v6, v7
	v_cvt_pk_bf16_f32 v5, v8, v9
	ds_bpermute_b32 v232, v244, v2
	ds_bpermute_b32 v233, v244, v3
	ds_bpermute_b32 v234, v244, v4
	ds_bpermute_b32 v235, v244, v5
	ds_bpermute_b32 v236, v244, v18
	ds_bpermute_b32 v237, v244, v19
	s_waitcnt lgkmcnt(0)
	global_store_dwordx4 v[236:237], v[232:235], off offset:2048
	v_pk_fma_f32 v[22:23], v[6:7], v[6:7], v[22:23]
	s_nop 0
	v_pk_mul_f32 v[2:3], v[12:13], v[12:13]
	v_pk_mul_f32 v[4:5], v[16:17], v[16:17]
	v_pk_fma_f32 v[2:3], v[10:11], v[10:11], v[2:3]
	v_pk_fma_f32 v[4:5], v[14:15], v[14:15], v[4:5]
	v_pk_add_f32 v[20:21], v[20:21], v[22:23]
	v_pk_add_f32 v[2:3], v[2:3], v[4:5]
	s_nop 0
	v_pk_add_f32 v[4:5], v[20:21], v[2:3]
	v_cvt_pk_bf16_f32 v2, v10, v11
	v_cvt_pk_bf16_f32 v3, v12, v13
	s_nop 0
	v_add_f32_e32 v6, v4, v5
	ds_swizzle_b32 v7, v6 offset:swizzle(SWAP,16)
	v_cvt_pk_bf16_f32 v4, v14, v15
	v_cvt_pk_bf16_f32 v5, v16, v17
	ds_bpermute_b32 v238, v244, v2
	ds_bpermute_b32 v239, v244, v3
	ds_bpermute_b32 v240, v244, v4
	ds_bpermute_b32 v241, v244, v5
	ds_bpermute_b32 v242, v244, v18
	ds_bpermute_b32 v243, v244, v19
	s_waitcnt lgkmcnt(0)
	global_store_dwordx4 v[242:243], v[238:241], off offset:2112
	s_waitcnt lgkmcnt(0)
	s_nop 0
	v_add_f32_e32 v2, v6, v7
	v_mov_b32_e32 v3, v2
	s_nop 1
	v_permlane32_swap_b32_e32 v2, v3
	s_and_saveexec_b64 s[48:49], s[38:39]
	s_cbranch_execz .LBB0_1098
	v_ashrrev_i32_e32 v145, 31, v144
	v_add_f32_e32 v4, v2, v3
	v_lshlrev_b64 v[2:3], 7, v[144:145]
	v_lshl_add_u64 v[2:3], s[8:9], 0, v[2:3]
	v_lshl_add_u64 v[2:3], s[46:47], 2, v[2:3]
	s_lshl_b32 s24, s12, 2
	v_lshl_add_u64 v[2:3], v[2:3], 0, s[24:25]
	v_add_co_u32_e32 v2, vcc, 0x5000, v2
	s_nop 1
	v_addc_co_u32_e32 v3, vcc, 0, v3, vcc
	global_store_dword v[2:3], v4, off offset:2048

.LBB0_1233:
	v_mbcnt_lo_u32_b32 v244, -1, 0
	v_mbcnt_hi_u32_b32 v244, -1, v244
	v_lshrrev_b32_e32 v245, 2, v244
	v_and_b32_e32 v244, 3, v244
	v_lshl_add_u32 v244, v244, 4, v245
	v_lshlrev_b32_e32 v244, 2, v244
	v_lshl_add_u32 v148, s59, 10, v146
	ds_read2_b32 v[150:151], v148 offset1:16
	s_lshl_b32 s17, s58, 2
	v_med3_f32 v124, v124, 0, v193
	v_med3_f32 v125, v125, 0, v193
	s_lshl_b32 s16, s44, 7
	s_or_b32 s17, s17, s45
	s_waitcnt lgkmcnt(0)
	v_mul_f32_e32 v150, v150, v150
	v_pk_mul_f32 v[124:125], v[124:125], v[124:125]
	s_add_i32 s16, s17, s16
	v_pk_mul_f32 v[152:153], v[124:125], v[150:151] op_sel_hi:[1,0]
	v_med3_f32 v124, v130, 0, v193
	v_med3_f32 v125, v131, 0, v193
	s_ashr_i32 s17, s16, 31
	v_med3_f32 v128, v128, 0, v193
	v_med3_f32 v129, v129, 0, v193
	v_med3_f32 v126, v126, 0, v193
	v_med3_f32 v127, v127, 0, v193
	v_pk_mul_f32 v[124:125], v[124:125], v[124:125]
	s_lshl_b64 s[16:17], s[16:17], 15
	v_pk_mul_f32 v[128:129], v[128:129], v[128:129]
	v_pk_mul_f32 v[130:131], v[124:125], v[150:151] op_sel_hi:[1,0]
	v_pk_mul_f32 v[124:125], v[126:127], v[126:127]
	v_med3_f32 v116, v116, 0, v193
	v_med3_f32 v117, v117, 0, v193
	v_lshl_add_u64 v[144:145], v[138:139], 0, s[16:17]
	v_pk_mul_f32 v[128:129], v[128:129], v[150:151] op_sel_hi:[1,0]
	v_pk_mul_f32 v[154:155], v[124:125], v[150:151] op_sel_hi:[1,0]
	v_cvt_pk_bf16_f32 v124, v128, v129
	v_cvt_pk_bf16_f32 v125, v130, v131
	v_pk_mul_f32 v[116:117], v[116:117], v[116:117]
	v_cvt_pk_bf16_f32 v126, v152, v153
	v_cvt_pk_bf16_f32 v127, v154, v155
	ds_bpermute_b32 v232, v244, v124
	ds_bpermute_b32 v233, v244, v125
	ds_bpermute_b32 v234, v244, v126
	ds_bpermute_b32 v235, v244, v127
	ds_bpermute_b32 v236, v244, v144
	ds_bpermute_b32 v237, v244, v145
	s_waitcnt lgkmcnt(0)
	global_store_dwordx4 v[236:237], v[232:235], off
	v_med3_f32 v120, v120, 0, v193
	v_med3_f32 v121, v121, 0, v193
	v_pk_mul_f32 v[124:125], v[116:117], v[150:151] op_sel_hi:[1,0]
	v_med3_f32 v116, v122, 0, v193
	v_med3_f32 v117, v123, 0, v193
	v_med3_f32 v118, v118, 0, v193
	v_med3_f32 v119, v119, 0, v193
	v_pk_mul_f32 v[116:117], v[116:117], v[116:117]
	v_pk_mul_f32 v[120:121], v[120:121], v[120:121]
	v_pk_mul_f32 v[122:123], v[116:117], v[150:151] op_sel_hi:[1,0]
	v_pk_mul_f32 v[116:117], v[118:119], v[118:119]
	v_pk_mul_f32 v[120:121], v[120:121], v[150:151] op_sel_hi:[1,0]
	v_pk_mul_f32 v[126:127], v[116:117], v[150:151] op_sel_hi:[1,0]
	v_cvt_pk_bf16_f32 v116, v120, v121
	v_med3_f32 v106, v106, 0, v193
	v_med3_f32 v107, v107, 0, v193
	v_cvt_pk_bf16_f32 v117, v122, v123
	v_cvt_pk_bf16_f32 v118, v124, v125
	v_cvt_pk_bf16_f32 v119, v126, v127
	ds_bpermute_b32 v238, v244, v116
	ds_bpermute_b32 v239, v244, v117
	ds_bpermute_b32 v240, v244, v118
	ds_bpermute_b32 v241, v244, v119
	ds_bpermute_b32 v242, v244, v144
	ds_bpermute_b32 v243, v244, v145
	s_waitcnt lgkmcnt(0)
	global_store_dwordx4 v[242:243], v[238:241], off offset:64
	v_pk_mul_f32 v[106:107], v[106:107], v[106:107]
	v_med3_f32 v110, v110, 0, v193
	v_mul_f32_e32 v116, v151, v151
	v_pk_mul_f32 v[118:119], v[106:107], v[116:117] op_sel_hi:[1,0]
	v_med3_f32 v106, v112, 0, v193
	v_med3_f32 v107, v113, 0, v193
	v_med3_f32 v111, v111, 0, v193
	v_med3_f32 v108, v108, 0, v193
	v_med3_f32 v109, v109, 0, v193
	v_pk_mul_f32 v[106:107], v[106:107], v[106:107]
	v_pk_mul_f32 v[110:111], v[110:111], v[110:111]
	v_pk_mul_f32 v[112:113], v[106:107], v[116:117] op_sel_hi:[1,0]
	v_pk_mul_f32 v[106:107], v[108:109], v[108:109]
	v_med3_f32 v98, v98, 0, v193
	v_med3_f32 v99, v99, 0, v193
	v_pk_mul_f32 v[110:111], v[110:111], v[116:117] op_sel_hi:[1,0]
	v_pk_mul_f32 v[120:121], v[106:107], v[116:117] op_sel_hi:[1,0]
	v_cvt_pk_bf16_f32 v106, v110, v111
	v_cvt_pk_bf16_f32 v107, v112, v113
	v_pk_mul_f32 v[98:99], v[98:99], v[98:99]
	v_cvt_pk_bf16_f32 v108, v118, v119
	v_cvt_pk_bf16_f32 v109, v120, v121
	ds_bpermute_b32 v232, v244, v106
	ds_bpermute_b32 v233, v244, v107
	ds_bpermute_b32 v234, v244, v108
	ds_bpermute_b32 v235, v244, v109
	ds_bpermute_b32 v236, v244, v144
	ds_bpermute_b32 v237, v244, v145
	s_waitcnt lgkmcnt(0)
	global_store_dwordx4 v[236:237], v[232:235], off offset:2048
	v_med3_f32 v102, v102, 0, v193
	v_med3_f32 v103, v103, 0, v193
	v_pk_mul_f32 v[106:107], v[98:99], v[116:117] op_sel_hi:[1,0]
	v_med3_f32 v98, v104, 0, v193
	v_med3_f32 v99, v105, 0, v193
	v_pk_mul_f32 v[102:103], v[102:103], v[102:103]
	v_med3_f32 v100, v100, 0, v193
	v_med3_f32 v101, v101, 0, v193
	v_pk_mul_f32 v[98:99], v[98:99], v[98:99]
	v_pk_mul_f32 v[102:103], v[102:103], v[116:117] op_sel_hi:[1,0]
	v_pk_mul_f32 v[104:105], v[98:99], v[116:117] op_sel_hi:[1,0]
	v_pk_mul_f32 v[98:99], v[100:101], v[100:101]
	v_med3_f32 v90, v90, 0, v193
	v_pk_mul_f32 v[108:109], v[98:99], v[116:117] op_sel_hi:[1,0]
	v_cvt_pk_bf16_f32 v98, v102, v103
	ds_read2_b32 v[102:103], v148 offset0:32 offset1:48
	v_med3_f32 v91, v91, 0, v193
	v_cvt_pk_bf16_f32 v99, v104, v105
	v_cvt_pk_bf16_f32 v100, v106, v107
	v_cvt_pk_bf16_f32 v101, v108, v109
	ds_bpermute_b32 v238, v244, v98
	ds_bpermute_b32 v239, v244, v99
	ds_bpermute_b32 v240, v244, v100
	ds_bpermute_b32 v241, v244, v101
	ds_bpermute_b32 v242, v244, v144
	ds_bpermute_b32 v243, v244, v145
	s_waitcnt lgkmcnt(0)
	global_store_dwordx4 v[242:243], v[238:241], off offset:2112
	v_pk_mul_f32 v[90:91], v[90:91], v[90:91]
	v_med3_f32 v94, v94, 0, v193
	s_waitcnt lgkmcnt(0)
	v_mul_f32_e32 v98, v102, v102
	v_med3_f32 v95, v95, 0, v193
	v_pk_mul_f32 v[100:101], v[90:91], v[98:99] op_sel_hi:[1,0]
	v_med3_f32 v90, v96, 0, v193
	v_med3_f32 v91, v97, 0, v193
	v_pk_mul_f32 v[94:95], v[94:95], v[94:95]
	v_med3_f32 v92, v92, 0, v193
	v_med3_f32 v93, v93, 0, v193
	v_pk_mul_f32 v[90:91], v[90:91], v[90:91]
	v_pk_mul_f32 v[94:95], v[94:95], v[98:99] op_sel_hi:[1,0]
	v_pk_mul_f32 v[96:97], v[90:91], v[98:99] op_sel_hi:[1,0]
	v_pk_mul_f32 v[90:91], v[92:93], v[92:93]
	v_med3_f32 v82, v82, 0, v193
	v_pk_mul_f32 v[104:105], v[90:91], v[98:99] op_sel_hi:[1,0]
	v_cvt_pk_bf16_f32 v90, v94, v95
	v_add_co_u32_e32 v94, vcc, s73, v144
	v_med3_f32 v83, v83, 0, v193
	v_cvt_pk_bf16_f32 v91, v96, v97
	s_nop 0
	v_addc_co_u32_e32 v95, vcc, 0, v145, vcc
	v_pk_mul_f32 v[82:83], v[82:83], v[82:83]
	v_cvt_pk_bf16_f32 v92, v100, v101
	v_cvt_pk_bf16_f32 v93, v104, v105
	ds_bpermute_b32 v232, v244, v90
	ds_bpermute_b32 v233, v244, v91
	ds_bpermute_b32 v234, v244, v92
	ds_bpermute_b32 v235, v244, v93
	ds_bpermute_b32 v236, v244, v94
	ds_bpermute_b32 v237, v244, v95
	s_waitcnt lgkmcnt(0)
	global_store_dwordx4 v[236:237], v[232:235], off
	v_med3_f32 v86, v86, 0, v193
	v_med3_f32 v87, v87, 0, v193
	v_pk_mul_f32 v[90:91], v[82:83], v[98:99] op_sel_hi:[1,0]
	v_med3_f32 v82, v88, 0, v193
	v_med3_f32 v83, v89, 0, v193
	v_med3_f32 v84, v84, 0, v193
	v_med3_f32 v85, v85, 0, v193
	v_pk_mul_f32 v[82:83], v[82:83], v[82:83]
	v_pk_mul_f32 v[86:87], v[86:87], v[86:87]
	v_pk_mul_f32 v[88:89], v[82:83], v[98:99] op_sel_hi:[1,0]
	v_pk_mul_f32 v[82:83], v[84:85], v[84:85]
	v_pk_mul_f32 v[86:87], v[86:87], v[98:99] op_sel_hi:[1,0]
	v_pk_mul_f32 v[92:93], v[82:83], v[98:99] op_sel_hi:[1,0]
	v_cvt_pk_bf16_f32 v82, v86, v87
	v_med3_f32 v74, v74, 0, v193
	v_med3_f32 v75, v75, 0, v193
	v_cvt_pk_bf16_f32 v83, v88, v89
	v_cvt_pk_bf16_f32 v84, v90, v91
	v_cvt_pk_bf16_f32 v85, v92, v93
	ds_bpermute_b32 v238, v244, v82
	ds_bpermute_b32 v239, v244, v83
	ds_bpermute_b32 v240, v244, v84
	ds_bpermute_b32 v241, v244, v85
	ds_bpermute_b32 v242, v244, v94
	ds_bpermute_b32 v243, v244, v95
	s_waitcnt lgkmcnt(0)
	global_store_dwordx4 v[242:243], v[238:241], off offset:64
	v_pk_mul_f32 v[74:75], v[74:75], v[74:75]
	v_med3_f32 v78, v78, 0, v193
	v_mul_f32_e32 v82, v103, v103
	v_pk_mul_f32 v[84:85], v[74:75], v[82:83] op_sel_hi:[1,0]
	v_med3_f32 v74, v80, 0, v193
	v_med3_f32 v75, v81, 0, v193
	v_med3_f32 v79, v79, 0, v193
	v_med3_f32 v76, v76, 0, v193
	v_med3_f32 v77, v77, 0, v193
	v_pk_mul_f32 v[74:75], v[74:75], v[74:75]
	v_pk_mul_f32 v[78:79], v[78:79], v[78:79]
	v_pk_mul_f32 v[80:81], v[74:75], v[82:83] op_sel_hi:[1,0]
	v_pk_mul_f32 v[74:75], v[76:77], v[76:77]
	v_med3_f32 v66, v66, 0, v193
	v_med3_f32 v67, v67, 0, v193
	v_pk_mul_f32 v[78:79], v[78:79], v[82:83] op_sel_hi:[1,0]
	v_pk_mul_f32 v[86:87], v[74:75], v[82:83] op_sel_hi:[1,0]
	v_cvt_pk_bf16_f32 v74, v78, v79
	v_cvt_pk_bf16_f32 v75, v80, v81
	v_pk_mul_f32 v[66:67], v[66:67], v[66:67]
	v_cvt_pk_bf16_f32 v76, v84, v85
	v_cvt_pk_bf16_f32 v77, v86, v87
	ds_bpermute_b32 v232, v244, v74
	ds_bpermute_b32 v233, v244, v75
	ds_bpermute_b32 v234, v244, v76
	ds_bpermute_b32 v235, v244, v77
	ds_bpermute_b32 v236, v244, v94
	ds_bpermute_b32 v237, v244, v95
	s_waitcnt lgkmcnt(0)
	global_store_dwordx4 v[236:237], v[232:235], off offset:2048
	v_med3_f32 v70, v70, 0, v193
	v_med3_f32 v71, v71, 0, v193
	v_pk_mul_f32 v[74:75], v[66:67], v[82:83] op_sel_hi:[1,0]
	v_med3_f32 v66, v72, 0, v193
	v_med3_f32 v67, v73, 0, v193
	v_pk_mul_f32 v[70:71], v[70:71], v[70:71]
	v_med3_f32 v68, v68, 0, v193
	v_med3_f32 v69, v69, 0, v193
	v_pk_mul_f32 v[66:67], v[66:67], v[66:67]
	v_pk_mul_f32 v[70:71], v[70:71], v[82:83] op_sel_hi:[1,0]
	v_pk_mul_f32 v[72:73], v[66:67], v[82:83] op_sel_hi:[1,0]
	v_pk_mul_f32 v[66:67], v[68:69], v[68:69]
	v_med3_f32 v64, v64, 0, v193
	v_pk_mul_f32 v[76:77], v[66:67], v[82:83] op_sel_hi:[1,0]
	v_cvt_pk_bf16_f32 v66, v70, v71
	ds_read2_b32 v[70:71], v148 offset0:128 offset1:144
	v_med3_f32 v65, v65, 0, v193
	v_cvt_pk_bf16_f32 v67, v72, v73
	v_cvt_pk_bf16_f32 v68, v74, v75
	v_cvt_pk_bf16_f32 v69, v76, v77
	ds_bpermute_b32 v238, v244, v66
	ds_bpermute_b32 v239, v244, v67
	ds_bpermute_b32 v240, v244, v68
	ds_bpermute_b32 v241, v244, v69
	ds_bpermute_b32 v242, v244, v94
	ds_bpermute_b32 v243, v244, v95
	s_waitcnt lgkmcnt(0)
	global_store_dwordx4 v[242:243], v[238:241], off offset:2112
	v_med3_f32 v60, v60, 0, v193
	v_med3_f32 v61, v61, 0, v193
	s_waitcnt lgkmcnt(0)
	v_mul_f32_e32 v66, v70, v70
	v_pk_mul_f32 v[64:65], v[64:65], v[64:65]
	v_med3_f32 v62, v62, 0, v193
	v_med3_f32 v63, v63, 0, v193
	v_med3_f32 v58, v58, 0, v193
	v_med3_f32 v59, v59, 0, v193
	v_pk_mul_f32 v[64:65], v[64:65], v[66:67] op_sel_hi:[1,0]
	v_pk_mul_f32 v[60:61], v[60:61], v[60:61]
	v_pk_mul_f32 v[62:63], v[62:63], v[62:63]
	v_pk_mul_f32 v[58:59], v[58:59], v[58:59]
	v_pk_mul_f32 v[68:69], v[60:61], v[66:67] op_sel_hi:[1,0]
	v_cvt_pk_bf16_f32 v61, v64, v65
	v_add_co_u32_e32 v64, vcc, s72, v144
	v_pk_mul_f32 v[62:63], v[62:63], v[66:67] op_sel_hi:[1,0]
	v_pk_mul_f32 v[58:59], v[58:59], v[66:67] op_sel_hi:[1,0]
	v_addc_co_u32_e32 v65, vcc, 0, v145, vcc
	v_cvt_pk_bf16_f32 v60, v62, v63
	v_cvt_pk_bf16_f32 v62, v58, v59
	v_add_co_u32_e32 v58, vcc, s31, v144
	v_med3_f32 v50, v50, 0, v193
	v_med3_f32 v51, v51, 0, v193
	v_addc_co_u32_e32 v59, vcc, 0, v145, vcc
	v_pk_mul_f32 v[50:51], v[50:51], v[50:51]
	v_cvt_pk_bf16_f32 v63, v68, v69
	ds_bpermute_b32 v232, v244, v60
	ds_bpermute_b32 v233, v244, v61
	ds_bpermute_b32 v234, v244, v62
	ds_bpermute_b32 v235, v244, v63
	ds_bpermute_b32 v236, v244, v58
	ds_bpermute_b32 v237, v244, v59
	s_waitcnt lgkmcnt(0)
	global_store_dwordx4 v[236:237], v[232:235], off offset:-4096
	v_med3_f32 v54, v54, 0, v193
	v_med3_f32 v55, v55, 0, v193
	v_pk_mul_f32 v[60:61], v[50:51], v[66:67] op_sel_hi:[1,0]
	v_med3_f32 v50, v56, 0, v193
	v_med3_f32 v51, v57, 0, v193
	v_med3_f32 v52, v52, 0, v193
	v_med3_f32 v53, v53, 0, v193
	v_pk_mul_f32 v[50:51], v[50:51], v[50:51]
	v_pk_mul_f32 v[54:55], v[54:55], v[54:55]
	v_pk_mul_f32 v[56:57], v[50:51], v[66:67] op_sel_hi:[1,0]
	v_pk_mul_f32 v[50:51], v[52:53], v[52:53]
	v_pk_mul_f32 v[54:55], v[54:55], v[66:67] op_sel_hi:[1,0]
	v_pk_mul_f32 v[62:63], v[50:51], v[66:67] op_sel_hi:[1,0]
	v_cvt_pk_bf16_f32 v50, v54, v55
	v_med3_f32 v42, v42, 0, v193
	v_med3_f32 v43, v43, 0, v193
	v_cvt_pk_bf16_f32 v51, v56, v57
	v_cvt_pk_bf16_f32 v52, v60, v61
	v_cvt_pk_bf16_f32 v53, v62, v63
	ds_bpermute_b32 v238, v244, v50
	ds_bpermute_b32 v239, v244, v51
	ds_bpermute_b32 v240, v244, v52
	ds_bpermute_b32 v241, v244, v53
	ds_bpermute_b32 v242, v244, v64
	ds_bpermute_b32 v243, v244, v65
	s_waitcnt lgkmcnt(0)
	global_store_dwordx4 v[242:243], v[238:241], off offset:64
	v_pk_mul_f32 v[42:43], v[42:43], v[42:43]
	v_med3_f32 v46, v46, 0, v193
	v_mul_f32_e32 v50, v71, v71
	v_pk_mul_f32 v[52:53], v[42:43], v[50:51] op_sel_hi:[1,0]
	v_med3_f32 v42, v48, 0, v193
	v_med3_f32 v43, v49, 0, v193
	v_med3_f32 v47, v47, 0, v193
	v_med3_f32 v44, v44, 0, v193
	v_med3_f32 v45, v45, 0, v193
	v_pk_mul_f32 v[42:43], v[42:43], v[42:43]
	v_pk_mul_f32 v[46:47], v[46:47], v[46:47]
	v_pk_mul_f32 v[48:49], v[42:43], v[50:51] op_sel_hi:[1,0]
	v_pk_mul_f32 v[42:43], v[44:45], v[44:45]
	v_med3_f32 v34, v34, 0, v193
	v_med3_f32 v35, v35, 0, v193
	v_pk_mul_f32 v[46:47], v[46:47], v[50:51] op_sel_hi:[1,0]
	v_pk_mul_f32 v[54:55], v[42:43], v[50:51] op_sel_hi:[1,0]
	v_cvt_pk_bf16_f32 v42, v46, v47
	v_cvt_pk_bf16_f32 v43, v48, v49
	v_pk_mul_f32 v[34:35], v[34:35], v[34:35]
	v_cvt_pk_bf16_f32 v44, v52, v53
	v_cvt_pk_bf16_f32 v45, v54, v55
	ds_bpermute_b32 v232, v244, v42
	ds_bpermute_b32 v233, v244, v43
	ds_bpermute_b32 v234, v244, v44
	ds_bpermute_b32 v235, v244, v45
	ds_bpermute_b32 v236, v244, v64
	ds_bpermute_b32 v237, v244, v65
	s_waitcnt lgkmcnt(0)
	global_store_dwordx4 v[236:237], v[232:235], off offset:2048
	v_med3_f32 v38, v38, 0, v193
	v_med3_f32 v39, v39, 0, v193
	v_pk_mul_f32 v[42:43], v[34:35], v[50:51] op_sel_hi:[1,0]
	v_med3_f32 v34, v40, 0, v193
	v_med3_f32 v35, v41, 0, v193
	v_pk_mul_f32 v[38:39], v[38:39], v[38:39]
	v_med3_f32 v36, v36, 0, v193
	v_med3_f32 v37, v37, 0, v193
	v_pk_mul_f32 v[34:35], v[34:35], v[34:35]
	v_pk_mul_f32 v[38:39], v[38:39], v[50:51] op_sel_hi:[1,0]
	v_pk_mul_f32 v[40:41], v[34:35], v[50:51] op_sel_hi:[1,0]
	v_pk_mul_f32 v[34:35], v[36:37], v[36:37]
	v_med3_f32 v26, v26, 0, v193
	v_pk_mul_f32 v[44:45], v[34:35], v[50:51] op_sel_hi:[1,0]
	v_cvt_pk_bf16_f32 v34, v38, v39
	ds_read2_b32 v[38:39], v148 offset0:160 offset1:176
	v_med3_f32 v27, v27, 0, v193
	v_cvt_pk_bf16_f32 v35, v40, v41
	v_cvt_pk_bf16_f32 v36, v42, v43
	v_cvt_pk_bf16_f32 v37, v44, v45
	ds_bpermute_b32 v238, v244, v34
	ds_bpermute_b32 v239, v244, v35
	ds_bpermute_b32 v240, v244, v36
	ds_bpermute_b32 v241, v244, v37
	ds_bpermute_b32 v242, v244, v64
	ds_bpermute_b32 v243, v244, v65
	s_waitcnt lgkmcnt(0)
	global_store_dwordx4 v[242:243], v[238:241], off offset:2112
	v_pk_mul_f32 v[26:27], v[26:27], v[26:27]
	v_med3_f32 v30, v30, 0, v193
	s_waitcnt lgkmcnt(0)
	v_mul_f32_e32 v34, v38, v38
	v_pk_mul_f32 v[36:37], v[26:27], v[34:35] op_sel_hi:[1,0]
	v_med3_f32 v26, v32, 0, v193
	v_med3_f32 v27, v33, 0, v193
	v_med3_f32 v31, v31, 0, v193
	v_med3_f32 v28, v28, 0, v193
	v_med3_f32 v29, v29, 0, v193
	v_pk_mul_f32 v[26:27], v[26:27], v[26:27]
	v_pk_mul_f32 v[30:31], v[30:31], v[30:31]
	v_pk_mul_f32 v[32:33], v[26:27], v[34:35] op_sel_hi:[1,0]
	v_pk_mul_f32 v[26:27], v[28:29], v[28:29]
	v_med3_f32 v18, v18, 0, v193
	v_med3_f32 v19, v19, 0, v193
	v_pk_mul_f32 v[30:31], v[30:31], v[34:35] op_sel_hi:[1,0]
	v_pk_mul_f32 v[40:41], v[26:27], v[34:35] op_sel_hi:[1,0]
	v_cvt_pk_bf16_f32 v26, v30, v31
	v_cvt_pk_bf16_f32 v27, v32, v33
	v_pk_mul_f32 v[18:19], v[18:19], v[18:19]
	v_cvt_pk_bf16_f32 v28, v36, v37
	v_cvt_pk_bf16_f32 v29, v40, v41
	ds_bpermute_b32 v232, v244, v26
	ds_bpermute_b32 v233, v244, v27
	ds_bpermute_b32 v234, v244, v28
	ds_bpermute_b32 v235, v244, v29
	ds_bpermute_b32 v236, v244, v58
	ds_bpermute_b32 v237, v244, v59
	s_waitcnt lgkmcnt(0)
	global_store_dwordx4 v[236:237], v[232:235], off
	v_med3_f32 v22, v22, 0, v193
	v_med3_f32 v23, v23, 0, v193
	v_pk_mul_f32 v[26:27], v[18:19], v[34:35] op_sel_hi:[1,0]
	v_med3_f32 v18, v24, 0, v193
	v_med3_f32 v19, v25, 0, v193
	v_med3_f32 v20, v20, 0, v193
	v_med3_f32 v21, v21, 0, v193
	v_pk_mul_f32 v[18:19], v[18:19], v[18:19]
	v_pk_mul_f32 v[22:23], v[22:23], v[22:23]
	v_pk_mul_f32 v[24:25], v[18:19], v[34:35] op_sel_hi:[1,0]
	v_pk_mul_f32 v[18:19], v[20:21], v[20:21]
	v_pk_mul_f32 v[22:23], v[22:23], v[34:35] op_sel_hi:[1,0]
	v_pk_mul_f32 v[28:29], v[18:19], v[34:35] op_sel_hi:[1,0]
	v_cvt_pk_bf16_f32 v18, v22, v23
	v_med3_f32 v10, v10, 0, v193
	v_med3_f32 v11, v11, 0, v193
	v_cvt_pk_bf16_f32 v19, v24, v25
	v_cvt_pk_bf16_f32 v20, v26, v27
	v_cvt_pk_bf16_f32 v21, v28, v29
	ds_bpermute_b32 v238, v244, v18
	ds_bpermute_b32 v239, v244, v19
	ds_bpermute_b32 v240, v244, v20
	ds_bpermute_b32 v241, v244, v21
	ds_bpermute_b32 v242, v244, v58
	ds_bpermute_b32 v243, v244, v59
	s_waitcnt lgkmcnt(0)
	global_store_dwordx4 v[242:243], v[238:241], off offset:64
	v_pk_mul_f32 v[10:11], v[10:11], v[10:11]
	v_med3_f32 v14, v14, 0, v193
	v_mul_f32_e32 v18, v39, v39
	v_pk_mul_f32 v[20:21], v[10:11], v[18:19] op_sel_hi:[1,0]
	v_med3_f32 v10, v16, 0, v193
	v_med3_f32 v11, v17, 0, v193
	v_med3_f32 v15, v15, 0, v193
	v_med3_f32 v12, v12, 0, v193
	v_med3_f32 v13, v13, 0, v193
	v_pk_mul_f32 v[10:11], v[10:11], v[10:11]
	v_pk_mul_f32 v[14:15], v[14:15], v[14:15]
	v_pk_mul_f32 v[16:17], v[10:11], v[18:19] op_sel_hi:[1,0]
	v_pk_mul_f32 v[10:11], v[12:13], v[12:13]
	v_med3_f32 v2, v2, 0, v193
	v_med3_f32 v3, v3, 0, v193
	v_pk_mul_f32 v[14:15], v[14:15], v[18:19] op_sel_hi:[1,0]
	v_pk_mul_f32 v[22:23], v[10:11], v[18:19] op_sel_hi:[1,0]
	v_cvt_pk_bf16_f32 v10, v14, v15
	v_cvt_pk_bf16_f32 v11, v16, v17
	v_pk_mul_f32 v[2:3], v[2:3], v[2:3]
	v_cvt_pk_bf16_f32 v12, v20, v21
	v_cvt_pk_bf16_f32 v13, v22, v23
	ds_bpermute_b32 v232, v244, v10
	ds_bpermute_b32 v233, v244, v11
	ds_bpermute_b32 v234, v244, v12
	ds_bpermute_b32 v235, v244, v13
	ds_bpermute_b32 v236, v244, v58
	ds_bpermute_b32 v237, v244, v59
	s_waitcnt lgkmcnt(0)
	global_store_dwordx4 v[236:237], v[232:235], off offset:2048
	v_med3_f32 v6, v6, 0, v193
	v_med3_f32 v7, v7, 0, v193
	v_pk_mul_f32 v[10:11], v[2:3], v[18:19] op_sel_hi:[1,0]
	v_med3_f32 v2, v8, 0, v193
	v_med3_f32 v3, v9, 0, v193
	v_med3_f32 v4, v4, 0, v193
	v_med3_f32 v5, v5, 0, v193
	v_pk_mul_f32 v[2:3], v[2:3], v[2:3]
	v_pk_mul_f32 v[6:7], v[6:7], v[6:7]
	v_pk_mul_f32 v[8:9], v[2:3], v[18:19] op_sel_hi:[1,0]
	v_pk_mul_f32 v[2:3], v[4:5], v[4:5]
	s_andn2_b64 vcc, exec, s[38:39]
	s_mov_b64 s[38:39], -1
	v_pk_mul_f32 v[6:7], v[6:7], v[18:19] op_sel_hi:[1,0]
	v_pk_mul_f32 v[12:13], v[2:3], v[18:19] op_sel_hi:[1,0]
	v_cvt_pk_bf16_f32 v2, v6, v7
	v_cvt_pk_bf16_f32 v3, v8, v9
	v_cvt_pk_bf16_f32 v4, v10, v11
	s_nop 0
	v_cvt_pk_bf16_f32 v5, v12, v13
	ds_bpermute_b32 v238, v244, v2
	ds_bpermute_b32 v239, v244, v3
	ds_bpermute_b32 v240, v244, v4
	ds_bpermute_b32 v241, v244, v5
	ds_bpermute_b32 v242, v244, v58
	ds_bpermute_b32 v243, v244, v59
	s_waitcnt lgkmcnt(0)
	global_store_dwordx4 v[242:243], v[238:241], off offset:2112
	s_cbranch_vccnz .LBB0_1222
	s_andn2_b64 vcc, exec, s[0:1]
	s_cbranch_vccnz .LBB0_1221
	s_barrier
	s_branch .LBB0_1221

.LBB0_1337:
	v_mbcnt_lo_u32_b32 v244, -1, 0
	v_mbcnt_hi_u32_b32 v244, -1, v244
	v_lshrrev_b32_e32 v245, 2, v244
	v_and_b32_e32 v244, 3, v244
	v_lshl_add_u32 v244, v244, 4, v245
	v_lshlrev_b32_e32 v244, 2, v244
	v_pk_mul_f32 v[148:149], v[118:119], v[118:119]
	v_pk_mul_f32 v[150:151], v[126:127], v[126:127]
	v_pk_fma_f32 v[148:149], v[116:117], v[116:117], v[148:149]
	v_pk_fma_f32 v[150:151], v[124:125], v[124:125], v[150:151]
	v_lshl_add_u32 v144, s46, 8, v1
	v_pk_add_f32 v[152:153], v[148:149], v[150:151]
	v_cvt_pk_bf16_f32 v149, v118, v119
	v_cvt_pk_bf16_f32 v150, v124, v125
	v_pk_mul_f32 v[118:119], v[122:123], v[122:123]
	v_pk_mul_f32 v[124:125], v[130:131], v[130:131]
	v_pk_fma_f32 v[118:119], v[120:121], v[120:121], v[118:119]
	v_pk_fma_f32 v[124:125], v[128:129], v[128:129], v[124:125]
	s_lshl_b32 s16, s46, 5
	v_pk_add_f32 v[118:119], v[118:119], v[124:125]
	s_lshl_b32 s46, s48, 2
	v_pk_add_f32 v[124:125], v[152:153], v[118:119]
	s_or_b32 s17, s46, s14
	v_add_f32_e32 v124, v124, v125
	ds_swizzle_b32 v125, v124 offset:swizzle(SWAP,16)
	s_add_i32 s16, s17, s16
	s_ashr_i32 s17, s16, 31
	s_lshl_b64 s[16:17], s[16:17], 15
	v_cvt_pk_bf16_f32 v148, v116, v117
	v_lshl_add_u64 v[116:117], v[138:139], 0, s[16:17]
	v_cvt_pk_bf16_f32 v118, v120, v121
	v_cvt_pk_bf16_f32 v119, v122, v123
	v_cvt_pk_bf16_f32 v120, v128, v129
	v_cvt_pk_bf16_f32 v121, v130, v131
	ds_bpermute_b32 v232, v244, v118
	ds_bpermute_b32 v233, v244, v119
	ds_bpermute_b32 v234, v244, v120
	ds_bpermute_b32 v235, v244, v121
	ds_bpermute_b32 v236, v244, v116
	ds_bpermute_b32 v237, v244, v117
	s_waitcnt lgkmcnt(0)
	global_store_dwordx4 v[236:237], v[232:235], off offset:64
	s_ashr_i32 s47, s46, 31
	v_cvt_pk_bf16_f32 v151, v126, v127
	ds_bpermute_b32 v238, v244, v148
	ds_bpermute_b32 v239, v244, v149
	ds_bpermute_b32 v240, v244, v150
	ds_bpermute_b32 v241, v244, v151
	ds_bpermute_b32 v242, v244, v116
	ds_bpermute_b32 v243, v244, v117
	s_waitcnt lgkmcnt(0)
	global_store_dwordx4 v[242:243], v[238:241], off
	s_waitcnt lgkmcnt(0)
	v_add_f32_e32 v118, v124, v125
	v_mov_b32_e32 v119, v118
	s_nop 1
	v_permlane32_swap_b32_e32 v118, v119
	s_and_saveexec_b64 s[48:49], s[38:39]
	s_cbranch_execz .LBB0_1339
	v_ashrrev_i32_e32 v145, 31, v144
	v_add_f32_e32 v120, v118, v119
	v_lshlrev_b64 v[118:119], 7, v[144:145]
	v_lshl_add_u64 v[118:119], s[8:9], 0, v[118:119]
	v_lshl_add_u64 v[118:119], s[46:47], 2, v[118:119]
	s_lshl_b32 s24, s14, 2
	v_lshl_add_u64 v[118:119], v[118:119], 0, s[24:25]
	global_store_dword v[118:119], v120, off
.LBB0_1339:
	s_or_b64 exec, exec, s[48:49]
	v_pk_mul_f32 v[118:119], v[100:101], v[100:101]
	v_pk_mul_f32 v[120:121], v[104:105], v[104:105]
	v_pk_fma_f32 v[118:119], v[98:99], v[98:99], v[118:119]
	v_cvt_pk_bf16_f32 v98, v98, v99
	v_cvt_pk_bf16_f32 v99, v100, v101
	v_cvt_pk_bf16_f32 v100, v102, v103
	v_cvt_pk_bf16_f32 v101, v104, v105
	ds_bpermute_b32 v232, v244, v98
	ds_bpermute_b32 v233, v244, v99
	ds_bpermute_b32 v234, v244, v100
	ds_bpermute_b32 v235, v244, v101
	ds_bpermute_b32 v236, v244, v116
	ds_bpermute_b32 v237, v244, v117
	s_waitcnt lgkmcnt(0)
	global_store_dwordx4 v[236:237], v[232:235], off offset:2048
	v_pk_fma_f32 v[120:121], v[102:103], v[102:103], v[120:121]
	s_nop 0
	v_pk_mul_f32 v[98:99], v[108:109], v[108:109]
	v_pk_mul_f32 v[100:101], v[112:113], v[112:113]
	v_pk_fma_f32 v[98:99], v[106:107], v[106:107], v[98:99]
	v_pk_fma_f32 v[100:101], v[110:111], v[110:111], v[100:101]
	v_pk_add_f32 v[118:119], v[118:119], v[120:121]
	v_pk_add_f32 v[98:99], v[98:99], v[100:101]
	s_nop 0
	v_pk_add_f32 v[100:101], v[118:119], v[98:99]
	v_cvt_pk_bf16_f32 v98, v106, v107
	v_cvt_pk_bf16_f32 v99, v108, v109
	s_nop 0
	v_add_f32_e32 v102, v100, v101
	ds_swizzle_b32 v103, v102 offset:swizzle(SWAP,16)
	v_cvt_pk_bf16_f32 v100, v110, v111
	v_cvt_pk_bf16_f32 v101, v112, v113
	ds_bpermute_b32 v238, v244, v98
	ds_bpermute_b32 v239, v244, v99
	ds_bpermute_b32 v240, v244, v100
	ds_bpermute_b32 v241, v244, v101
	ds_bpermute_b32 v242, v244, v116
	ds_bpermute_b32 v243, v244, v117
	s_waitcnt lgkmcnt(0)
	global_store_dwordx4 v[242:243], v[238:241], off offset:2112
	s_waitcnt lgkmcnt(0)
	s_nop 0
	v_add_f32_e32 v98, v102, v103
	v_mov_b32_e32 v99, v98
	s_nop 1
	v_permlane32_swap_b32_e32 v98, v99
	s_and_saveexec_b64 s[48:49], s[38:39]
	s_cbranch_execz .LBB0_1341
	v_or_b32_e32 v100, 16, v144
	v_ashrrev_i32_e32 v101, 31, v100
	v_add_f32_e32 v102, v98, v99
	v_lshlrev_b64 v[98:99], 7, v[100:101]
	v_lshl_add_u64 v[98:99], s[8:9], 0, v[98:99]
	v_lshl_add_u64 v[98:99], s[46:47], 2, v[98:99]
	s_lshl_b32 s24, s14, 2
	v_lshl_add_u64 v[98:99], v[98:99], 0, s[24:25]
	global_store_dword v[98:99], v102, off
.LBB0_1341:
	s_or_b64 exec, exec, s[48:49]
	v_pk_mul_f32 v[98:99], v[84:85], v[84:85]
	v_pk_mul_f32 v[100:101], v[92:93], v[92:93]
	v_pk_fma_f32 v[98:99], v[82:83], v[82:83], v[98:99]
	v_pk_fma_f32 v[100:101], v[90:91], v[90:91], v[100:101]
	s_nop 0
	v_pk_add_f32 v[102:103], v[98:99], v[100:101]
	v_cvt_pk_bf16_f32 v99, v84, v85
	v_cvt_pk_bf16_f32 v100, v90, v91
	v_pk_mul_f32 v[84:85], v[88:89], v[88:89]
	v_pk_mul_f32 v[90:91], v[96:97], v[96:97]
	v_pk_fma_f32 v[84:85], v[86:87], v[86:87], v[84:85]
	v_pk_fma_f32 v[90:91], v[94:95], v[94:95], v[90:91]
	v_cvt_pk_bf16_f32 v98, v82, v83
	v_add_co_u32_e32 v82, vcc, s73, v116
	v_pk_add_f32 v[84:85], v[84:85], v[90:91]
	s_nop 0
	v_addc_co_u32_e32 v83, vcc, 0, v117, vcc
	v_pk_add_f32 v[90:91], v[102:103], v[84:85]
	v_cvt_pk_bf16_f32 v84, v86, v87
	v_cvt_pk_bf16_f32 v85, v88, v89
	v_cvt_pk_bf16_f32 v86, v94, v95
	v_cvt_pk_bf16_f32 v87, v96, v97
	ds_bpermute_b32 v232, v244, v84
	ds_bpermute_b32 v233, v244, v85
	ds_bpermute_b32 v234, v244, v86
	ds_bpermute_b32 v235, v244, v87
	ds_bpermute_b32 v236, v244, v82
	ds_bpermute_b32 v237, v244, v83
	s_waitcnt lgkmcnt(0)
	global_store_dwordx4 v[236:237], v[232:235], off offset:64
	v_add_f32_e32 v90, v90, v91
	ds_swizzle_b32 v91, v90 offset:swizzle(SWAP,16)
	v_cvt_pk_bf16_f32 v101, v92, v93
	ds_bpermute_b32 v238, v244, v98
	ds_bpermute_b32 v239, v244, v99
	ds_bpermute_b32 v240, v244, v100
	ds_bpermute_b32 v241, v244, v101
	ds_bpermute_b32 v242, v244, v82
	ds_bpermute_b32 v243, v244, v83
	s_waitcnt lgkmcnt(0)
	global_store_dwordx4 v[242:243], v[238:241], off
	s_waitcnt lgkmcnt(0)
	v_add_f32_e32 v84, v90, v91
	v_mov_b32_e32 v85, v84
	s_nop 1
	v_permlane32_swap_b32_e32 v84, v85
	s_and_saveexec_b64 s[48:49], s[38:39]
	s_cbranch_execz .LBB0_1343
	v_or_b32_e32 v86, 32, v144
	v_ashrrev_i32_e32 v87, 31, v86
	v_add_f32_e32 v88, v84, v85
	v_lshlrev_b64 v[84:85], 7, v[86:87]
	v_lshl_add_u64 v[84:85], s[8:9], 0, v[84:85]
	v_lshl_add_u64 v[84:85], s[46:47], 2, v[84:85]
	s_lshl_b32 s24, s14, 2
	v_lshl_add_u64 v[84:85], v[84:85], 0, s[24:25]
	global_store_dword v[84:85], v88, off
.LBB0_1343:
	s_or_b64 exec, exec, s[48:49]
	v_pk_mul_f32 v[84:85], v[60:61], v[60:61]
	v_pk_mul_f32 v[86:87], v[72:73], v[72:73]
	v_pk_fma_f32 v[84:85], v[58:59], v[58:59], v[84:85]
	v_cvt_pk_bf16_f32 v58, v58, v59
	v_cvt_pk_bf16_f32 v59, v60, v61
	v_cvt_pk_bf16_f32 v60, v70, v71
	v_cvt_pk_bf16_f32 v61, v72, v73
	ds_bpermute_b32 v232, v244, v58
	ds_bpermute_b32 v233, v244, v59
	ds_bpermute_b32 v234, v244, v60
	ds_bpermute_b32 v235, v244, v61
	ds_bpermute_b32 v236, v244, v82
	ds_bpermute_b32 v237, v244, v83
	s_waitcnt lgkmcnt(0)
	global_store_dwordx4 v[236:237], v[232:235], off offset:2048
	v_pk_fma_f32 v[86:87], v[70:71], v[70:71], v[86:87]
	s_nop 0
	v_pk_mul_f32 v[58:59], v[76:77], v[76:77]
	v_pk_mul_f32 v[60:61], v[80:81], v[80:81]
	v_pk_fma_f32 v[58:59], v[74:75], v[74:75], v[58:59]
	v_pk_fma_f32 v[60:61], v[78:79], v[78:79], v[60:61]
	v_pk_add_f32 v[84:85], v[84:85], v[86:87]
	v_pk_add_f32 v[58:59], v[58:59], v[60:61]
	s_nop 0
	v_pk_add_f32 v[60:61], v[84:85], v[58:59]
	v_cvt_pk_bf16_f32 v58, v74, v75
	v_cvt_pk_bf16_f32 v59, v76, v77
	s_nop 0
	v_add_f32_e32 v70, v60, v61
	ds_swizzle_b32 v71, v70 offset:swizzle(SWAP,16)
	v_cvt_pk_bf16_f32 v60, v78, v79
	v_cvt_pk_bf16_f32 v61, v80, v81
	ds_bpermute_b32 v238, v244, v58
	ds_bpermute_b32 v239, v244, v59
	ds_bpermute_b32 v240, v244, v60
	ds_bpermute_b32 v241, v244, v61
	ds_bpermute_b32 v242, v244, v82
	ds_bpermute_b32 v243, v244, v83
	s_waitcnt lgkmcnt(0)
	global_store_dwordx4 v[242:243], v[238:241], off offset:2112
	s_waitcnt lgkmcnt(0)
	s_nop 0
	v_add_f32_e32 v58, v70, v71
	v_mov_b32_e32 v59, v58
	s_nop 1
	v_permlane32_swap_b32_e32 v58, v59
	s_and_saveexec_b64 s[48:49], s[38:39]
	s_cbranch_execz .LBB0_1345
	v_or_b32_e32 v60, 48, v144
	v_ashrrev_i32_e32 v61, 31, v60
	v_add_f32_e32 v70, v58, v59
	v_lshlrev_b64 v[58:59], 7, v[60:61]
	v_lshl_add_u64 v[58:59], s[8:9], 0, v[58:59]
	v_lshl_add_u64 v[58:59], s[46:47], 2, v[58:59]
	s_lshl_b32 s24, s14, 2
	v_lshl_add_u64 v[58:59], v[58:59], 0, s[24:25]
	global_store_dword v[58:59], v70, off
.LBB0_1345:
	s_or_b64 exec, exec, s[48:49]
	v_pk_mul_f32 v[58:59], v[52:53], v[52:53]
	v_pk_mul_f32 v[60:61], v[64:65], v[64:65]
	v_pk_fma_f32 v[58:59], v[50:51], v[50:51], v[58:59]
	v_pk_fma_f32 v[60:61], v[62:63], v[62:63], v[60:61]
	s_nop 0
	v_pk_add_f32 v[70:71], v[58:59], v[60:61]
	v_cvt_pk_bf16_f32 v58, v50, v51
	v_add_co_u32_e32 v50, vcc, s72, v116
	v_cvt_pk_bf16_f32 v59, v52, v53
	v_cvt_pk_bf16_f32 v60, v62, v63
	v_cvt_pk_bf16_f32 v61, v64, v65
	v_pk_mul_f32 v[52:53], v[56:57], v[56:57]
	s_nop 0
	v_addc_co_u32_e32 v51, vcc, 0, v117, vcc
	ds_bpermute_b32 v232, v244, v58
	ds_bpermute_b32 v233, v244, v59
	ds_bpermute_b32 v234, v244, v60
	ds_bpermute_b32 v235, v244, v61
	ds_bpermute_b32 v236, v244, v50
	ds_bpermute_b32 v237, v244, v51
	s_waitcnt lgkmcnt(0)
	global_store_dwordx4 v[236:237], v[232:235], off
	v_pk_fma_f32 v[52:53], v[54:55], v[54:55], v[52:53]
	s_nop 0
	v_pk_mul_f32 v[58:59], v[68:69], v[68:69]
	s_nop 0
	v_pk_fma_f32 v[58:59], v[66:67], v[66:67], v[58:59]
	s_nop 0
	v_pk_add_f32 v[52:53], v[52:53], v[58:59]
	s_nop 0
	v_pk_add_f32 v[58:59], v[70:71], v[52:53]
	v_cvt_pk_bf16_f32 v52, v54, v55
	v_cvt_pk_bf16_f32 v53, v56, v57
	v_cvt_pk_bf16_f32 v54, v66, v67
	v_cvt_pk_bf16_f32 v55, v68, v69
	ds_bpermute_b32 v238, v244, v52
	ds_bpermute_b32 v239, v244, v53
	ds_bpermute_b32 v240, v244, v54
	ds_bpermute_b32 v241, v244, v55
	ds_bpermute_b32 v242, v244, v50
	ds_bpermute_b32 v243, v244, v51
	s_waitcnt lgkmcnt(0)
	global_store_dwordx4 v[242:243], v[238:241], off offset:64
	v_add_f32_e32 v58, v58, v59
	ds_swizzle_b32 v59, v58 offset:swizzle(SWAP,16)
	s_waitcnt lgkmcnt(0)
	v_add_f32_e32 v52, v58, v59
	v_mov_b32_e32 v53, v52
	s_nop 1
	v_permlane32_swap_b32_e32 v52, v53
	s_and_saveexec_b64 s[48:49], s[38:39]
	s_cbranch_execz .LBB0_1347
	v_ashrrev_i32_e32 v145, 31, v144
	v_add_f32_e32 v54, v52, v53
	v_lshlrev_b64 v[52:53], 7, v[144:145]
	v_lshl_add_u64 v[52:53], s[8:9], 0, v[52:53]
	v_lshl_add_u64 v[52:53], s[46:47], 2, v[52:53]
	s_lshl_b32 s24, s14, 2
	v_lshl_add_u64 v[52:53], v[52:53], 0, s[24:25]
	v_add_co_u32_e32 v52, vcc, 0x4000, v52
	s_nop 1
	v_addc_co_u32_e32 v53, vcc, 0, v53, vcc
	global_store_dword v[52:53], v54, off
.LBB0_1347:
	s_or_b64 exec, exec, s[48:49]
	v_pk_mul_f32 v[52:53], v[36:37], v[36:37]
	v_pk_mul_f32 v[54:55], v[40:41], v[40:41]
	v_pk_fma_f32 v[52:53], v[34:35], v[34:35], v[52:53]
	v_cvt_pk_bf16_f32 v34, v34, v35
	v_cvt_pk_bf16_f32 v35, v36, v37
	v_cvt_pk_bf16_f32 v36, v38, v39
	v_cvt_pk_bf16_f32 v37, v40, v41
	ds_bpermute_b32 v232, v244, v34
	ds_bpermute_b32 v233, v244, v35
	ds_bpermute_b32 v234, v244, v36
	ds_bpermute_b32 v235, v244, v37
	ds_bpermute_b32 v236, v244, v50
	ds_bpermute_b32 v237, v244, v51
	s_waitcnt lgkmcnt(0)
	global_store_dwordx4 v[236:237], v[232:235], off offset:2048
	v_pk_fma_f32 v[54:55], v[38:39], v[38:39], v[54:55]
	s_nop 0
	v_pk_mul_f32 v[34:35], v[44:45], v[44:45]
	v_pk_mul_f32 v[36:37], v[48:49], v[48:49]
	v_pk_fma_f32 v[34:35], v[42:43], v[42:43], v[34:35]
	v_pk_fma_f32 v[36:37], v[46:47], v[46:47], v[36:37]
	v_pk_add_f32 v[52:53], v[52:53], v[54:55]
	v_pk_add_f32 v[34:35], v[34:35], v[36:37]
	s_nop 0
	v_pk_add_f32 v[36:37], v[52:53], v[34:35]
	v_cvt_pk_bf16_f32 v34, v42, v43
	v_cvt_pk_bf16_f32 v35, v44, v45
	s_nop 0
	v_add_f32_e32 v38, v36, v37
	ds_swizzle_b32 v39, v38 offset:swizzle(SWAP,16)
	v_cvt_pk_bf16_f32 v36, v46, v47
	v_cvt_pk_bf16_f32 v37, v48, v49
	ds_bpermute_b32 v238, v244, v34
	ds_bpermute_b32 v239, v244, v35
	ds_bpermute_b32 v240, v244, v36
	ds_bpermute_b32 v241, v244, v37
	ds_bpermute_b32 v242, v244, v50
	ds_bpermute_b32 v243, v244, v51
	s_waitcnt lgkmcnt(0)
	global_store_dwordx4 v[242:243], v[238:241], off offset:2112
	s_waitcnt lgkmcnt(0)
	s_nop 0
	v_add_f32_e32 v34, v38, v39
	v_mov_b32_e32 v35, v34
	s_nop 1
	v_permlane32_swap_b32_e32 v34, v35
	s_and_saveexec_b64 s[48:49], s[38:39]
	s_cbranch_execz .LBB0_1349
	v_ashrrev_i32_e32 v145, 31, v144
	v_add_f32_e32 v36, v34, v35
	v_lshlrev_b64 v[34:35], 7, v[144:145]
	v_lshl_add_u64 v[34:35], s[8:9], 0, v[34:35]
	v_lshl_add_u64 v[34:35], s[46:47], 2, v[34:35]
	s_lshl_b32 s24, s14, 2
	v_lshl_add_u64 v[34:35], v[34:35], 0, s[24:25]
	v_add_co_u32_e32 v34, vcc, 0x4000, v34
	s_nop 1
	v_addc_co_u32_e32 v35, vcc, 0, v35, vcc
	global_store_dword v[34:35], v36, off offset:2048
.LBB0_1349:
	s_or_b64 exec, exec, s[48:49]
	v_pk_mul_f32 v[34:35], v[20:21], v[20:21]
	v_pk_mul_f32 v[36:37], v[28:29], v[28:29]
	v_pk_fma_f32 v[34:35], v[18:19], v[18:19], v[34:35]
	v_pk_fma_f32 v[36:37], v[26:27], v[26:27], v[36:37]
	s_nop 0
	v_pk_add_f32 v[38:39], v[34:35], v[36:37]
	v_cvt_pk_bf16_f32 v35, v20, v21
	v_cvt_pk_bf16_f32 v36, v26, v27
	v_pk_mul_f32 v[20:21], v[24:25], v[24:25]
	v_pk_mul_f32 v[26:27], v[32:33], v[32:33]
	v_pk_fma_f32 v[20:21], v[22:23], v[22:23], v[20:21]
	v_pk_fma_f32 v[26:27], v[30:31], v[30:31], v[26:27]
	v_cvt_pk_bf16_f32 v34, v18, v19
	v_add_co_u32_e32 v18, vcc, s31, v116
	v_pk_add_f32 v[20:21], v[20:21], v[26:27]
	s_nop 0
	v_addc_co_u32_e32 v19, vcc, 0, v117, vcc
	v_pk_add_f32 v[26:27], v[38:39], v[20:21]
	v_cvt_pk_bf16_f32 v20, v22, v23
	v_cvt_pk_bf16_f32 v21, v24, v25
	v_cvt_pk_bf16_f32 v22, v30, v31
	v_cvt_pk_bf16_f32 v23, v32, v33
	ds_bpermute_b32 v232, v244, v20
	ds_bpermute_b32 v233, v244, v21
	ds_bpermute_b32 v234, v244, v22
	ds_bpermute_b32 v235, v244, v23
	ds_bpermute_b32 v236, v244, v18
	ds_bpermute_b32 v237, v244, v19
	s_waitcnt lgkmcnt(0)
	global_store_dwordx4 v[236:237], v[232:235], off offset:64
	v_add_f32_e32 v26, v26, v27
	ds_swizzle_b32 v27, v26 offset:swizzle(SWAP,16)
	v_cvt_pk_bf16_f32 v37, v28, v29
	ds_bpermute_b32 v238, v244, v34
	ds_bpermute_b32 v239, v244, v35
	ds_bpermute_b32 v240, v244, v36
	ds_bpermute_b32 v241, v244, v37
	ds_bpermute_b32 v242, v244, v18
	ds_bpermute_b32 v243, v244, v19
	s_waitcnt lgkmcnt(0)
	global_store_dwordx4 v[242:243], v[238:241], off
	s_waitcnt lgkmcnt(0)
	v_add_f32_e32 v20, v26, v27
	v_mov_b32_e32 v21, v20
	s_nop 1
	v_permlane32_swap_b32_e32 v20, v21
	s_and_saveexec_b64 s[48:49], s[38:39]
	s_cbranch_execz .LBB0_1351
	v_ashrrev_i32_e32 v145, 31, v144
	v_add_f32_e32 v22, v20, v21
	v_lshlrev_b64 v[20:21], 7, v[144:145]
	v_lshl_add_u64 v[20:21], s[8:9], 0, v[20:21]
	v_lshl_add_u64 v[20:21], s[46:47], 2, v[20:21]
	s_lshl_b32 s24, s14, 2
	v_lshl_add_u64 v[20:21], v[20:21], 0, s[24:25]
	v_add_co_u32_e32 v20, vcc, 0x5000, v20
	s_nop 1
	v_addc_co_u32_e32 v21, vcc, 0, v21, vcc
	global_store_dword v[20:21], v22, off
.LBB0_1351:
	s_or_b64 exec, exec, s[48:49]
	v_pk_mul_f32 v[20:21], v[4:5], v[4:5]
	v_pk_mul_f32 v[22:23], v[8:9], v[8:9]
	v_pk_fma_f32 v[20:21], v[2:3], v[2:3], v[20:21]
	v_cvt_pk_bf16_f32 v2, v2, v3
	v_cvt_pk_bf16_f32 v3, v4, v5
	v_cvt_pk_bf16_f32 v4, v6, v7
	v_cvt_pk_bf16_f32 v5, v8, v9
	ds_bpermute_b32 v232, v244, v2
	ds_bpermute_b32 v233, v244, v3
	ds_bpermute_b32 v234, v244, v4
	ds_bpermute_b32 v235, v244, v5
	ds_bpermute_b32 v236, v244, v18
	ds_bpermute_b32 v237, v244, v19
	s_waitcnt lgkmcnt(0)
	global_store_dwordx4 v[236:237], v[232:235], off offset:2048
	v_pk_fma_f32 v[22:23], v[6:7], v[6:7], v[22:23]
	s_nop 0
	v_pk_mul_f32 v[2:3], v[12:13], v[12:13]
	v_pk_mul_f32 v[4:5], v[16:17], v[16:17]
	v_pk_fma_f32 v[2:3], v[10:11], v[10:11], v[2:3]
	v_pk_fma_f32 v[4:5], v[14:15], v[14:15], v[4:5]
	v_pk_add_f32 v[20:21], v[20:21], v[22:23]
	v_pk_add_f32 v[2:3], v[2:3], v[4:5]
	s_nop 0
	v_pk_add_f32 v[4:5], v[20:21], v[2:3]
	v_cvt_pk_bf16_f32 v2, v10, v11
	v_cvt_pk_bf16_f32 v3, v12, v13
	s_nop 0
	v_add_f32_e32 v6, v4, v5
	ds_swizzle_b32 v7, v6 offset:swizzle(SWAP,16)
	v_cvt_pk_bf16_f32 v4, v14, v15
	v_cvt_pk_bf16_f32 v5, v16, v17
	ds_bpermute_b32 v238, v244, v2
	ds_bpermute_b32 v239, v244, v3
	ds_bpermute_b32 v240, v244, v4
	ds_bpermute_b32 v241, v244, v5
	ds_bpermute_b32 v242, v244, v18
	ds_bpermute_b32 v243, v244, v19
	s_waitcnt lgkmcnt(0)
	global_store_dwordx4 v[242:243], v[238:241], off offset:2112
	s_waitcnt lgkmcnt(0)
	s_nop 0
	v_add_f32_e32 v2, v6, v7
	v_mov_b32_e32 v3, v2
	s_nop 1
	v_permlane32_swap_b32_e32 v2, v3
	s_and_saveexec_b64 s[48:49], s[38:39]
	s_cbranch_execz .LBB0_1353
	v_ashrrev_i32_e32 v145, 31, v144
	v_add_f32_e32 v4, v2, v3
	v_lshlrev_b64 v[2:3], 7, v[144:145]
	v_lshl_add_u64 v[2:3], s[8:9], 0, v[2:3]
	v_lshl_add_u64 v[2:3], s[46:47], 2, v[2:3]
	s_lshl_b32 s24, s14, 2
	v_lshl_add_u64 v[2:3], v[2:3], 0, s[24:25]
	v_add_co_u32_e32 v2, vcc, 0x5000, v2
	s_nop 1
	v_addc_co_u32_e32 v3, vcc, 0, v3, vcc
	global_store_dword v[2:3], v4, off offset:2048
